# scan state: packed f32 adds on the MFMA-feeding chain split into scalar adds; GEMM loops: B-fragment LDS reads moved into the empty read slots of phases 4/8; plus static older-half priority
# speedup vs baseline: 1.0180x; 1.0057x over previous
.LBB0_388:
	s_ashr_i32 s25, s24, 31
	v_mov_b64_e32 v[2:3], 0xc60
	s_lshl_b64 s[0:1], s[24:25], 19
	v_cmp_lt_i64_e32 vcc, s[26:27], v[2:3]
	s_add_u32 s26, s12, s0
	s_addc_u32 s27, s13, s1
	s_and_b64 s[0:1], vcc, exec
	s_cselect_b32 s7, s27, s31
	s_cselect_b32 s9, s26, s30
	s_ashr_i32 s23, s22, 31
	s_lshl_b64 s[0:1], s[22:23], 19
	s_add_u32 s28, s16, s0
	s_addc_u32 s29, s17, s1
	s_and_b64 s[0:1], vcc, exec
	s_cselect_b32 s23, s29, s65
	s_cselect_b32 s25, s28, s64
	s_add_u32 s30, s30, 0x40080
	s_addc_u32 s31, s31, 0
	s_add_u32 s77, s64, 0x100
	v_mov_b32_e32 v2, 0
	s_addc_u32 s78, s65, 0
	s_mov_b32 s79, -2
	v_mov_b32_e32 v3, v2
	v_mov_b32_e32 v4, v2
	v_mov_b32_e32 v5, v2
	v_mov_b32_e32 v6, v2
	v_mov_b32_e32 v7, v2
	v_mov_b32_e32 v8, v2
	v_mov_b32_e32 v9, v2
	v_mov_b32_e32 v18, v2
	v_mov_b32_e32 v19, v2
	v_mov_b32_e32 v20, v2
	v_mov_b32_e32 v21, v2
	v_mov_b32_e32 v22, v2
	v_mov_b32_e32 v23, v2
	v_mov_b32_e32 v24, v2
	v_mov_b32_e32 v25, v2
	v_mov_b32_e32 v34, v2
	v_mov_b32_e32 v35, v2
	v_mov_b32_e32 v36, v2
	v_mov_b32_e32 v37, v2
	v_mov_b32_e32 v38, v2
	v_mov_b32_e32 v39, v2
	v_mov_b32_e32 v40, v2
	v_mov_b32_e32 v41, v2
	v_mov_b32_e32 v50, v2
	v_mov_b32_e32 v51, v2
	v_mov_b32_e32 v52, v2
	v_mov_b32_e32 v53, v2
	v_mov_b32_e32 v54, v2
	v_mov_b32_e32 v55, v2
	v_mov_b32_e32 v56, v2
	v_mov_b32_e32 v57, v2
	v_mov_b32_e32 v10, v2
	v_mov_b32_e32 v11, v2
	v_mov_b32_e32 v12, v2
	v_mov_b32_e32 v13, v2
	v_mov_b32_e32 v14, v2
	v_mov_b32_e32 v15, v2
	v_mov_b32_e32 v16, v2
	v_mov_b32_e32 v17, v2
	v_mov_b32_e32 v26, v2
	v_mov_b32_e32 v27, v2
	v_mov_b32_e32 v28, v2
	v_mov_b32_e32 v29, v2
	v_mov_b32_e32 v30, v2
	v_mov_b32_e32 v31, v2
	v_mov_b32_e32 v32, v2
	v_mov_b32_e32 v33, v2
	v_mov_b32_e32 v42, v2
	v_mov_b32_e32 v43, v2
	v_mov_b32_e32 v44, v2
	v_mov_b32_e32 v45, v2
	v_mov_b32_e32 v46, v2
	v_mov_b32_e32 v47, v2
	v_mov_b32_e32 v48, v2
	v_mov_b32_e32 v49, v2
	v_mov_b32_e32 v58, v2
	v_mov_b32_e32 v59, v2
	v_mov_b32_e32 v60, v2
	v_mov_b32_e32 v61, v2
	v_mov_b32_e32 v62, v2
	v_mov_b32_e32 v63, v2
	v_mov_b32_e32 v64, v2
	v_mov_b32_e32 v65, v2
	v_mov_b32_e32 v66, v2
	v_mov_b32_e32 v67, v2
	v_mov_b32_e32 v68, v2
	v_mov_b32_e32 v69, v2
	v_mov_b32_e32 v70, v2
	v_mov_b32_e32 v71, v2
	v_mov_b32_e32 v72, v2
	v_mov_b32_e32 v73, v2
	v_mov_b32_e32 v82, v2
	v_mov_b32_e32 v83, v2
	v_mov_b32_e32 v84, v2
	v_mov_b32_e32 v85, v2
	v_mov_b32_e32 v86, v2
	v_mov_b32_e32 v87, v2
	v_mov_b32_e32 v88, v2
	v_mov_b32_e32 v89, v2
	v_mov_b32_e32 v98, v2
	v_mov_b32_e32 v99, v2
	v_mov_b32_e32 v100, v2
	v_mov_b32_e32 v101, v2
	v_mov_b32_e32 v102, v2
	v_mov_b32_e32 v103, v2
	v_mov_b32_e32 v104, v2
	v_mov_b32_e32 v105, v2
	v_mov_b32_e32 v114, v2
	v_mov_b32_e32 v115, v2
	v_mov_b32_e32 v116, v2
	v_mov_b32_e32 v117, v2
	v_mov_b32_e32 v118, v2
	v_mov_b32_e32 v119, v2
	v_mov_b32_e32 v120, v2
	v_mov_b32_e32 v121, v2
	v_mov_b32_e32 v74, v2
	v_mov_b32_e32 v75, v2
	v_mov_b32_e32 v76, v2
	v_mov_b32_e32 v77, v2
	v_mov_b32_e32 v78, v2
	v_mov_b32_e32 v79, v2
	v_mov_b32_e32 v80, v2
	v_mov_b32_e32 v81, v2
	v_mov_b32_e32 v90, v2
	v_mov_b32_e32 v91, v2
	v_mov_b32_e32 v92, v2
	v_mov_b32_e32 v93, v2
	v_mov_b32_e32 v94, v2
	v_mov_b32_e32 v95, v2
	v_mov_b32_e32 v96, v2
	v_mov_b32_e32 v97, v2
	v_mov_b32_e32 v106, v2
	v_mov_b32_e32 v107, v2
	v_mov_b32_e32 v108, v2
	v_mov_b32_e32 v109, v2
	v_mov_b32_e32 v110, v2
	v_mov_b32_e32 v111, v2
	v_mov_b32_e32 v112, v2
	v_mov_b32_e32 v113, v2
	v_mov_b32_e32 v122, v2
	v_mov_b32_e32 v123, v2
	v_mov_b32_e32 v124, v2
	v_mov_b32_e32 v125, v2
	v_mov_b32_e32 v126, v2
	v_mov_b32_e32 v127, v2
	v_mov_b32_e32 v128, v2
	v_mov_b32_e32 v129, v2
	v_add_u32_e32 v170, 0x10000, v158
	ds_read_b128 v[152:155], v170
	ds_read_b128 v[162:165], v170 offset:1024
	ds_read_b128 v[166:169], v170 offset:2048
	ds_read_b128 v[170:173], v170 offset:3072
.LBB0_389:
	s_add_u32 s0, s30, 0xfffc0080
	s_addc_u32 s1, s31, -1
	s_add_i32 s33, 0, 0x10000
	s_cmp_eq_u32 s79, 12
	s_cselect_b32 s67, s7, s1
	s_cselect_b32 s66, s9, s0
	s_cselect_b32 s65, s23, s78
	s_cselect_b32 s64, s25, s77
	v_lshl_add_u64 v[156:157], s[30:31], 0, v[148:149]
	s_add_i32 m0, s40, 0xc000
	ds_read_b128 v[174:177], v161
	ds_read_b128 v[178:181], v161 offset:1024
	ds_read_b128 v[182:185], v161 offset:2048
	ds_read_b128 v[186:189], v161 offset:3072
	ds_read_b128 v[190:193], v161 offset:4096
	ds_read_b128 v[198:201], v161 offset:5120
	ds_read_b128 v[202:205], v161 offset:6144
	ds_read_b128 v[206:209], v161 offset:7168
	global_load_lds_dwordx4 v[156:157], off
	v_lshl_add_u64 v[156:157], s[30:31], 0, v[150:151]
	s_add_i32 m0, s40, 0xe000
	s_nop 0
	global_load_lds_dwordx4 v[156:157], off
	s_waitcnt lgkmcnt(8)
	s_barrier
	s_waitcnt lgkmcnt(0)
	s_waitcnt lgkmcnt(0)
	v_mfma_f32_16x16x32_bf16 v[126:129], v[152:155], v[174:177], v[126:129]
	v_mfma_f32_16x16x32_bf16 v[122:125], v[166:169], v[174:177], v[122:125]
	v_mfma_f32_16x16x32_bf16 v[110:113], v[152:155], v[182:185], v[110:113]
	v_mfma_f32_16x16x32_bf16 v[106:109], v[166:169], v[182:185], v[106:109]
	v_mfma_f32_16x16x32_bf16 v[94:97], v[152:155], v[190:193], v[94:97]
	v_mfma_f32_16x16x32_bf16 v[90:93], v[166:169], v[190:193], v[90:93]
	v_mfma_f32_16x16x32_bf16 v[78:81], v[152:155], v[202:205], v[78:81]
	v_mfma_f32_16x16x32_bf16 v[74:77], v[166:169], v[202:205], v[74:77]
	v_mfma_f32_16x16x32_bf16 v[126:129], v[162:165], v[178:181], v[126:129]
	v_mfma_f32_16x16x32_bf16 v[122:125], v[170:173], v[178:181], v[122:125]
	v_mfma_f32_16x16x32_bf16 v[110:113], v[162:165], v[186:189], v[110:113]
	v_mfma_f32_16x16x32_bf16 v[106:109], v[170:173], v[186:189], v[106:109]
	v_mfma_f32_16x16x32_bf16 v[94:97], v[162:165], v[198:201], v[94:97]
	v_mfma_f32_16x16x32_bf16 v[90:93], v[170:173], v[198:201], v[90:93]
	v_mfma_f32_16x16x32_bf16 v[78:81], v[162:165], v[206:209], v[78:81]
	v_mfma_f32_16x16x32_bf16 v[74:77], v[170:173], v[206:209], v[74:77]
	s_barrier
	s_add_i32 s36, 0, 0x14000
	v_add_u32_e32 v156, s36, v158
	s_add_i32 s0, s33, s38
	ds_read_b128 v[210:213], v156
	ds_read_b128 v[214:217], v156 offset:1024
	ds_read_b128 v[218:221], v156 offset:2048
	ds_read_b128 v[238:241], v156 offset:3072
	v_lshl_add_u64 v[156:157], s[64:65], 0, v[132:133]
	s_mov_b32 m0, s0
	v_lshl_add_u64 v[242:243], s[64:65], 0, v[136:137]
	global_load_lds_dwordx4 v[156:157], off
	s_add_i32 m0, s0, 0x2000
	s_nop 0
	global_load_lds_dwordx4 v[242:243], off
	s_barrier
	s_waitcnt lgkmcnt(0)
	s_waitcnt lgkmcnt(0)
	v_mfma_f32_16x16x32_bf16 v[118:121], v[210:213], v[174:177], v[118:121]
	v_mfma_f32_16x16x32_bf16 v[114:117], v[218:221], v[174:177], v[114:117]
	v_mfma_f32_16x16x32_bf16 v[102:105], v[210:213], v[182:185], v[102:105]
	v_mfma_f32_16x16x32_bf16 v[98:101], v[218:221], v[182:185], v[98:101]
	v_mfma_f32_16x16x32_bf16 v[86:89], v[210:213], v[190:193], v[86:89]
	v_mfma_f32_16x16x32_bf16 v[82:85], v[218:221], v[190:193], v[82:85]
	v_mfma_f32_16x16x32_bf16 v[70:73], v[210:213], v[202:205], v[70:73]
	v_mfma_f32_16x16x32_bf16 v[66:69], v[218:221], v[202:205], v[66:69]
	v_mfma_f32_16x16x32_bf16 v[118:121], v[214:217], v[178:181], v[118:121]
	v_mfma_f32_16x16x32_bf16 v[114:117], v[238:241], v[178:181], v[114:117]
	v_mfma_f32_16x16x32_bf16 v[102:105], v[214:217], v[186:189], v[102:105]
	v_mfma_f32_16x16x32_bf16 v[98:101], v[238:241], v[186:189], v[98:101]
	v_mfma_f32_16x16x32_bf16 v[86:89], v[214:217], v[198:201], v[86:89]
	v_mfma_f32_16x16x32_bf16 v[82:85], v[238:241], v[198:201], v[82:85]
	v_mfma_f32_16x16x32_bf16 v[70:73], v[214:217], v[206:209], v[70:73]
	v_mfma_f32_16x16x32_bf16 v[66:69], v[238:241], v[206:209], v[66:69]
	s_mov_b32 m0, s40
	v_lshl_add_u64 v[244:245], s[66:67], 0, v[130:131]
	s_barrier
	ds_read_b128 v[174:177], v161 offset:16384
	ds_read_b128 v[178:181], v161 offset:17408
	ds_read_b128 v[182:185], v161 offset:18432
	ds_read_b128 v[186:189], v161 offset:19456
	ds_read_b128 v[190:193], v161 offset:20480
	ds_read_b128 v[198:201], v161 offset:21504
	ds_read_b128 v[202:205], v161 offset:22528
	ds_read_b128 v[206:209], v161 offset:23552
	global_load_lds_dwordx4 v[244:245], off
	v_lshl_add_u64 v[246:247], s[66:67], 0, v[134:135]
	s_mov_b32 m0, s43
	s_nop 0
	global_load_lds_dwordx4 v[246:247], off
	s_waitcnt vmcnt(10)
	s_barrier
	s_waitcnt lgkmcnt(0)
	s_waitcnt lgkmcnt(0)
	v_mfma_f32_16x16x32_bf16 v[62:65], v[152:155], v[174:177], v[62:65]
	v_mfma_f32_16x16x32_bf16 v[58:61], v[166:169], v[174:177], v[58:61]
	v_mfma_f32_16x16x32_bf16 v[46:49], v[152:155], v[182:185], v[46:49]
	v_mfma_f32_16x16x32_bf16 v[42:45], v[166:169], v[182:185], v[42:45]
	v_mfma_f32_16x16x32_bf16 v[30:33], v[152:155], v[190:193], v[30:33]
	v_mfma_f32_16x16x32_bf16 v[26:29], v[166:169], v[190:193], v[26:29]
	v_mfma_f32_16x16x32_bf16 v[14:17], v[152:155], v[202:205], v[14:17]
	v_mfma_f32_16x16x32_bf16 v[10:13], v[166:169], v[202:205], v[10:13]
	v_mfma_f32_16x16x32_bf16 v[62:65], v[162:165], v[178:181], v[62:65]
	v_mfma_f32_16x16x32_bf16 v[58:61], v[170:173], v[178:181], v[58:61]
	v_mfma_f32_16x16x32_bf16 v[46:49], v[162:165], v[186:189], v[46:49]
	v_mfma_f32_16x16x32_bf16 v[42:45], v[170:173], v[186:189], v[42:45]
	v_mfma_f32_16x16x32_bf16 v[30:33], v[162:165], v[198:201], v[30:33]
	v_mfma_f32_16x16x32_bf16 v[26:29], v[170:173], v[198:201], v[26:29]
	v_mfma_f32_16x16x32_bf16 v[14:17], v[162:165], v[206:209], v[14:17]
	v_mfma_f32_16x16x32_bf16 v[10:13], v[170:173], v[206:209], v[10:13]
	s_barrier
	s_add_u32 s0, s64, 0x40000
	s_addc_u32 s1, s65, 0
	s_add_i32 s33, s36, s38
	v_lshl_add_u64 v[152:153], s[0:1], 0, v[132:133]
	s_mov_b32 m0, s33
	s_nop 0
	global_load_lds_dwordx4 v[152:153], off
	v_lshl_add_u64 v[152:153], s[0:1], 0, v[136:137]
	s_add_i32 m0, s33, 0x2000
	s_nop 0
	global_load_lds_dwordx4 v[152:153], off
	v_add_u32_e32 v170, 0x18000, v158
	ds_read_b128 v[152:155], v170
	ds_read_b128 v[162:165], v170 offset:1024
	ds_read_b128 v[166:169], v170 offset:2048
	ds_read_b128 v[170:173], v170 offset:3072
	s_waitcnt vmcnt(6)
	s_barrier
	v_mfma_f32_16x16x32_bf16 v[54:57], v[210:213], v[174:177], v[54:57]
	v_mfma_f32_16x16x32_bf16 v[50:53], v[218:221], v[174:177], v[50:53]
	v_mfma_f32_16x16x32_bf16 v[38:41], v[210:213], v[182:185], v[38:41]
	v_mfma_f32_16x16x32_bf16 v[34:37], v[218:221], v[182:185], v[34:37]
	v_mfma_f32_16x16x32_bf16 v[22:25], v[210:213], v[190:193], v[22:25]
	v_mfma_f32_16x16x32_bf16 v[18:21], v[218:221], v[190:193], v[18:21]
	v_mfma_f32_16x16x32_bf16 v[6:9], v[210:213], v[202:205], v[6:9]
	v_mfma_f32_16x16x32_bf16 v[2:5], v[218:221], v[202:205], v[2:5]
	v_mfma_f32_16x16x32_bf16 v[54:57], v[214:217], v[178:181], v[54:57]
	v_mfma_f32_16x16x32_bf16 v[50:53], v[238:241], v[178:181], v[50:53]
	v_mfma_f32_16x16x32_bf16 v[38:41], v[214:217], v[186:189], v[38:41]
	v_mfma_f32_16x16x32_bf16 v[34:37], v[238:241], v[186:189], v[34:37]
	v_mfma_f32_16x16x32_bf16 v[22:25], v[214:217], v[198:201], v[22:25]
	v_mfma_f32_16x16x32_bf16 v[18:21], v[238:241], v[198:201], v[18:21]
	v_mfma_f32_16x16x32_bf16 v[6:9], v[214:217], v[206:209], v[6:9]
	v_mfma_f32_16x16x32_bf16 v[2:5], v[238:241], v[206:209], v[2:5]
	s_add_i32 s33, 0, 0x18000
	s_barrier
	s_add_u32 s0, s66, 0x40000
	s_addc_u32 s1, s67, 0
	s_mov_b32 m0, s69
	v_lshl_add_u64 v[210:211], s[0:1], 0, v[130:131]
	ds_read_b128 v[174:177], v161 offset:32768
	ds_read_b128 v[178:181], v161 offset:33792
	ds_read_b128 v[182:185], v161 offset:34816
	ds_read_b128 v[186:189], v161 offset:35840
	ds_read_b128 v[190:193], v161 offset:36864
	ds_read_b128 v[198:201], v161 offset:37888
	ds_read_b128 v[202:205], v161 offset:38912
	ds_read_b128 v[206:209], v161 offset:39936
	global_load_lds_dwordx4 v[210:211], off
	v_lshl_add_u64 v[210:211], s[0:1], 0, v[134:135]
	s_mov_b32 m0, s70
	s_nop 0
	global_load_lds_dwordx4 v[210:211], off
	s_waitcnt lgkmcnt(8)
	s_barrier
	s_waitcnt lgkmcnt(0)
	s_waitcnt lgkmcnt(0)
	v_mfma_f32_16x16x32_bf16 v[126:129], v[152:155], v[174:177], v[126:129]
	v_mfma_f32_16x16x32_bf16 v[122:125], v[166:169], v[174:177], v[122:125]
	v_mfma_f32_16x16x32_bf16 v[110:113], v[152:155], v[182:185], v[110:113]
	v_mfma_f32_16x16x32_bf16 v[106:109], v[166:169], v[182:185], v[106:109]
	v_mfma_f32_16x16x32_bf16 v[94:97], v[152:155], v[190:193], v[94:97]
	v_mfma_f32_16x16x32_bf16 v[90:93], v[166:169], v[190:193], v[90:93]
	v_mfma_f32_16x16x32_bf16 v[78:81], v[152:155], v[202:205], v[78:81]
	v_mfma_f32_16x16x32_bf16 v[74:77], v[166:169], v[202:205], v[74:77]
	v_mfma_f32_16x16x32_bf16 v[126:129], v[162:165], v[178:181], v[126:129]
	v_mfma_f32_16x16x32_bf16 v[122:125], v[170:173], v[178:181], v[122:125]
	v_mfma_f32_16x16x32_bf16 v[110:113], v[162:165], v[186:189], v[110:113]
	v_mfma_f32_16x16x32_bf16 v[106:109], v[170:173], v[186:189], v[106:109]
	v_mfma_f32_16x16x32_bf16 v[94:97], v[162:165], v[198:201], v[94:97]
	v_mfma_f32_16x16x32_bf16 v[90:93], v[170:173], v[198:201], v[90:93]
	v_mfma_f32_16x16x32_bf16 v[78:81], v[162:165], v[206:209], v[78:81]
	v_mfma_f32_16x16x32_bf16 v[74:77], v[170:173], v[206:209], v[74:77]
	s_barrier
	s_add_i32 s36, 0, 0x1c000
	s_add_i32 s0, s33, s38
	v_add_u32_e32 v194, s36, v158
	v_lshl_add_u64 v[156:157], v[156:157], 0, s[54:55]
	s_mov_b32 m0, s0
	ds_read_b128 v[210:213], v194
	ds_read_b128 v[214:217], v194 offset:1024
	ds_read_b128 v[218:221], v194 offset:2048
	ds_read_b128 v[238:241], v194 offset:3072
	global_load_lds_dwordx4 v[156:157], off
	v_lshl_add_u64 v[156:157], v[242:243], 0, s[54:55]
	s_add_i32 m0, s0, 0x2000
	s_nop 0
	global_load_lds_dwordx4 v[156:157], off
	s_barrier
	s_waitcnt lgkmcnt(0)
	s_waitcnt lgkmcnt(0)
	v_mfma_f32_16x16x32_bf16 v[118:121], v[210:213], v[174:177], v[118:121]
	v_mfma_f32_16x16x32_bf16 v[114:117], v[218:221], v[174:177], v[114:117]
	v_mfma_f32_16x16x32_bf16 v[102:105], v[210:213], v[182:185], v[102:105]
	v_mfma_f32_16x16x32_bf16 v[98:101], v[218:221], v[182:185], v[98:101]
	v_mfma_f32_16x16x32_bf16 v[86:89], v[210:213], v[190:193], v[86:89]
	v_mfma_f32_16x16x32_bf16 v[82:85], v[218:221], v[190:193], v[82:85]
	v_mfma_f32_16x16x32_bf16 v[70:73], v[210:213], v[202:205], v[70:73]
	v_mfma_f32_16x16x32_bf16 v[66:69], v[218:221], v[202:205], v[66:69]
	v_mfma_f32_16x16x32_bf16 v[118:121], v[214:217], v[178:181], v[118:121]
	v_mfma_f32_16x16x32_bf16 v[114:117], v[238:241], v[178:181], v[114:117]
	v_mfma_f32_16x16x32_bf16 v[102:105], v[214:217], v[186:189], v[102:105]
	v_mfma_f32_16x16x32_bf16 v[98:101], v[238:241], v[186:189], v[98:101]
	v_mfma_f32_16x16x32_bf16 v[86:89], v[214:217], v[198:201], v[86:89]
	v_mfma_f32_16x16x32_bf16 v[82:85], v[238:241], v[198:201], v[82:85]
	v_mfma_f32_16x16x32_bf16 v[70:73], v[214:217], v[206:209], v[70:73]
	v_mfma_f32_16x16x32_bf16 v[66:69], v[238:241], v[206:209], v[66:69]
	s_mov_b32 m0, s71
	v_lshl_add_u64 v[156:157], v[244:245], 0, s[54:55]
	s_barrier
	ds_read_b128 v[174:177], v161 offset:49152
	ds_read_b128 v[178:181], v161 offset:50176
	ds_read_b128 v[182:185], v161 offset:51200
	ds_read_b128 v[186:189], v161 offset:52224
	ds_read_b128 v[190:193], v161 offset:53248
	ds_read_b128 v[198:201], v161 offset:54272
	ds_read_b128 v[202:205], v161 offset:55296
	ds_read_b128 v[206:209], v161 offset:56320
	global_load_lds_dwordx4 v[156:157], off
	v_lshl_add_u64 v[156:157], v[246:247], 0, s[54:55]
	s_mov_b32 m0, s72
	s_nop 0
	global_load_lds_dwordx4 v[156:157], off
	s_waitcnt vmcnt(10)
	s_barrier
	s_waitcnt lgkmcnt(0)
	s_waitcnt lgkmcnt(0)
	v_mfma_f32_16x16x32_bf16 v[62:65], v[152:155], v[174:177], v[62:65]
	v_mfma_f32_16x16x32_bf16 v[58:61], v[166:169], v[174:177], v[58:61]
	v_mfma_f32_16x16x32_bf16 v[46:49], v[152:155], v[182:185], v[46:49]
	v_mfma_f32_16x16x32_bf16 v[42:45], v[166:169], v[182:185], v[42:45]
	v_mfma_f32_16x16x32_bf16 v[30:33], v[152:155], v[190:193], v[30:33]
	v_mfma_f32_16x16x32_bf16 v[26:29], v[166:169], v[190:193], v[26:29]
	v_mfma_f32_16x16x32_bf16 v[14:17], v[152:155], v[202:205], v[14:17]
	v_mfma_f32_16x16x32_bf16 v[10:13], v[166:169], v[202:205], v[10:13]
	v_mfma_f32_16x16x32_bf16 v[62:65], v[162:165], v[178:181], v[62:65]
	v_mfma_f32_16x16x32_bf16 v[58:61], v[170:173], v[178:181], v[58:61]
	v_mfma_f32_16x16x32_bf16 v[46:49], v[162:165], v[186:189], v[46:49]
	v_mfma_f32_16x16x32_bf16 v[42:45], v[170:173], v[186:189], v[42:45]
	v_mfma_f32_16x16x32_bf16 v[30:33], v[162:165], v[198:201], v[30:33]
	v_mfma_f32_16x16x32_bf16 v[26:29], v[170:173], v[198:201], v[26:29]
	v_mfma_f32_16x16x32_bf16 v[14:17], v[162:165], v[206:209], v[14:17]
	v_mfma_f32_16x16x32_bf16 v[10:13], v[170:173], v[206:209], v[10:13]
	s_barrier
	s_add_u32 s0, s64, 0x40080
	s_addc_u32 s1, s65, 0
	s_add_i32 s33, s36, s38
	v_lshl_add_u64 v[152:153], s[0:1], 0, v[132:133]
	s_mov_b32 m0, s33
	s_nop 0
	global_load_lds_dwordx4 v[152:153], off
	v_lshl_add_u64 v[152:153], s[0:1], 0, v[136:137]
	s_add_i32 m0, s33, 0x2000
	s_nop 0
	global_load_lds_dwordx4 v[152:153], off
	v_add_u32_e32 v170, 0x10000, v158
	ds_read_b128 v[152:155], v170
	ds_read_b128 v[162:165], v170 offset:1024
	ds_read_b128 v[166:169], v170 offset:2048
	ds_read_b128 v[170:173], v170 offset:3072
	s_waitcnt vmcnt(6)
	s_barrier
	v_mfma_f32_16x16x32_bf16 v[54:57], v[210:213], v[174:177], v[54:57]
	v_mfma_f32_16x16x32_bf16 v[50:53], v[218:221], v[174:177], v[50:53]
	v_mfma_f32_16x16x32_bf16 v[38:41], v[210:213], v[182:185], v[38:41]
	v_mfma_f32_16x16x32_bf16 v[34:37], v[218:221], v[182:185], v[34:37]
	v_mfma_f32_16x16x32_bf16 v[22:25], v[210:213], v[190:193], v[22:25]
	v_mfma_f32_16x16x32_bf16 v[18:21], v[218:221], v[190:193], v[18:21]
	v_mfma_f32_16x16x32_bf16 v[6:9], v[210:213], v[202:205], v[6:9]
	v_mfma_f32_16x16x32_bf16 v[2:5], v[218:221], v[202:205], v[2:5]
	v_mfma_f32_16x16x32_bf16 v[54:57], v[214:217], v[178:181], v[54:57]
	v_mfma_f32_16x16x32_bf16 v[50:53], v[238:241], v[178:181], v[50:53]
	v_mfma_f32_16x16x32_bf16 v[38:41], v[214:217], v[186:189], v[38:41]
	v_mfma_f32_16x16x32_bf16 v[34:37], v[238:241], v[186:189], v[34:37]
	v_mfma_f32_16x16x32_bf16 v[22:25], v[214:217], v[198:201], v[22:25]
	v_mfma_f32_16x16x32_bf16 v[18:21], v[238:241], v[198:201], v[18:21]
	v_mfma_f32_16x16x32_bf16 v[6:9], v[214:217], v[206:209], v[6:9]
	v_mfma_f32_16x16x32_bf16 v[2:5], v[238:241], v[206:209], v[2:5]
	s_add_i32 s79, s79, 2
	s_add_u32 s30, s30, 0x100
	s_addc_u32 s31, s31, 0
	s_add_u32 s77, s77, 0x100
	s_addc_u32 s78, s78, 0
	s_cmp_gt_u32 s79, 13
	s_barrier
	s_cbranch_scc0 .LBB0_389
	s_waitcnt lgkmcnt(0)
	s_lshl_b32 s0, s8, 8
	v_lshl_add_u32 v162, s6, 8, v139
	v_or_b32_e32 v152, s0, v138
	s_addk_i32 s0, 0xf200
	v_ashrrev_i32_e32 v155, 5, v162
	s_lshr_b32 s23, s0, 8
	v_and_b32_e32 v155, -8, v155
	v_add_u32_e32 v156, s23, v155
	v_add_u32_e32 v154, 0xfffffe00, v152
	s_movk_i32 s1, 0x3ff
	v_ashrrev_i32_e32 v157, 31, v156
	v_cmp_lt_u32_e64 s[8:9], s1, v154
	s_movk_i32 s1, 0xdff
	v_ashrrev_i32_e32 v153, 31, v152
	v_lshlrev_b64 v[156:157], 17, v[156:157]
	v_cmp_lt_i32_e64 s[6:7], s1, v152
	v_lshl_add_u64 v[152:153], v[152:153], 1, s[18:19]
	v_lshl_add_u64 v[156:157], s[20:21], 0, v[156:157]
	s_and_saveexec_b64 s[0:1], s[8:9]
	s_xor_b64 s[30:31], exec, s[0:1]
	s_cbranch_execz .LBB0_396
	s_and_saveexec_b64 s[0:1], s[6:7]
	s_xor_b64 s[64:65], exec, s[0:1]
	s_cbranch_execz .LBB0_393
	v_mul_f32_e32 v155, 0xbfb8aa3b, v126
	v_exp_f32_e32 v155, v155
	v_mul_f32_e32 v163, 0xbfb8aa3b, v122
	v_exp_f32_e32 v163, v163
	v_mul_f32_e32 v165, 0xbfb8aa3b, v114
	v_add_f32_e32 v155, 1.0, v155
	v_rcp_f32_e32 v168, v155
	v_add_f32_e32 v155, 1.0, v163
	v_rcp_f32_e32 v170, v155
	v_mul_f32_e32 v155, 0xbfb8aa3b, v127
	v_exp_f32_e32 v155, v155
	v_mul_f32_e32 v163, 0xbfb8aa3b, v123
	v_exp_f32_e32 v163, v163
	v_mul_f32_e32 v164, 0xbfb8aa3b, v118
	v_exp_f32_e32 v166, v165
	v_mul_f32_e32 v165, 0xbfb8aa3b, v119
	v_exp_f32_e32 v164, v164
	v_exp_f32_e32 v165, v165
	v_mul_f32_e32 v167, 0xbfb8aa3b, v115
	v_add_f32_e32 v155, 1.0, v155
	v_rcp_f32_e32 v169, v155
	v_exp_f32_e32 v167, v167
	v_add_f32_e32 v163, 1.0, v163
	v_rcp_f32_e32 v171, v163
	v_pk_add_f32 v[164:165], v[164:165], 1.0 op_sel_hi:[1,0]
	v_mul_f32_e32 v178, 0xbfb8aa3b, v117
	v_rcp_f32_e32 v155, v164
	v_pk_mul_f32 v[168:169], v[168:169], v[164:165]
	v_rcp_f32_e32 v163, v165
	v_pk_add_f32 v[164:165], v[166:167], 1.0 op_sel_hi:[1,0]
	s_nop 0
	v_rcp_f32_e32 v176, v164
	v_pk_mul_f32 v[166:167], v[170:171], v[164:165]
	v_mul_f32_e32 v164, 0xbfb8aa3b, v128
	v_rcp_f32_e32 v177, v165
	v_exp_f32_e32 v165, v164
	v_mul_f32_e32 v164, 0xbfb8aa3b, v124
	v_exp_f32_e32 v171, v164
	v_mul_f32_e32 v164, 0xbfb8aa3b, v120
	v_add_f32_e32 v165, 1.0, v165
	v_rcp_f32_e32 v172, v165
	v_add_f32_e32 v165, 1.0, v171
	v_rcp_f32_e32 v174, v165
	v_mul_f32_e32 v165, 0xbfb8aa3b, v129
	v_exp_f32_e32 v171, v165
	v_mul_f32_e32 v165, 0xbfb8aa3b, v125
	v_exp_f32_e32 v175, v165
	v_mul_f32_e32 v165, 0xbfb8aa3b, v121
	v_exp_f32_e32 v164, v164
	v_exp_f32_e32 v165, v165
	v_add_f32_e32 v171, 1.0, v171
	v_rcp_f32_e32 v173, v171
	v_mul_f32_e32 v170, 0xbfb8aa3b, v116
	v_exp_f32_e32 v170, v170
	v_exp_f32_e32 v171, v178
	v_pk_add_f32 v[164:165], v[164:165], 1.0 op_sel_hi:[1,0]
	v_cvt_pk_bf16_f32 v166, v166, v167
	v_rcp_f32_e32 v178, v164
	v_pk_mul_f32 v[172:173], v[172:173], v[164:165]
	v_add_f32_e32 v164, 1.0, v175
	v_rcp_f32_e32 v175, v164
	v_rcp_f32_e32 v179, v165
	v_pk_add_f32 v[164:165], v[170:171], 1.0 op_sel_hi:[1,0]
	s_nop 0
	v_rcp_f32_e32 v180, v164
	v_rcp_f32_e32 v181, v165
	v_pk_mul_f32 v[170:171], v[174:175], v[164:165]
	v_lshl_add_u64 v[174:175], v[140:141], 1, v[156:157]
	v_cvt_pk_bf16_f32 v164, v168, v169
	v_cvt_pk_bf16_f32 v165, v172, v173
	v_cvt_pk_bf16_f32 v167, v170, v171
	v_add_co_u32_e32 v168, vcc, 0x10000, v174
	global_store_dwordx4 v[174:175], v[164:167], off
	s_nop 0
	v_addc_co_u32_e32 v169, vcc, 0, v175, vcc
	v_cvt_pk_bf16_f32 v164, v155, v163
	v_cvt_pk_bf16_f32 v165, v178, v179
	v_cvt_pk_bf16_f32 v166, v176, v177
	v_cvt_pk_bf16_f32 v167, v180, v181
	global_store_dwordx4 v[168:169], v[164:167], off

.LBB0_474:
	s_ashr_i32 s23, s22, 31
	s_xor_b64 s[26:27], s[66:67], -1
	s_lshl_b64 s[0:1], s[22:23], 19
	s_add_u32 s24, s12, s0
	s_addc_u32 s25, s13, s1
	s_and_b64 s[0:1], s[66:67], exec
	s_cselect_b32 s5, s25, s31
	s_cselect_b32 s7, s24, s30
	s_ashr_i32 s9, s8, 31
	s_lshl_b64 s[0:1], s[8:9], 19
	s_add_u32 s28, s16, s0
	s_addc_u32 s29, s17, s1
	s_and_b64 s[0:1], s[66:67], exec
	s_cselect_b32 s9, s29, s65
	s_cselect_b32 s23, s28, s64
	s_add_u32 s30, s30, 0x40080
	s_addc_u32 s31, s31, 0
	s_add_u32 s77, s64, 0x100
	v_mov_b32_e32 v2, 0
	s_addc_u32 s78, s65, 0
	s_mov_b32 s79, -2
	v_mov_b32_e32 v3, v2
	v_mov_b32_e32 v4, v2
	v_mov_b32_e32 v5, v2
	v_mov_b32_e32 v6, v2
	v_mov_b32_e32 v7, v2
	v_mov_b32_e32 v8, v2
	v_mov_b32_e32 v9, v2
	v_mov_b32_e32 v18, v2
	v_mov_b32_e32 v19, v2
	v_mov_b32_e32 v20, v2
	v_mov_b32_e32 v21, v2
	v_mov_b32_e32 v22, v2
	v_mov_b32_e32 v23, v2
	v_mov_b32_e32 v24, v2
	v_mov_b32_e32 v25, v2
	v_mov_b32_e32 v34, v2
	v_mov_b32_e32 v35, v2
	v_mov_b32_e32 v36, v2
	v_mov_b32_e32 v37, v2
	v_mov_b32_e32 v38, v2
	v_mov_b32_e32 v39, v2
	v_mov_b32_e32 v40, v2
	v_mov_b32_e32 v41, v2
	v_mov_b32_e32 v50, v2
	v_mov_b32_e32 v51, v2
	v_mov_b32_e32 v52, v2
	v_mov_b32_e32 v53, v2
	v_mov_b32_e32 v54, v2
	v_mov_b32_e32 v55, v2
	v_mov_b32_e32 v56, v2
	v_mov_b32_e32 v57, v2
	v_mov_b32_e32 v10, v2
	v_mov_b32_e32 v11, v2
	v_mov_b32_e32 v12, v2
	v_mov_b32_e32 v13, v2
	v_mov_b32_e32 v14, v2
	v_mov_b32_e32 v15, v2
	v_mov_b32_e32 v16, v2
	v_mov_b32_e32 v17, v2
	v_mov_b32_e32 v26, v2
	v_mov_b32_e32 v27, v2
	v_mov_b32_e32 v28, v2
	v_mov_b32_e32 v29, v2
	v_mov_b32_e32 v30, v2
	v_mov_b32_e32 v31, v2
	v_mov_b32_e32 v32, v2
	v_mov_b32_e32 v33, v2
	v_mov_b32_e32 v42, v2
	v_mov_b32_e32 v43, v2
	v_mov_b32_e32 v44, v2
	v_mov_b32_e32 v45, v2
	v_mov_b32_e32 v46, v2
	v_mov_b32_e32 v47, v2
	v_mov_b32_e32 v48, v2
	v_mov_b32_e32 v49, v2
	v_mov_b32_e32 v58, v2
	v_mov_b32_e32 v59, v2
	v_mov_b32_e32 v60, v2
	v_mov_b32_e32 v61, v2
	v_mov_b32_e32 v62, v2
	v_mov_b32_e32 v63, v2
	v_mov_b32_e32 v64, v2
	v_mov_b32_e32 v65, v2
	v_mov_b32_e32 v66, v2
	v_mov_b32_e32 v67, v2
	v_mov_b32_e32 v68, v2
	v_mov_b32_e32 v69, v2
	v_mov_b32_e32 v70, v2
	v_mov_b32_e32 v71, v2
	v_mov_b32_e32 v72, v2
	v_mov_b32_e32 v73, v2
	v_mov_b32_e32 v82, v2
	v_mov_b32_e32 v83, v2
	v_mov_b32_e32 v84, v2
	v_mov_b32_e32 v85, v2
	v_mov_b32_e32 v86, v2
	v_mov_b32_e32 v87, v2
	v_mov_b32_e32 v88, v2
	v_mov_b32_e32 v89, v2
	v_mov_b32_e32 v98, v2
	v_mov_b32_e32 v99, v2
	v_mov_b32_e32 v100, v2
	v_mov_b32_e32 v101, v2
	v_mov_b32_e32 v102, v2
	v_mov_b32_e32 v103, v2
	v_mov_b32_e32 v104, v2
	v_mov_b32_e32 v105, v2
	v_mov_b32_e32 v114, v2
	v_mov_b32_e32 v115, v2
	v_mov_b32_e32 v116, v2
	v_mov_b32_e32 v117, v2
	v_mov_b32_e32 v118, v2
	v_mov_b32_e32 v119, v2
	v_mov_b32_e32 v120, v2
	v_mov_b32_e32 v121, v2
	v_mov_b32_e32 v74, v2
	v_mov_b32_e32 v75, v2
	v_mov_b32_e32 v76, v2
	v_mov_b32_e32 v77, v2
	v_mov_b32_e32 v78, v2
	v_mov_b32_e32 v79, v2
	v_mov_b32_e32 v80, v2
	v_mov_b32_e32 v81, v2
	v_mov_b32_e32 v90, v2
	v_mov_b32_e32 v91, v2
	v_mov_b32_e32 v92, v2
	v_mov_b32_e32 v93, v2
	v_mov_b32_e32 v94, v2
	v_mov_b32_e32 v95, v2
	v_mov_b32_e32 v96, v2
	v_mov_b32_e32 v97, v2
	v_mov_b32_e32 v106, v2
	v_mov_b32_e32 v107, v2
	v_mov_b32_e32 v108, v2
	v_mov_b32_e32 v109, v2
	v_mov_b32_e32 v110, v2
	v_mov_b32_e32 v111, v2
	v_mov_b32_e32 v112, v2
	v_mov_b32_e32 v113, v2
	v_mov_b32_e32 v122, v2
	v_mov_b32_e32 v123, v2
	v_mov_b32_e32 v124, v2
	v_mov_b32_e32 v125, v2
	v_mov_b32_e32 v126, v2
	v_mov_b32_e32 v127, v2
	v_mov_b32_e32 v128, v2
	v_mov_b32_e32 v129, v2
	v_add_u32_e32 v170, 0x10000, v158
	ds_read_b128 v[152:155], v170
	ds_read_b128 v[162:165], v170 offset:1024
	ds_read_b128 v[166:169], v170 offset:2048
	ds_read_b128 v[170:173], v170 offset:3072
.LBB0_475:
	s_add_u32 s0, s30, 0xfffc0080
	s_addc_u32 s1, s31, -1
	s_add_i32 s33, 0, 0x10000
	s_cmp_eq_u32 s79, 12
	s_cselect_b32 s67, s5, s1
	s_cselect_b32 s66, s7, s0
	s_cselect_b32 s65, s9, s78
	s_cselect_b32 s64, s23, s77
	v_lshl_add_u64 v[156:157], s[30:31], 0, v[148:149]
	s_add_i32 m0, s40, 0xc000
	ds_read_b128 v[174:177], v161
	ds_read_b128 v[178:181], v161 offset:1024
	ds_read_b128 v[182:185], v161 offset:2048
	ds_read_b128 v[186:189], v161 offset:3072
	ds_read_b128 v[190:193], v161 offset:4096
	ds_read_b128 v[198:201], v161 offset:5120
	ds_read_b128 v[202:205], v161 offset:6144
	ds_read_b128 v[206:209], v161 offset:7168
	global_load_lds_dwordx4 v[156:157], off
	v_lshl_add_u64 v[156:157], s[30:31], 0, v[150:151]
	s_add_i32 m0, s40, 0xe000
	s_nop 0
	global_load_lds_dwordx4 v[156:157], off
	s_waitcnt lgkmcnt(8)
	s_barrier
	s_waitcnt lgkmcnt(0)
	s_waitcnt lgkmcnt(0)
	v_mfma_f32_16x16x32_bf16 v[126:129], v[152:155], v[174:177], v[126:129]
	v_mfma_f32_16x16x32_bf16 v[122:125], v[166:169], v[174:177], v[122:125]
	v_mfma_f32_16x16x32_bf16 v[110:113], v[152:155], v[182:185], v[110:113]
	v_mfma_f32_16x16x32_bf16 v[106:109], v[166:169], v[182:185], v[106:109]
	v_mfma_f32_16x16x32_bf16 v[94:97], v[152:155], v[190:193], v[94:97]
	v_mfma_f32_16x16x32_bf16 v[90:93], v[166:169], v[190:193], v[90:93]
	v_mfma_f32_16x16x32_bf16 v[78:81], v[152:155], v[202:205], v[78:81]
	v_mfma_f32_16x16x32_bf16 v[74:77], v[166:169], v[202:205], v[74:77]
	v_mfma_f32_16x16x32_bf16 v[126:129], v[162:165], v[178:181], v[126:129]
	v_mfma_f32_16x16x32_bf16 v[122:125], v[170:173], v[178:181], v[122:125]
	v_mfma_f32_16x16x32_bf16 v[110:113], v[162:165], v[186:189], v[110:113]
	v_mfma_f32_16x16x32_bf16 v[106:109], v[170:173], v[186:189], v[106:109]
	v_mfma_f32_16x16x32_bf16 v[94:97], v[162:165], v[198:201], v[94:97]
	v_mfma_f32_16x16x32_bf16 v[90:93], v[170:173], v[198:201], v[90:93]
	v_mfma_f32_16x16x32_bf16 v[78:81], v[162:165], v[206:209], v[78:81]
	v_mfma_f32_16x16x32_bf16 v[74:77], v[170:173], v[206:209], v[74:77]
	s_barrier
	s_add_i32 s36, 0, 0x14000
	v_add_u32_e32 v156, s36, v158
	s_add_i32 s0, s33, s38
	ds_read_b128 v[210:213], v156
	ds_read_b128 v[214:217], v156 offset:1024
	ds_read_b128 v[218:221], v156 offset:2048
	ds_read_b128 v[238:241], v156 offset:3072
	v_lshl_add_u64 v[156:157], s[64:65], 0, v[132:133]
	s_mov_b32 m0, s0
	v_lshl_add_u64 v[242:243], s[64:65], 0, v[136:137]
	global_load_lds_dwordx4 v[156:157], off
	s_add_i32 m0, s0, 0x2000
	s_nop 0
	global_load_lds_dwordx4 v[242:243], off
	s_barrier
	s_waitcnt lgkmcnt(0)
	s_waitcnt lgkmcnt(0)
	v_mfma_f32_16x16x32_bf16 v[118:121], v[210:213], v[174:177], v[118:121]
	v_mfma_f32_16x16x32_bf16 v[114:117], v[218:221], v[174:177], v[114:117]
	v_mfma_f32_16x16x32_bf16 v[102:105], v[210:213], v[182:185], v[102:105]
	v_mfma_f32_16x16x32_bf16 v[98:101], v[218:221], v[182:185], v[98:101]
	v_mfma_f32_16x16x32_bf16 v[86:89], v[210:213], v[190:193], v[86:89]
	v_mfma_f32_16x16x32_bf16 v[82:85], v[218:221], v[190:193], v[82:85]
	v_mfma_f32_16x16x32_bf16 v[70:73], v[210:213], v[202:205], v[70:73]
	v_mfma_f32_16x16x32_bf16 v[66:69], v[218:221], v[202:205], v[66:69]
	v_mfma_f32_16x16x32_bf16 v[118:121], v[214:217], v[178:181], v[118:121]
	v_mfma_f32_16x16x32_bf16 v[114:117], v[238:241], v[178:181], v[114:117]
	v_mfma_f32_16x16x32_bf16 v[102:105], v[214:217], v[186:189], v[102:105]
	v_mfma_f32_16x16x32_bf16 v[98:101], v[238:241], v[186:189], v[98:101]
	v_mfma_f32_16x16x32_bf16 v[86:89], v[214:217], v[198:201], v[86:89]
	v_mfma_f32_16x16x32_bf16 v[82:85], v[238:241], v[198:201], v[82:85]
	v_mfma_f32_16x16x32_bf16 v[70:73], v[214:217], v[206:209], v[70:73]
	v_mfma_f32_16x16x32_bf16 v[66:69], v[238:241], v[206:209], v[66:69]
	s_mov_b32 m0, s40
	v_lshl_add_u64 v[244:245], s[66:67], 0, v[130:131]
	s_barrier
	ds_read_b128 v[174:177], v161 offset:16384
	ds_read_b128 v[178:181], v161 offset:17408
	ds_read_b128 v[182:185], v161 offset:18432
	ds_read_b128 v[186:189], v161 offset:19456
	ds_read_b128 v[190:193], v161 offset:20480
	ds_read_b128 v[198:201], v161 offset:21504
	ds_read_b128 v[202:205], v161 offset:22528
	ds_read_b128 v[206:209], v161 offset:23552
	global_load_lds_dwordx4 v[244:245], off
	v_lshl_add_u64 v[246:247], s[66:67], 0, v[134:135]
	s_mov_b32 m0, s43
	s_nop 0
	global_load_lds_dwordx4 v[246:247], off
	s_waitcnt vmcnt(10)
	s_barrier
	s_waitcnt lgkmcnt(0)
	s_waitcnt lgkmcnt(0)
	v_mfma_f32_16x16x32_bf16 v[62:65], v[152:155], v[174:177], v[62:65]
	v_mfma_f32_16x16x32_bf16 v[58:61], v[166:169], v[174:177], v[58:61]
	v_mfma_f32_16x16x32_bf16 v[46:49], v[152:155], v[182:185], v[46:49]
	v_mfma_f32_16x16x32_bf16 v[42:45], v[166:169], v[182:185], v[42:45]
	v_mfma_f32_16x16x32_bf16 v[30:33], v[152:155], v[190:193], v[30:33]
	v_mfma_f32_16x16x32_bf16 v[26:29], v[166:169], v[190:193], v[26:29]
	v_mfma_f32_16x16x32_bf16 v[14:17], v[152:155], v[202:205], v[14:17]
	v_mfma_f32_16x16x32_bf16 v[10:13], v[166:169], v[202:205], v[10:13]
	v_mfma_f32_16x16x32_bf16 v[62:65], v[162:165], v[178:181], v[62:65]
	v_mfma_f32_16x16x32_bf16 v[58:61], v[170:173], v[178:181], v[58:61]
	v_mfma_f32_16x16x32_bf16 v[46:49], v[162:165], v[186:189], v[46:49]
	v_mfma_f32_16x16x32_bf16 v[42:45], v[170:173], v[186:189], v[42:45]
	v_mfma_f32_16x16x32_bf16 v[30:33], v[162:165], v[198:201], v[30:33]
	v_mfma_f32_16x16x32_bf16 v[26:29], v[170:173], v[198:201], v[26:29]
	v_mfma_f32_16x16x32_bf16 v[14:17], v[162:165], v[206:209], v[14:17]
	v_mfma_f32_16x16x32_bf16 v[10:13], v[170:173], v[206:209], v[10:13]
	s_barrier
	s_add_u32 s0, s64, 0x40000
	s_addc_u32 s1, s65, 0
	s_add_i32 s33, s36, s38
	v_lshl_add_u64 v[152:153], s[0:1], 0, v[132:133]
	s_mov_b32 m0, s33
	s_nop 0
	global_load_lds_dwordx4 v[152:153], off
	v_lshl_add_u64 v[152:153], s[0:1], 0, v[136:137]
	s_add_i32 m0, s33, 0x2000
	s_nop 0
	global_load_lds_dwordx4 v[152:153], off
	v_add_u32_e32 v170, 0x18000, v158
	ds_read_b128 v[152:155], v170
	ds_read_b128 v[162:165], v170 offset:1024
	ds_read_b128 v[166:169], v170 offset:2048
	ds_read_b128 v[170:173], v170 offset:3072
	s_waitcnt vmcnt(6)
	s_barrier
	v_mfma_f32_16x16x32_bf16 v[54:57], v[210:213], v[174:177], v[54:57]
	v_mfma_f32_16x16x32_bf16 v[50:53], v[218:221], v[174:177], v[50:53]
	v_mfma_f32_16x16x32_bf16 v[38:41], v[210:213], v[182:185], v[38:41]
	v_mfma_f32_16x16x32_bf16 v[34:37], v[218:221], v[182:185], v[34:37]
	v_mfma_f32_16x16x32_bf16 v[22:25], v[210:213], v[190:193], v[22:25]
	v_mfma_f32_16x16x32_bf16 v[18:21], v[218:221], v[190:193], v[18:21]
	v_mfma_f32_16x16x32_bf16 v[6:9], v[210:213], v[202:205], v[6:9]
	v_mfma_f32_16x16x32_bf16 v[2:5], v[218:221], v[202:205], v[2:5]
	v_mfma_f32_16x16x32_bf16 v[54:57], v[214:217], v[178:181], v[54:57]
	v_mfma_f32_16x16x32_bf16 v[50:53], v[238:241], v[178:181], v[50:53]
	v_mfma_f32_16x16x32_bf16 v[38:41], v[214:217], v[186:189], v[38:41]
	v_mfma_f32_16x16x32_bf16 v[34:37], v[238:241], v[186:189], v[34:37]
	v_mfma_f32_16x16x32_bf16 v[22:25], v[214:217], v[198:201], v[22:25]
	v_mfma_f32_16x16x32_bf16 v[18:21], v[238:241], v[198:201], v[18:21]
	v_mfma_f32_16x16x32_bf16 v[6:9], v[214:217], v[206:209], v[6:9]
	v_mfma_f32_16x16x32_bf16 v[2:5], v[238:241], v[206:209], v[2:5]
	s_add_i32 s33, 0, 0x18000
	s_barrier
	s_add_u32 s0, s66, 0x40000
	s_addc_u32 s1, s67, 0
	s_mov_b32 m0, s69
	v_lshl_add_u64 v[210:211], s[0:1], 0, v[130:131]
	ds_read_b128 v[174:177], v161 offset:32768
	ds_read_b128 v[178:181], v161 offset:33792
	ds_read_b128 v[182:185], v161 offset:34816
	ds_read_b128 v[186:189], v161 offset:35840
	ds_read_b128 v[190:193], v161 offset:36864
	ds_read_b128 v[198:201], v161 offset:37888
	ds_read_b128 v[202:205], v161 offset:38912
	ds_read_b128 v[206:209], v161 offset:39936
	global_load_lds_dwordx4 v[210:211], off
	v_lshl_add_u64 v[210:211], s[0:1], 0, v[134:135]
	s_mov_b32 m0, s70
	s_nop 0
	global_load_lds_dwordx4 v[210:211], off
	s_waitcnt lgkmcnt(8)
	s_barrier
	s_waitcnt lgkmcnt(0)
	s_waitcnt lgkmcnt(0)
	v_mfma_f32_16x16x32_bf16 v[126:129], v[152:155], v[174:177], v[126:129]
	v_mfma_f32_16x16x32_bf16 v[122:125], v[166:169], v[174:177], v[122:125]
	v_mfma_f32_16x16x32_bf16 v[110:113], v[152:155], v[182:185], v[110:113]
	v_mfma_f32_16x16x32_bf16 v[106:109], v[166:169], v[182:185], v[106:109]
	v_mfma_f32_16x16x32_bf16 v[94:97], v[152:155], v[190:193], v[94:97]
	v_mfma_f32_16x16x32_bf16 v[90:93], v[166:169], v[190:193], v[90:93]
	v_mfma_f32_16x16x32_bf16 v[78:81], v[152:155], v[202:205], v[78:81]
	v_mfma_f32_16x16x32_bf16 v[74:77], v[166:169], v[202:205], v[74:77]
	v_mfma_f32_16x16x32_bf16 v[126:129], v[162:165], v[178:181], v[126:129]
	v_mfma_f32_16x16x32_bf16 v[122:125], v[170:173], v[178:181], v[122:125]
	v_mfma_f32_16x16x32_bf16 v[110:113], v[162:165], v[186:189], v[110:113]
	v_mfma_f32_16x16x32_bf16 v[106:109], v[170:173], v[186:189], v[106:109]
	v_mfma_f32_16x16x32_bf16 v[94:97], v[162:165], v[198:201], v[94:97]
	v_mfma_f32_16x16x32_bf16 v[90:93], v[170:173], v[198:201], v[90:93]
	v_mfma_f32_16x16x32_bf16 v[78:81], v[162:165], v[206:209], v[78:81]
	v_mfma_f32_16x16x32_bf16 v[74:77], v[170:173], v[206:209], v[74:77]
	s_barrier
	s_add_i32 s36, 0, 0x1c000
	s_add_i32 s0, s33, s38
	v_add_u32_e32 v194, s36, v158
	v_lshl_add_u64 v[156:157], v[156:157], 0, s[54:55]
	s_mov_b32 m0, s0
	ds_read_b128 v[210:213], v194
	ds_read_b128 v[214:217], v194 offset:1024
	ds_read_b128 v[218:221], v194 offset:2048
	ds_read_b128 v[238:241], v194 offset:3072
	global_load_lds_dwordx4 v[156:157], off
	v_lshl_add_u64 v[156:157], v[242:243], 0, s[54:55]
	s_add_i32 m0, s0, 0x2000
	s_nop 0
	global_load_lds_dwordx4 v[156:157], off
	s_barrier
	s_waitcnt lgkmcnt(0)
	s_waitcnt lgkmcnt(0)
	v_mfma_f32_16x16x32_bf16 v[118:121], v[210:213], v[174:177], v[118:121]
	v_mfma_f32_16x16x32_bf16 v[114:117], v[218:221], v[174:177], v[114:117]
	v_mfma_f32_16x16x32_bf16 v[102:105], v[210:213], v[182:185], v[102:105]
	v_mfma_f32_16x16x32_bf16 v[98:101], v[218:221], v[182:185], v[98:101]
	v_mfma_f32_16x16x32_bf16 v[86:89], v[210:213], v[190:193], v[86:89]
	v_mfma_f32_16x16x32_bf16 v[82:85], v[218:221], v[190:193], v[82:85]
	v_mfma_f32_16x16x32_bf16 v[70:73], v[210:213], v[202:205], v[70:73]
	v_mfma_f32_16x16x32_bf16 v[66:69], v[218:221], v[202:205], v[66:69]
	v_mfma_f32_16x16x32_bf16 v[118:121], v[214:217], v[178:181], v[118:121]
	v_mfma_f32_16x16x32_bf16 v[114:117], v[238:241], v[178:181], v[114:117]
	v_mfma_f32_16x16x32_bf16 v[102:105], v[214:217], v[186:189], v[102:105]
	v_mfma_f32_16x16x32_bf16 v[98:101], v[238:241], v[186:189], v[98:101]
	v_mfma_f32_16x16x32_bf16 v[86:89], v[214:217], v[198:201], v[86:89]
	v_mfma_f32_16x16x32_bf16 v[82:85], v[238:241], v[198:201], v[82:85]
	v_mfma_f32_16x16x32_bf16 v[70:73], v[214:217], v[206:209], v[70:73]
	v_mfma_f32_16x16x32_bf16 v[66:69], v[238:241], v[206:209], v[66:69]
	s_mov_b32 m0, s71
	v_lshl_add_u64 v[156:157], v[244:245], 0, s[54:55]
	s_barrier
	ds_read_b128 v[174:177], v161 offset:49152
	ds_read_b128 v[178:181], v161 offset:50176
	ds_read_b128 v[182:185], v161 offset:51200
	ds_read_b128 v[186:189], v161 offset:52224
	ds_read_b128 v[190:193], v161 offset:53248
	ds_read_b128 v[198:201], v161 offset:54272
	ds_read_b128 v[202:205], v161 offset:55296
	ds_read_b128 v[206:209], v161 offset:56320
	global_load_lds_dwordx4 v[156:157], off
	v_lshl_add_u64 v[156:157], v[246:247], 0, s[54:55]
	s_mov_b32 m0, s72
	s_nop 0
	global_load_lds_dwordx4 v[156:157], off
	s_waitcnt vmcnt(10)
	s_barrier
	s_waitcnt lgkmcnt(0)
	s_waitcnt lgkmcnt(0)
	v_mfma_f32_16x16x32_bf16 v[62:65], v[152:155], v[174:177], v[62:65]
	v_mfma_f32_16x16x32_bf16 v[58:61], v[166:169], v[174:177], v[58:61]
	v_mfma_f32_16x16x32_bf16 v[46:49], v[152:155], v[182:185], v[46:49]
	v_mfma_f32_16x16x32_bf16 v[42:45], v[166:169], v[182:185], v[42:45]
	v_mfma_f32_16x16x32_bf16 v[30:33], v[152:155], v[190:193], v[30:33]
	v_mfma_f32_16x16x32_bf16 v[26:29], v[166:169], v[190:193], v[26:29]
	v_mfma_f32_16x16x32_bf16 v[14:17], v[152:155], v[202:205], v[14:17]
	v_mfma_f32_16x16x32_bf16 v[10:13], v[166:169], v[202:205], v[10:13]
	v_mfma_f32_16x16x32_bf16 v[62:65], v[162:165], v[178:181], v[62:65]
	v_mfma_f32_16x16x32_bf16 v[58:61], v[170:173], v[178:181], v[58:61]
	v_mfma_f32_16x16x32_bf16 v[46:49], v[162:165], v[186:189], v[46:49]
	v_mfma_f32_16x16x32_bf16 v[42:45], v[170:173], v[186:189], v[42:45]
	v_mfma_f32_16x16x32_bf16 v[30:33], v[162:165], v[198:201], v[30:33]
	v_mfma_f32_16x16x32_bf16 v[26:29], v[170:173], v[198:201], v[26:29]
	v_mfma_f32_16x16x32_bf16 v[14:17], v[162:165], v[206:209], v[14:17]
	v_mfma_f32_16x16x32_bf16 v[10:13], v[170:173], v[206:209], v[10:13]
	s_barrier
	s_add_u32 s0, s64, 0x40080
	s_addc_u32 s1, s65, 0
	s_add_i32 s33, s36, s38
	v_lshl_add_u64 v[152:153], s[0:1], 0, v[132:133]
	s_mov_b32 m0, s33
	s_nop 0
	global_load_lds_dwordx4 v[152:153], off
	v_lshl_add_u64 v[152:153], s[0:1], 0, v[136:137]
	s_add_i32 m0, s33, 0x2000
	s_nop 0
	global_load_lds_dwordx4 v[152:153], off
	v_add_u32_e32 v170, 0x10000, v158
	ds_read_b128 v[152:155], v170
	ds_read_b128 v[162:165], v170 offset:1024
	ds_read_b128 v[166:169], v170 offset:2048
	ds_read_b128 v[170:173], v170 offset:3072
	s_waitcnt vmcnt(6)
	s_barrier
	v_mfma_f32_16x16x32_bf16 v[54:57], v[210:213], v[174:177], v[54:57]
	v_mfma_f32_16x16x32_bf16 v[50:53], v[218:221], v[174:177], v[50:53]
	v_mfma_f32_16x16x32_bf16 v[38:41], v[210:213], v[182:185], v[38:41]
	v_mfma_f32_16x16x32_bf16 v[34:37], v[218:221], v[182:185], v[34:37]
	v_mfma_f32_16x16x32_bf16 v[22:25], v[210:213], v[190:193], v[22:25]
	v_mfma_f32_16x16x32_bf16 v[18:21], v[218:221], v[190:193], v[18:21]
	v_mfma_f32_16x16x32_bf16 v[6:9], v[210:213], v[202:205], v[6:9]
	v_mfma_f32_16x16x32_bf16 v[2:5], v[218:221], v[202:205], v[2:5]
	v_mfma_f32_16x16x32_bf16 v[54:57], v[214:217], v[178:181], v[54:57]
	v_mfma_f32_16x16x32_bf16 v[50:53], v[238:241], v[178:181], v[50:53]
	v_mfma_f32_16x16x32_bf16 v[38:41], v[214:217], v[186:189], v[38:41]
	v_mfma_f32_16x16x32_bf16 v[34:37], v[238:241], v[186:189], v[34:37]
	v_mfma_f32_16x16x32_bf16 v[22:25], v[214:217], v[198:201], v[22:25]
	v_mfma_f32_16x16x32_bf16 v[18:21], v[238:241], v[198:201], v[18:21]
	v_mfma_f32_16x16x32_bf16 v[6:9], v[214:217], v[206:209], v[6:9]
	v_mfma_f32_16x16x32_bf16 v[2:5], v[238:241], v[206:209], v[2:5]
	s_add_i32 s79, s79, 2
	s_add_u32 s30, s30, 0x100
	s_addc_u32 s31, s31, 0
	s_add_u32 s77, s77, 0x100
	s_addc_u32 s78, s78, 0
	s_cmp_gt_u32 s79, 13
	s_barrier
	s_cbranch_scc0 .LBB0_475
	s_waitcnt lgkmcnt(0)
	s_lshl_b32 s0, s6, 8
	v_lshl_add_u32 v162, s4, 8, v139
	v_or_b32_e32 v152, s0, v138
	s_addk_i32 s0, 0xf200
	v_ashrrev_i32_e32 v155, 5, v162
	s_lshr_b32 s9, s0, 8
	v_and_b32_e32 v155, -8, v155
	v_add_u32_e32 v154, 0xfffffe00, v152
	s_movk_i32 s1, 0x3ff
	v_add_u32_e32 v156, s9, v155
	v_cmp_lt_u32_e64 s[6:7], s1, v154
	s_movk_i32 s1, 0xdff
	v_ashrrev_i32_e32 v157, 31, v156
	v_cmp_lt_i32_e64 s[4:5], s1, v152
	v_ashrrev_i32_e32 v153, 31, v152
	v_lshlrev_b64 v[156:157], 17, v[156:157]
	s_and_saveexec_b64 s[0:1], s[6:7]
	s_xor_b64 s[30:31], exec, s[0:1]
	s_cbranch_execz .LBB0_482
	s_and_saveexec_b64 s[0:1], s[4:5]
	s_xor_b64 s[64:65], exec, s[0:1]
	s_cbranch_execz .LBB0_479
	v_mul_f32_e32 v155, 0xbfb8aa3b, v126
	v_exp_f32_e32 v155, v155
	v_mul_f32_e32 v163, 0xbfb8aa3b, v122
	v_exp_f32_e32 v163, v163
	v_mul_f32_e32 v165, 0xbfb8aa3b, v114
	v_add_f32_e32 v155, 1.0, v155
	v_rcp_f32_e32 v168, v155
	v_add_f32_e32 v155, 1.0, v163
	v_rcp_f32_e32 v170, v155
	v_mul_f32_e32 v155, 0xbfb8aa3b, v127
	v_exp_f32_e32 v155, v155
	v_mul_f32_e32 v163, 0xbfb8aa3b, v123
	v_exp_f32_e32 v163, v163
	v_mul_f32_e32 v164, 0xbfb8aa3b, v118
	v_exp_f32_e32 v166, v165
	v_mul_f32_e32 v165, 0xbfb8aa3b, v119
	v_exp_f32_e32 v164, v164
	v_exp_f32_e32 v165, v165
	v_mul_f32_e32 v167, 0xbfb8aa3b, v115
	v_add_f32_e32 v155, 1.0, v155
	v_rcp_f32_e32 v169, v155
	v_exp_f32_e32 v167, v167
	v_add_f32_e32 v163, 1.0, v163
	v_rcp_f32_e32 v171, v163
	v_pk_add_f32 v[164:165], v[164:165], 1.0 op_sel_hi:[1,0]
	v_mul_f32_e32 v178, 0xbfb8aa3b, v117
	v_rcp_f32_e32 v155, v164
	v_pk_mul_f32 v[168:169], v[168:169], v[164:165]
	v_rcp_f32_e32 v163, v165
	v_pk_add_f32 v[164:165], v[166:167], 1.0 op_sel_hi:[1,0]
	s_nop 0
	v_rcp_f32_e32 v176, v164
	v_pk_mul_f32 v[166:167], v[170:171], v[164:165]
	v_mul_f32_e32 v164, 0xbfb8aa3b, v128
	v_rcp_f32_e32 v177, v165
	v_exp_f32_e32 v165, v164
	v_mul_f32_e32 v164, 0xbfb8aa3b, v124
	v_exp_f32_e32 v171, v164
	v_mul_f32_e32 v164, 0xbfb8aa3b, v120
	v_add_f32_e32 v165, 1.0, v165
	v_rcp_f32_e32 v172, v165
	v_add_f32_e32 v165, 1.0, v171
	v_rcp_f32_e32 v174, v165
	v_mul_f32_e32 v165, 0xbfb8aa3b, v129
	v_exp_f32_e32 v171, v165
	v_mul_f32_e32 v165, 0xbfb8aa3b, v125
	v_exp_f32_e32 v175, v165
	v_mul_f32_e32 v165, 0xbfb8aa3b, v121
	v_exp_f32_e32 v164, v164
	v_exp_f32_e32 v165, v165
	v_add_f32_e32 v171, 1.0, v171
	v_rcp_f32_e32 v173, v171
	v_mul_f32_e32 v170, 0xbfb8aa3b, v116
	v_exp_f32_e32 v170, v170
	v_exp_f32_e32 v171, v178
	v_pk_add_f32 v[164:165], v[164:165], 1.0 op_sel_hi:[1,0]
	v_cvt_pk_bf16_f32 v166, v166, v167
	v_rcp_f32_e32 v178, v164
	v_pk_mul_f32 v[172:173], v[172:173], v[164:165]
	v_add_f32_e32 v164, 1.0, v175
	v_rcp_f32_e32 v175, v164
	v_rcp_f32_e32 v179, v165
	v_pk_add_f32 v[164:165], v[170:171], 1.0 op_sel_hi:[1,0]
	s_nop 0
	v_rcp_f32_e32 v180, v164
	v_rcp_f32_e32 v181, v165
	v_pk_mul_f32 v[170:171], v[174:175], v[164:165]
	v_lshl_add_u64 v[174:175], v[140:141], 0, v[156:157]
	v_cvt_pk_bf16_f32 v164, v168, v169
	v_cvt_pk_bf16_f32 v165, v172, v173
	v_cvt_pk_bf16_f32 v167, v170, v171
	v_add_co_u32_e32 v168, vcc, 0x10000, v174
	global_store_dwordx4 v[174:175], v[164:167], off
	s_nop 0
	v_addc_co_u32_e32 v169, vcc, 0, v175, vcc
	v_cvt_pk_bf16_f32 v164, v155, v163
	v_cvt_pk_bf16_f32 v165, v178, v179
	v_cvt_pk_bf16_f32 v166, v176, v177
	v_cvt_pk_bf16_f32 v167, v180, v181
	global_store_dwordx4 v[168:169], v[164:167], off

.LBB0_1114:
	v_writelane_b32 v255, s0, 11
	s_and_b32 s5, s0, 1
	v_readlane_b32 s0, v254, 35
	v_readlane_b32 s1, v254, 36
	s_andn2_b64 vcc, exec, s[0:1]
	s_mov_b64 s[76:77], -1
	v_cndmask_b32_e64 v194, 0, 1, s[0:1]
	v_cmp_ne_u32_e64 s[8:9], 1, v194
	s_mul_i32 s0, s5, 0x1e00
	v_writelane_b32 v255, s8, 17
	v_writelane_b32 v255, s9, 18
	v_writelane_b32 v255, s5, 13
	s_cbranch_vccnz .LBB0_1116
	v_readlane_b32 s0, v255, 13
	s_nop 1
	s_nop 0
	s_mul_i32 s1, s0, 0x1e00
	s_lshl_b32 s0, s0, 13
	v_add_u32_e32 v252, s1, v166
	v_add_u32_e32 v253, s0, v165
	ds_read2_b64 v[68:71], v252 offset1:80
	v_cvt_pk_bf16_f32 v198, v2, v3
	v_cvt_pk_bf16_f32 v199, v4, v5
	v_cvt_pk_bf16_f32 v202, v10, v11
	v_cvt_pk_bf16_f32 v203, v12, v13
	v_cvt_pk_bf16_f32 v200, v6, v7
	v_cvt_pk_bf16_f32 v201, v8, v9
	v_cvt_pk_bf16_f32 v204, v14, v15
	v_cvt_pk_bf16_f32 v205, v16, v17
	ds_read2_b64 v[26:29], v247 offset1:4
	ds_read2_b64 v[30:33], v247 offset0:8 offset1:12
	ds_read2_b64 v[72:75], v252 offset0:160 offset1:240
	v_mfma_f32_16x16x16_bf16 v[206:209], v[18:19], v[198:199], 0
	v_mfma_f32_16x16x16_bf16 v[210:213], v[22:23], v[202:203], 0
	ds_read_b64_tr_b16 v[34:35], v248 offset:9216
	ds_read_b64_tr_b16 v[36:37], v248 offset:9248
	ds_read_b64_tr_b16 v[38:39], v248 offset:9280
	ds_read_b64_tr_b16 v[40:41], v248 offset:9312
	v_mfma_f32_16x16x16_bf16 v[206:209], v[20:21], v[200:201], v[206:209]
	v_mfma_f32_16x16x16_bf16 v[210:213], v[24:25], v[204:205], v[210:213]
	ds_read_b64_tr_b16 v[42:43], v248 offset:13824
	ds_read_b64_tr_b16 v[44:45], v248 offset:13856
	ds_read_b64_tr_b16 v[46:47], v248 offset:13888
	ds_read_b64_tr_b16 v[48:49], v248 offset:13920
	s_waitcnt lgkmcnt(11)
	v_mfma_f32_16x16x16_bf16 v[210:213], v[68:69], v[66:67], v[210:213]
	s_waitcnt lgkmcnt(10)
	v_mfma_f32_16x16x16_bf16 v[214:217], v[26:27], v[198:199], 0
	s_waitcnt lgkmcnt(9)
	v_mfma_f32_16x16x16_bf16 v[218:221], v[30:31], v[202:203], 0
	v_mfma_f32_16x16x16_bf16 v[214:217], v[28:29], v[200:201], v[214:217]
	v_mfma_f32_16x16x16_bf16 v[218:221], v[32:33], v[204:205], v[218:221]
	ds_read_b32 v50, v251 offset:33792
	ds_read_b32 v51, v251 offset:34048
	v_add_u32_e32 v246, 0x900, v246
	ds_read2_b64 v[76:79], v246 offset1:4
	ds_read2_b64 v[80:83], v246 offset0:8 offset1:12
	v_add_f32_e32 v206, v206, v210
	v_add_f32_e32 v207, v207, v211
	v_add_f32_e32 v208, v208, v212
	v_add_f32_e32 v209, v209, v213
	v_cvt_pk_bf16_f32 v242, v206, v207
	v_cvt_pk_bf16_f32 v243, v208, v209
	ds_read_b64_tr_b16 v[84:85], v250 offset:20736
	v_add_u32_e32 v252, 0xf00, v252
	s_waitcnt lgkmcnt(13)
	ds_read2_b64 v[86:89], v252 offset1:80
	v_mfma_f32_16x16x16_bf16 v[238:241], v[74:75], v[242:243], 0
	v_mfma_f32_16x16x16_bf16 v[214:217], v[70:71], v[66:67], v[214:217]
	s_waitcnt lgkmcnt(12)
	v_mfma_f32_16x16x16_bf16 v[2:5], v[34:35], v[66:67], v[2:5]
	v_mfma_f32_16x16x16_bf16 v[6:9], v[36:37], v[66:67], v[6:9]
	s_waitcnt lgkmcnt(10)
	v_mfma_f32_16x16x16_bf16 v[10:13], v[38:39], v[66:67], v[10:13]
	v_mfma_f32_16x16x16_bf16 v[14:17], v[40:41], v[66:67], v[14:17]
	ds_read2_b64 v[90:93], v252 offset0:160 offset1:240
	v_add_u32_e32 v247, 0x900, v247
	ds_read2_b64 v[26:29], v247 offset1:4
	ds_read2_b64 v[30:33], v247 offset0:8 offset1:12
	v_cvt_pk_bf16_f32 v244, -v238, -v239
	v_cvt_pk_bf16_f32 v245, -v240, -v241
	ds_read_b64_tr_b16 v[34:35], v248 offset:11520
	s_waitcnt lgkmcnt(13)
	ds_read_b64_tr_b16 v[36:37], v248 offset:11552
	s_waitcnt lgkmcnt(13)
	ds_read_b64_tr_b16 v[38:39], v248 offset:11584
	s_waitcnt lgkmcnt(13)
	ds_read_b64_tr_b16 v[40:41], v248 offset:11616
	v_mfma_f32_16x16x16_bf16 v[2:5], v[42:43], v[244:245], v[2:5]
	v_mfma_f32_16x16x16_bf16 v[6:9], v[44:45], v[244:245], v[6:9]
	s_waitcnt lgkmcnt(13)
	v_mfma_f32_16x16x16_bf16 v[10:13], v[46:47], v[244:245], v[10:13]
	v_mfma_f32_16x16x16_bf16 v[14:17], v[48:49], v[244:245], v[14:17]
	v_mfma_f32_16x16x16_bf16 v[218:221], v[72:73], v[244:245], v[218:221]
	ds_read_b64_tr_b16 v[42:43], v248 offset:16128
	s_waitcnt lgkmcnt(13)
	ds_read_b64_tr_b16 v[44:45], v248 offset:16160
	s_waitcnt lgkmcnt(13)
	ds_read_b64_tr_b16 v[46:47], v248 offset:16192
	s_waitcnt lgkmcnt(13)
	ds_read_b64_tr_b16 v[48:49], v248 offset:16224
	v_mul_f32_dpp v2, v50, v2 row_newbcast:0 row_mask:0xf bank_mask:0xf
	v_mul_f32_dpp v3, v50, v3 row_newbcast:1 row_mask:0xf bank_mask:0xf
	v_mul_f32_dpp v4, v50, v4 row_newbcast:2 row_mask:0xf bank_mask:0xf
	v_mul_f32_dpp v5, v50, v5 row_newbcast:3 row_mask:0xf bank_mask:0xf
	v_mul_f32_dpp v6, v50, v6 row_newbcast:4 row_mask:0xf bank_mask:0xf
	v_mul_f32_dpp v7, v50, v7 row_newbcast:5 row_mask:0xf bank_mask:0xf
	v_mul_f32_dpp v8, v50, v8 row_newbcast:6 row_mask:0xf bank_mask:0xf
	v_mul_f32_dpp v9, v50, v9 row_newbcast:7 row_mask:0xf bank_mask:0xf
	v_mul_f32_dpp v10, v50, v10 row_newbcast:8 row_mask:0xf bank_mask:0xf
	v_mul_f32_dpp v11, v50, v11 row_newbcast:9 row_mask:0xf bank_mask:0xf
	v_mul_f32_dpp v12, v50, v12 row_newbcast:10 row_mask:0xf bank_mask:0xf
	v_mul_f32_dpp v13, v50, v13 row_newbcast:11 row_mask:0xf bank_mask:0xf
	v_mul_f32_dpp v14, v50, v14 row_newbcast:12 row_mask:0xf bank_mask:0xf
	v_mul_f32_dpp v15, v50, v15 row_newbcast:13 row_mask:0xf bank_mask:0xf
	v_mul_f32_dpp v16, v50, v16 row_newbcast:14 row_mask:0xf bank_mask:0xf
	v_mul_f32_dpp v17, v50, v17 row_newbcast:15 row_mask:0xf bank_mask:0xf
	v_add_f32_e32 v214, v214, v218
	v_add_f32_e32 v215, v215, v219
	v_add_f32_e32 v216, v216, v220
	v_add_f32_e32 v217, v217, v221
	s_waitcnt lgkmcnt(13)
	ds_write2st64_b32 v253, v214, v215 offset0:0 offset1:1
	s_waitcnt lgkmcnt(13)
	ds_write2st64_b32 v253, v216, v217 offset0:2 offset1:3
	v_cvt_pk_bf16_f32 v198, v2, v3
	v_cvt_pk_bf16_f32 v199, v4, v5
	v_cvt_pk_bf16_f32 v202, v10, v11
	v_cvt_pk_bf16_f32 v203, v12, v13
	v_cvt_pk_bf16_f32 v200, v6, v7
	v_cvt_pk_bf16_f32 v201, v8, v9
	v_cvt_pk_bf16_f32 v204, v14, v15
	v_cvt_pk_bf16_f32 v205, v16, v17
	v_add_u32_e32 v246, v115, v155
	v_bfe_u32 v248, v0, 4, 2
	v_mul_u32_u24_e32 v248, 0x240, v248
	v_bfe_u32 v249, v0, 2, 2
	v_mul_u32_u24_e32 v249, 0x90, v249
	v_and_b32_e32 v250, 3, v0
	v_add_u32_e32 v248, v248, v249
	v_lshl_add_u32 v248, v250, 3, v248
	v_bfe_u32 v249, v0, 6, 2
	v_add_u32_e32 v246, 0x8600, v246
	v_add_u32_e32 v248, 0x8600, v248
	v_and_b32_e32 v251, 12, v0
	v_lshl_add_u32 v251, v251, 4, v113
	v_lshl_add_u32 v251, v250, 2, v251
	v_add_u32_e32 v251, 0x8600, v251
	v_lshl_add_u32 v250, v249, 5, v248
	v_add_u32_e32 v247, 0x1200, v246
	s_waitcnt lgkmcnt(13)
	ds_read2_b64 v[18:21], v246 offset1:4
	s_waitcnt lgkmcnt(13)
	ds_read2_b64 v[22:25], v246 offset0:8 offset1:12
	s_waitcnt lgkmcnt(13)
	ds_read_b64_tr_b16 v[66:67], v250 offset:18432
	v_mfma_f32_16x16x16_bf16 v[206:209], v[76:77], v[198:199], 0
	v_mfma_f32_16x16x16_bf16 v[210:213], v[80:81], v[202:203], 0
	v_mfma_f32_16x16x16_bf16 v[206:209], v[78:79], v[200:201], v[206:209]
	v_mfma_f32_16x16x16_bf16 v[210:213], v[82:83], v[204:205], v[210:213]
	v_mfma_f32_16x16x16_bf16 v[210:213], v[86:87], v[84:85], v[210:213]
	v_mfma_f32_16x16x16_bf16 v[214:217], v[26:27], v[198:199], 0
	s_waitcnt lgkmcnt(13)
	v_mfma_f32_16x16x16_bf16 v[218:221], v[30:31], v[202:203], 0
	v_mfma_f32_16x16x16_bf16 v[214:217], v[28:29], v[200:201], v[214:217]
	v_mfma_f32_16x16x16_bf16 v[218:221], v[32:33], v[204:205], v[218:221]
	s_nop 2
	v_add_f32_e32 v206, v206, v210
	v_add_f32_e32 v207, v207, v211
	v_add_f32_e32 v208, v208, v212
	v_add_f32_e32 v209, v209, v213
	v_cvt_pk_bf16_f32 v242, v206, v207
	v_cvt_pk_bf16_f32 v243, v208, v209
	s_nop 1
	v_mfma_f32_16x16x16_bf16 v[238:241], v[92:93], v[242:243], 0
	v_mfma_f32_16x16x16_bf16 v[214:217], v[88:89], v[84:85], v[214:217]
	s_waitcnt lgkmcnt(11)
	v_mfma_f32_16x16x16_bf16 v[2:5], v[34:35], v[84:85], v[2:5]
	v_mfma_f32_16x16x16_bf16 v[6:9], v[36:37], v[84:85], v[6:9]
	s_waitcnt lgkmcnt(9)
	v_mfma_f32_16x16x16_bf16 v[10:13], v[38:39], v[84:85], v[10:13]
	v_mfma_f32_16x16x16_bf16 v[14:17], v[40:41], v[84:85], v[14:17]
	s_nop 0
	v_cvt_pk_bf16_f32 v244, -v238, -v239
	v_cvt_pk_bf16_f32 v245, -v240, -v241
	s_waitcnt lgkmcnt(7)
	s_nop 0
	v_mfma_f32_16x16x16_bf16 v[2:5], v[42:43], v[244:245], v[2:5]
	v_mfma_f32_16x16x16_bf16 v[6:9], v[44:45], v[244:245], v[6:9]
	s_waitcnt lgkmcnt(5)
	v_mfma_f32_16x16x16_bf16 v[10:13], v[46:47], v[244:245], v[10:13]
	v_mfma_f32_16x16x16_bf16 v[14:17], v[48:49], v[244:245], v[14:17]
	v_mfma_f32_16x16x16_bf16 v[218:221], v[90:91], v[244:245], v[218:221]
	s_nop 2
	v_mul_f32_dpp v2, v51, v2 row_newbcast:0 row_mask:0xf bank_mask:0xf
	v_mul_f32_dpp v3, v51, v3 row_newbcast:1 row_mask:0xf bank_mask:0xf
	v_mul_f32_dpp v4, v51, v4 row_newbcast:2 row_mask:0xf bank_mask:0xf
	v_mul_f32_dpp v5, v51, v5 row_newbcast:3 row_mask:0xf bank_mask:0xf
	v_mul_f32_dpp v6, v51, v6 row_newbcast:4 row_mask:0xf bank_mask:0xf
	v_mul_f32_dpp v7, v51, v7 row_newbcast:5 row_mask:0xf bank_mask:0xf
	v_mul_f32_dpp v8, v51, v8 row_newbcast:6 row_mask:0xf bank_mask:0xf
	v_mul_f32_dpp v9, v51, v9 row_newbcast:7 row_mask:0xf bank_mask:0xf
	v_mul_f32_dpp v10, v51, v10 row_newbcast:8 row_mask:0xf bank_mask:0xf
	v_mul_f32_dpp v11, v51, v11 row_newbcast:9 row_mask:0xf bank_mask:0xf
	v_mul_f32_dpp v12, v51, v12 row_newbcast:10 row_mask:0xf bank_mask:0xf
	v_mul_f32_dpp v13, v51, v13 row_newbcast:11 row_mask:0xf bank_mask:0xf
	v_mul_f32_dpp v14, v51, v14 row_newbcast:12 row_mask:0xf bank_mask:0xf
	v_mul_f32_dpp v15, v51, v15 row_newbcast:13 row_mask:0xf bank_mask:0xf
	v_mul_f32_dpp v16, v51, v16 row_newbcast:14 row_mask:0xf bank_mask:0xf
	v_mul_f32_dpp v17, v51, v17 row_newbcast:15 row_mask:0xf bank_mask:0xf
	v_add_f32_e32 v214, v214, v218
	v_add_f32_e32 v215, v215, v219
	v_add_f32_e32 v216, v216, v220
	v_add_f32_e32 v217, v217, v221
	ds_write2st64_b32 v253, v214, v215 offset0:16 offset1:17
	ds_write2st64_b32 v253, v216, v217 offset0:18 offset1:19
	s_branch .Lscan_join1

.LBB0_1140:
.Lscan_join1:
	s_waitcnt lgkmcnt(0)
	s_barrier
	v_readlane_b32 s0, v255, 17
	v_readlane_b32 s1, v255, 18
	s_and_b64 vcc, exec, s[0:1]
	s_mov_b64 s[76:77], -1
	s_cbranch_vccnz .LBB0_1142
	v_readlane_b32 s0, v255, 13
	s_nop 1
	s_xor_b32 s0, s0, 1
	s_mul_i32 s1, s0, 0x1e00
	s_lshl_b32 s0, s0, 13
	v_add_u32_e32 v252, s1, v166
	v_add_u32_e32 v253, s0, v165
	ds_read2_b64 v[68:71], v252 offset1:80
	v_cvt_pk_bf16_f32 v198, v2, v3
	v_cvt_pk_bf16_f32 v199, v4, v5
	v_cvt_pk_bf16_f32 v202, v10, v11
	v_cvt_pk_bf16_f32 v203, v12, v13
	v_cvt_pk_bf16_f32 v200, v6, v7
	v_cvt_pk_bf16_f32 v201, v8, v9
	v_cvt_pk_bf16_f32 v204, v14, v15
	v_cvt_pk_bf16_f32 v205, v16, v17
	ds_read2_b64 v[26:29], v247 offset1:4
	ds_read2_b64 v[30:33], v247 offset0:8 offset1:12
	ds_read2_b64 v[72:75], v252 offset0:160 offset1:240
	v_mfma_f32_16x16x16_bf16 v[206:209], v[18:19], v[198:199], 0
	v_mfma_f32_16x16x16_bf16 v[210:213], v[22:23], v[202:203], 0
	ds_read_b64_tr_b16 v[34:35], v248 offset:9216
	ds_read_b64_tr_b16 v[36:37], v248 offset:9248
	ds_read_b64_tr_b16 v[38:39], v248 offset:9280
	ds_read_b64_tr_b16 v[40:41], v248 offset:9312
	v_mfma_f32_16x16x16_bf16 v[206:209], v[20:21], v[200:201], v[206:209]
	v_mfma_f32_16x16x16_bf16 v[210:213], v[24:25], v[204:205], v[210:213]
	ds_read_b64_tr_b16 v[42:43], v248 offset:13824
	ds_read_b64_tr_b16 v[44:45], v248 offset:13856
	ds_read_b64_tr_b16 v[46:47], v248 offset:13888
	ds_read_b64_tr_b16 v[48:49], v248 offset:13920
	s_waitcnt lgkmcnt(11)
	v_mfma_f32_16x16x16_bf16 v[210:213], v[68:69], v[66:67], v[210:213]
	s_waitcnt lgkmcnt(10)
	v_mfma_f32_16x16x16_bf16 v[214:217], v[26:27], v[198:199], 0
	s_waitcnt lgkmcnt(9)
	v_mfma_f32_16x16x16_bf16 v[218:221], v[30:31], v[202:203], 0
	v_mfma_f32_16x16x16_bf16 v[214:217], v[28:29], v[200:201], v[214:217]
	v_mfma_f32_16x16x16_bf16 v[218:221], v[32:33], v[204:205], v[218:221]
	ds_read_b32 v50, v251 offset:33792
	ds_read_b32 v51, v251 offset:34048
	v_add_u32_e32 v246, 0x900, v246
	ds_read2_b64 v[76:79], v246 offset1:4
	ds_read2_b64 v[80:83], v246 offset0:8 offset1:12
	v_add_f32_e32 v206, v206, v210
	v_add_f32_e32 v207, v207, v211
	v_add_f32_e32 v208, v208, v212
	v_add_f32_e32 v209, v209, v213
	v_cvt_pk_bf16_f32 v242, v206, v207
	v_cvt_pk_bf16_f32 v243, v208, v209
	ds_read_b64_tr_b16 v[84:85], v250 offset:20736
	v_add_u32_e32 v252, 0xf00, v252
	s_waitcnt lgkmcnt(13)
	ds_read2_b64 v[86:89], v252 offset1:80
	v_mfma_f32_16x16x16_bf16 v[238:241], v[74:75], v[242:243], 0
	v_mfma_f32_16x16x16_bf16 v[214:217], v[70:71], v[66:67], v[214:217]
	s_waitcnt lgkmcnt(12)
	v_mfma_f32_16x16x16_bf16 v[2:5], v[34:35], v[66:67], v[2:5]
	v_mfma_f32_16x16x16_bf16 v[6:9], v[36:37], v[66:67], v[6:9]
	s_waitcnt lgkmcnt(10)
	v_mfma_f32_16x16x16_bf16 v[10:13], v[38:39], v[66:67], v[10:13]
	v_mfma_f32_16x16x16_bf16 v[14:17], v[40:41], v[66:67], v[14:17]
	ds_read2_b64 v[90:93], v252 offset0:160 offset1:240
	v_add_u32_e32 v247, 0x900, v247
	ds_read2_b64 v[26:29], v247 offset1:4
	ds_read2_b64 v[30:33], v247 offset0:8 offset1:12
	v_cvt_pk_bf16_f32 v244, -v238, -v239
	v_cvt_pk_bf16_f32 v245, -v240, -v241
	ds_read_b64_tr_b16 v[34:35], v248 offset:11520
	s_waitcnt lgkmcnt(13)
	ds_read_b64_tr_b16 v[36:37], v248 offset:11552
	s_waitcnt lgkmcnt(13)
	ds_read_b64_tr_b16 v[38:39], v248 offset:11584
	s_waitcnt lgkmcnt(13)
	ds_read_b64_tr_b16 v[40:41], v248 offset:11616
	v_mfma_f32_16x16x16_bf16 v[2:5], v[42:43], v[244:245], v[2:5]
	v_mfma_f32_16x16x16_bf16 v[6:9], v[44:45], v[244:245], v[6:9]
	s_waitcnt lgkmcnt(13)
	v_mfma_f32_16x16x16_bf16 v[10:13], v[46:47], v[244:245], v[10:13]
	v_mfma_f32_16x16x16_bf16 v[14:17], v[48:49], v[244:245], v[14:17]
	v_mfma_f32_16x16x16_bf16 v[218:221], v[72:73], v[244:245], v[218:221]
	ds_read_b64_tr_b16 v[42:43], v248 offset:16128
	s_waitcnt lgkmcnt(13)
	ds_read_b64_tr_b16 v[44:45], v248 offset:16160
	s_waitcnt lgkmcnt(13)
	ds_read_b64_tr_b16 v[46:47], v248 offset:16192
	s_waitcnt lgkmcnt(13)
	ds_read_b64_tr_b16 v[48:49], v248 offset:16224
	v_mul_f32_dpp v2, v50, v2 row_newbcast:0 row_mask:0xf bank_mask:0xf
	v_mul_f32_dpp v3, v50, v3 row_newbcast:1 row_mask:0xf bank_mask:0xf
	v_mul_f32_dpp v4, v50, v4 row_newbcast:2 row_mask:0xf bank_mask:0xf
	v_mul_f32_dpp v5, v50, v5 row_newbcast:3 row_mask:0xf bank_mask:0xf
	v_mul_f32_dpp v6, v50, v6 row_newbcast:4 row_mask:0xf bank_mask:0xf
	v_mul_f32_dpp v7, v50, v7 row_newbcast:5 row_mask:0xf bank_mask:0xf
	v_mul_f32_dpp v8, v50, v8 row_newbcast:6 row_mask:0xf bank_mask:0xf
	v_mul_f32_dpp v9, v50, v9 row_newbcast:7 row_mask:0xf bank_mask:0xf
	v_mul_f32_dpp v10, v50, v10 row_newbcast:8 row_mask:0xf bank_mask:0xf
	v_mul_f32_dpp v11, v50, v11 row_newbcast:9 row_mask:0xf bank_mask:0xf
	v_mul_f32_dpp v12, v50, v12 row_newbcast:10 row_mask:0xf bank_mask:0xf
	v_mul_f32_dpp v13, v50, v13 row_newbcast:11 row_mask:0xf bank_mask:0xf
	v_mul_f32_dpp v14, v50, v14 row_newbcast:12 row_mask:0xf bank_mask:0xf
	v_mul_f32_dpp v15, v50, v15 row_newbcast:13 row_mask:0xf bank_mask:0xf
	v_mul_f32_dpp v16, v50, v16 row_newbcast:14 row_mask:0xf bank_mask:0xf
	v_mul_f32_dpp v17, v50, v17 row_newbcast:15 row_mask:0xf bank_mask:0xf
	v_add_f32_e32 v214, v214, v218
	v_add_f32_e32 v215, v215, v219
	v_add_f32_e32 v216, v216, v220
	v_add_f32_e32 v217, v217, v221
	s_waitcnt lgkmcnt(13)
	ds_write2st64_b32 v253, v214, v215 offset0:0 offset1:1
	s_waitcnt lgkmcnt(13)
	ds_write2st64_b32 v253, v216, v217 offset0:2 offset1:3
	v_cvt_pk_bf16_f32 v198, v2, v3
	v_cvt_pk_bf16_f32 v199, v4, v5
	v_cvt_pk_bf16_f32 v202, v10, v11
	v_cvt_pk_bf16_f32 v203, v12, v13
	v_cvt_pk_bf16_f32 v200, v6, v7
	v_cvt_pk_bf16_f32 v201, v8, v9
	v_cvt_pk_bf16_f32 v204, v14, v15
	v_cvt_pk_bf16_f32 v205, v16, v17
	v_add_u32_e32 v246, v115, v155
	v_bfe_u32 v248, v0, 4, 2
	v_mul_u32_u24_e32 v248, 0x240, v248
	v_bfe_u32 v249, v0, 2, 2
	v_mul_u32_u24_e32 v249, 0x90, v249
	v_and_b32_e32 v250, 3, v0
	v_add_u32_e32 v248, v248, v249
	v_lshl_add_u32 v248, v250, 3, v248
	v_bfe_u32 v249, v0, 6, 2
	v_add_u32_e32 v246, 0x10c00, v246
	v_add_u32_e32 v248, 0x10c00, v248
	v_and_b32_e32 v251, 12, v0
	v_lshl_add_u32 v251, v251, 4, v113
	v_lshl_add_u32 v251, v250, 2, v251
	v_add_u32_e32 v251, 0x10c00, v251
	v_lshl_add_u32 v250, v249, 5, v248
	v_add_u32_e32 v247, 0x1200, v246
	s_waitcnt lgkmcnt(13)
	ds_read2_b64 v[18:21], v246 offset1:4
	s_waitcnt lgkmcnt(13)
	ds_read2_b64 v[22:25], v246 offset0:8 offset1:12
	s_waitcnt lgkmcnt(13)
	ds_read_b64_tr_b16 v[66:67], v250 offset:18432
	v_mfma_f32_16x16x16_bf16 v[206:209], v[76:77], v[198:199], 0
	v_mfma_f32_16x16x16_bf16 v[210:213], v[80:81], v[202:203], 0
	v_mfma_f32_16x16x16_bf16 v[206:209], v[78:79], v[200:201], v[206:209]
	v_mfma_f32_16x16x16_bf16 v[210:213], v[82:83], v[204:205], v[210:213]
	v_mfma_f32_16x16x16_bf16 v[210:213], v[86:87], v[84:85], v[210:213]
	v_mfma_f32_16x16x16_bf16 v[214:217], v[26:27], v[198:199], 0
	s_waitcnt lgkmcnt(13)
	v_mfma_f32_16x16x16_bf16 v[218:221], v[30:31], v[202:203], 0
	v_mfma_f32_16x16x16_bf16 v[214:217], v[28:29], v[200:201], v[214:217]
	v_mfma_f32_16x16x16_bf16 v[218:221], v[32:33], v[204:205], v[218:221]
	s_nop 2
	v_add_f32_e32 v206, v206, v210
	v_add_f32_e32 v207, v207, v211
	v_add_f32_e32 v208, v208, v212
	v_add_f32_e32 v209, v209, v213
	v_cvt_pk_bf16_f32 v242, v206, v207
	v_cvt_pk_bf16_f32 v243, v208, v209
	s_nop 1
	v_mfma_f32_16x16x16_bf16 v[238:241], v[92:93], v[242:243], 0
	v_mfma_f32_16x16x16_bf16 v[214:217], v[88:89], v[84:85], v[214:217]
	s_waitcnt lgkmcnt(11)
	v_mfma_f32_16x16x16_bf16 v[2:5], v[34:35], v[84:85], v[2:5]
	v_mfma_f32_16x16x16_bf16 v[6:9], v[36:37], v[84:85], v[6:9]
	s_waitcnt lgkmcnt(9)
	v_mfma_f32_16x16x16_bf16 v[10:13], v[38:39], v[84:85], v[10:13]
	v_mfma_f32_16x16x16_bf16 v[14:17], v[40:41], v[84:85], v[14:17]
	s_nop 0
	v_cvt_pk_bf16_f32 v244, -v238, -v239
	v_cvt_pk_bf16_f32 v245, -v240, -v241
	s_waitcnt lgkmcnt(7)
	s_nop 0
	v_mfma_f32_16x16x16_bf16 v[2:5], v[42:43], v[244:245], v[2:5]
	v_mfma_f32_16x16x16_bf16 v[6:9], v[44:45], v[244:245], v[6:9]
	s_waitcnt lgkmcnt(5)
	v_mfma_f32_16x16x16_bf16 v[10:13], v[46:47], v[244:245], v[10:13]
	v_mfma_f32_16x16x16_bf16 v[14:17], v[48:49], v[244:245], v[14:17]
	v_mfma_f32_16x16x16_bf16 v[218:221], v[90:91], v[244:245], v[218:221]
	s_nop 2
	v_mul_f32_dpp v2, v51, v2 row_newbcast:0 row_mask:0xf bank_mask:0xf
	v_mul_f32_dpp v3, v51, v3 row_newbcast:1 row_mask:0xf bank_mask:0xf
	v_mul_f32_dpp v4, v51, v4 row_newbcast:2 row_mask:0xf bank_mask:0xf
	v_mul_f32_dpp v5, v51, v5 row_newbcast:3 row_mask:0xf bank_mask:0xf
	v_mul_f32_dpp v6, v51, v6 row_newbcast:4 row_mask:0xf bank_mask:0xf
	v_mul_f32_dpp v7, v51, v7 row_newbcast:5 row_mask:0xf bank_mask:0xf
	v_mul_f32_dpp v8, v51, v8 row_newbcast:6 row_mask:0xf bank_mask:0xf
	v_mul_f32_dpp v9, v51, v9 row_newbcast:7 row_mask:0xf bank_mask:0xf
	v_mul_f32_dpp v10, v51, v10 row_newbcast:8 row_mask:0xf bank_mask:0xf
	v_mul_f32_dpp v11, v51, v11 row_newbcast:9 row_mask:0xf bank_mask:0xf
	v_mul_f32_dpp v12, v51, v12 row_newbcast:10 row_mask:0xf bank_mask:0xf
	v_mul_f32_dpp v13, v51, v13 row_newbcast:11 row_mask:0xf bank_mask:0xf
	v_mul_f32_dpp v14, v51, v14 row_newbcast:12 row_mask:0xf bank_mask:0xf
	v_mul_f32_dpp v15, v51, v15 row_newbcast:13 row_mask:0xf bank_mask:0xf
	v_mul_f32_dpp v16, v51, v16 row_newbcast:14 row_mask:0xf bank_mask:0xf
	v_mul_f32_dpp v17, v51, v17 row_newbcast:15 row_mask:0xf bank_mask:0xf
	v_add_f32_e32 v214, v214, v218
	v_add_f32_e32 v215, v215, v219
	v_add_f32_e32 v216, v216, v220
	v_add_f32_e32 v217, v217, v221
	ds_write2st64_b32 v253, v214, v215 offset0:16 offset1:17
	ds_write2st64_b32 v253, v216, v217 offset0:18 offset1:19
	s_branch .Lscan_join2

.LBB0_1160:
.Lscan_join2:
	s_waitcnt lgkmcnt(0)
	s_barrier
	v_readlane_b32 s0, v255, 17
	v_readlane_b32 s1, v255, 18
	s_and_b64 vcc, exec, s[0:1]
	s_mov_b64 s[30:31], -1
	s_cbranch_vccnz .LBB0_1162
	v_readlane_b32 s0, v255, 13
	s_nop 1
	s_nop 0
	s_mul_i32 s1, s0, 0x1e00
	s_lshl_b32 s0, s0, 13
	v_add_u32_e32 v252, s1, v166
	v_add_u32_e32 v253, s0, v165
	ds_read2_b64 v[68:71], v252 offset1:80
	v_cvt_pk_bf16_f32 v198, v2, v3
	v_cvt_pk_bf16_f32 v199, v4, v5
	v_cvt_pk_bf16_f32 v202, v10, v11
	v_cvt_pk_bf16_f32 v203, v12, v13
	v_cvt_pk_bf16_f32 v200, v6, v7
	v_cvt_pk_bf16_f32 v201, v8, v9
	v_cvt_pk_bf16_f32 v204, v14, v15
	v_cvt_pk_bf16_f32 v205, v16, v17
	ds_read2_b64 v[26:29], v247 offset1:4
	ds_read2_b64 v[30:33], v247 offset0:8 offset1:12
	ds_read2_b64 v[72:75], v252 offset0:160 offset1:240
	v_mfma_f32_16x16x16_bf16 v[206:209], v[18:19], v[198:199], 0
	v_mfma_f32_16x16x16_bf16 v[210:213], v[22:23], v[202:203], 0
	ds_read_b64_tr_b16 v[34:35], v248 offset:9216
	ds_read_b64_tr_b16 v[36:37], v248 offset:9248
	ds_read_b64_tr_b16 v[38:39], v248 offset:9280
	ds_read_b64_tr_b16 v[40:41], v248 offset:9312
	v_mfma_f32_16x16x16_bf16 v[206:209], v[20:21], v[200:201], v[206:209]
	v_mfma_f32_16x16x16_bf16 v[210:213], v[24:25], v[204:205], v[210:213]
	ds_read_b64_tr_b16 v[42:43], v248 offset:13824
	ds_read_b64_tr_b16 v[44:45], v248 offset:13856
	ds_read_b64_tr_b16 v[46:47], v248 offset:13888
	ds_read_b64_tr_b16 v[48:49], v248 offset:13920
	s_waitcnt lgkmcnt(11)
	v_mfma_f32_16x16x16_bf16 v[210:213], v[68:69], v[66:67], v[210:213]
	s_waitcnt lgkmcnt(10)
	v_mfma_f32_16x16x16_bf16 v[214:217], v[26:27], v[198:199], 0
	s_waitcnt lgkmcnt(9)
	v_mfma_f32_16x16x16_bf16 v[218:221], v[30:31], v[202:203], 0
	v_mfma_f32_16x16x16_bf16 v[214:217], v[28:29], v[200:201], v[214:217]
	v_mfma_f32_16x16x16_bf16 v[218:221], v[32:33], v[204:205], v[218:221]
	ds_read_b32 v50, v251 offset:33792
	ds_read_b32 v51, v251 offset:34048
	v_add_u32_e32 v246, 0x900, v246
	ds_read2_b64 v[76:79], v246 offset1:4
	ds_read2_b64 v[80:83], v246 offset0:8 offset1:12
	v_add_f32_e32 v206, v206, v210
	v_add_f32_e32 v207, v207, v211
	v_add_f32_e32 v208, v208, v212
	v_add_f32_e32 v209, v209, v213
	v_cvt_pk_bf16_f32 v242, v206, v207
	v_cvt_pk_bf16_f32 v243, v208, v209
	ds_read_b64_tr_b16 v[84:85], v250 offset:20736
	v_add_u32_e32 v252, 0xf00, v252
	s_waitcnt lgkmcnt(13)
	ds_read2_b64 v[86:89], v252 offset1:80
	v_mfma_f32_16x16x16_bf16 v[238:241], v[74:75], v[242:243], 0
	v_mfma_f32_16x16x16_bf16 v[214:217], v[70:71], v[66:67], v[214:217]
	s_waitcnt lgkmcnt(12)
	v_mfma_f32_16x16x16_bf16 v[2:5], v[34:35], v[66:67], v[2:5]
	v_mfma_f32_16x16x16_bf16 v[6:9], v[36:37], v[66:67], v[6:9]
	s_waitcnt lgkmcnt(10)
	v_mfma_f32_16x16x16_bf16 v[10:13], v[38:39], v[66:67], v[10:13]
	v_mfma_f32_16x16x16_bf16 v[14:17], v[40:41], v[66:67], v[14:17]
	ds_read2_b64 v[90:93], v252 offset0:160 offset1:240
	v_add_u32_e32 v247, 0x900, v247
	ds_read2_b64 v[26:29], v247 offset1:4
	ds_read2_b64 v[30:33], v247 offset0:8 offset1:12
	v_cvt_pk_bf16_f32 v244, -v238, -v239
	v_cvt_pk_bf16_f32 v245, -v240, -v241
	ds_read_b64_tr_b16 v[34:35], v248 offset:11520
	s_waitcnt lgkmcnt(13)
	ds_read_b64_tr_b16 v[36:37], v248 offset:11552
	s_waitcnt lgkmcnt(13)
	ds_read_b64_tr_b16 v[38:39], v248 offset:11584
	s_waitcnt lgkmcnt(13)
	ds_read_b64_tr_b16 v[40:41], v248 offset:11616
	v_mfma_f32_16x16x16_bf16 v[2:5], v[42:43], v[244:245], v[2:5]
	v_mfma_f32_16x16x16_bf16 v[6:9], v[44:45], v[244:245], v[6:9]
	s_waitcnt lgkmcnt(13)
	v_mfma_f32_16x16x16_bf16 v[10:13], v[46:47], v[244:245], v[10:13]
	v_mfma_f32_16x16x16_bf16 v[14:17], v[48:49], v[244:245], v[14:17]
	v_mfma_f32_16x16x16_bf16 v[218:221], v[72:73], v[244:245], v[218:221]
	ds_read_b64_tr_b16 v[42:43], v248 offset:16128
	s_waitcnt lgkmcnt(13)
	ds_read_b64_tr_b16 v[44:45], v248 offset:16160
	s_waitcnt lgkmcnt(13)
	ds_read_b64_tr_b16 v[46:47], v248 offset:16192
	s_waitcnt lgkmcnt(13)
	ds_read_b64_tr_b16 v[48:49], v248 offset:16224
	v_mul_f32_dpp v2, v50, v2 row_newbcast:0 row_mask:0xf bank_mask:0xf
	v_mul_f32_dpp v3, v50, v3 row_newbcast:1 row_mask:0xf bank_mask:0xf
	v_mul_f32_dpp v4, v50, v4 row_newbcast:2 row_mask:0xf bank_mask:0xf
	v_mul_f32_dpp v5, v50, v5 row_newbcast:3 row_mask:0xf bank_mask:0xf
	v_mul_f32_dpp v6, v50, v6 row_newbcast:4 row_mask:0xf bank_mask:0xf
	v_mul_f32_dpp v7, v50, v7 row_newbcast:5 row_mask:0xf bank_mask:0xf
	v_mul_f32_dpp v8, v50, v8 row_newbcast:6 row_mask:0xf bank_mask:0xf
	v_mul_f32_dpp v9, v50, v9 row_newbcast:7 row_mask:0xf bank_mask:0xf
	v_mul_f32_dpp v10, v50, v10 row_newbcast:8 row_mask:0xf bank_mask:0xf
	v_mul_f32_dpp v11, v50, v11 row_newbcast:9 row_mask:0xf bank_mask:0xf
	v_mul_f32_dpp v12, v50, v12 row_newbcast:10 row_mask:0xf bank_mask:0xf
	v_mul_f32_dpp v13, v50, v13 row_newbcast:11 row_mask:0xf bank_mask:0xf
	v_mul_f32_dpp v14, v50, v14 row_newbcast:12 row_mask:0xf bank_mask:0xf
	v_mul_f32_dpp v15, v50, v15 row_newbcast:13 row_mask:0xf bank_mask:0xf
	v_mul_f32_dpp v16, v50, v16 row_newbcast:14 row_mask:0xf bank_mask:0xf
	v_mul_f32_dpp v17, v50, v17 row_newbcast:15 row_mask:0xf bank_mask:0xf
	v_add_f32_e32 v214, v214, v218
	v_add_f32_e32 v215, v215, v219
	v_add_f32_e32 v216, v216, v220
	v_add_f32_e32 v217, v217, v221
	s_waitcnt lgkmcnt(13)
	ds_write2st64_b32 v253, v214, v215 offset0:0 offset1:1
	s_waitcnt lgkmcnt(13)
	ds_write2st64_b32 v253, v216, v217 offset0:2 offset1:3
	v_cvt_pk_bf16_f32 v198, v2, v3
	v_cvt_pk_bf16_f32 v199, v4, v5
	v_cvt_pk_bf16_f32 v202, v10, v11
	v_cvt_pk_bf16_f32 v203, v12, v13
	v_cvt_pk_bf16_f32 v200, v6, v7
	v_cvt_pk_bf16_f32 v201, v8, v9
	v_cvt_pk_bf16_f32 v204, v14, v15
	v_cvt_pk_bf16_f32 v205, v16, v17
	v_add_u32_e32 v246, v115, v155
	v_bfe_u32 v248, v0, 4, 2
	v_mul_u32_u24_e32 v248, 0x240, v248
	v_bfe_u32 v249, v0, 2, 2
	v_mul_u32_u24_e32 v249, 0x90, v249
	v_and_b32_e32 v250, 3, v0
	v_add_u32_e32 v248, v248, v249
	v_lshl_add_u32 v248, v250, 3, v248
	v_bfe_u32 v249, v0, 6, 2
	v_and_b32_e32 v251, 12, v0
	v_lshl_add_u32 v251, v251, 4, v113
	v_lshl_add_u32 v251, v250, 2, v251
	v_lshl_add_u32 v250, v249, 5, v248
	v_add_u32_e32 v247, 0x1200, v246
	s_waitcnt lgkmcnt(13)
	ds_read2_b64 v[18:21], v246 offset1:4
	s_waitcnt lgkmcnt(13)
	ds_read2_b64 v[22:25], v246 offset0:8 offset1:12
	s_waitcnt lgkmcnt(13)
	ds_read_b64_tr_b16 v[66:67], v250 offset:18432
	v_mfma_f32_16x16x16_bf16 v[206:209], v[76:77], v[198:199], 0
	v_mfma_f32_16x16x16_bf16 v[210:213], v[80:81], v[202:203], 0
	v_mfma_f32_16x16x16_bf16 v[206:209], v[78:79], v[200:201], v[206:209]
	v_mfma_f32_16x16x16_bf16 v[210:213], v[82:83], v[204:205], v[210:213]
	v_mfma_f32_16x16x16_bf16 v[210:213], v[86:87], v[84:85], v[210:213]
	v_mfma_f32_16x16x16_bf16 v[214:217], v[26:27], v[198:199], 0
	s_waitcnt lgkmcnt(13)
	v_mfma_f32_16x16x16_bf16 v[218:221], v[30:31], v[202:203], 0
	v_mfma_f32_16x16x16_bf16 v[214:217], v[28:29], v[200:201], v[214:217]
	v_mfma_f32_16x16x16_bf16 v[218:221], v[32:33], v[204:205], v[218:221]
	s_nop 2
	v_add_f32_e32 v206, v206, v210
	v_add_f32_e32 v207, v207, v211
	v_add_f32_e32 v208, v208, v212
	v_add_f32_e32 v209, v209, v213
	v_cvt_pk_bf16_f32 v242, v206, v207
	v_cvt_pk_bf16_f32 v243, v208, v209
	s_nop 1
	v_mfma_f32_16x16x16_bf16 v[238:241], v[92:93], v[242:243], 0
	v_mfma_f32_16x16x16_bf16 v[214:217], v[88:89], v[84:85], v[214:217]
	s_waitcnt lgkmcnt(11)
	v_mfma_f32_16x16x16_bf16 v[2:5], v[34:35], v[84:85], v[2:5]
	v_mfma_f32_16x16x16_bf16 v[6:9], v[36:37], v[84:85], v[6:9]
	s_waitcnt lgkmcnt(9)
	v_mfma_f32_16x16x16_bf16 v[10:13], v[38:39], v[84:85], v[10:13]
	v_mfma_f32_16x16x16_bf16 v[14:17], v[40:41], v[84:85], v[14:17]
	s_nop 0
	v_cvt_pk_bf16_f32 v244, -v238, -v239
	v_cvt_pk_bf16_f32 v245, -v240, -v241
	s_waitcnt lgkmcnt(7)
	s_nop 0
	v_mfma_f32_16x16x16_bf16 v[2:5], v[42:43], v[244:245], v[2:5]
	v_mfma_f32_16x16x16_bf16 v[6:9], v[44:45], v[244:245], v[6:9]
	s_waitcnt lgkmcnt(5)
	v_mfma_f32_16x16x16_bf16 v[10:13], v[46:47], v[244:245], v[10:13]
	v_mfma_f32_16x16x16_bf16 v[14:17], v[48:49], v[244:245], v[14:17]
	v_mfma_f32_16x16x16_bf16 v[218:221], v[90:91], v[244:245], v[218:221]
	s_nop 2
	v_mul_f32_dpp v2, v51, v2 row_newbcast:0 row_mask:0xf bank_mask:0xf
	v_mul_f32_dpp v3, v51, v3 row_newbcast:1 row_mask:0xf bank_mask:0xf
	v_mul_f32_dpp v4, v51, v4 row_newbcast:2 row_mask:0xf bank_mask:0xf
	v_mul_f32_dpp v5, v51, v5 row_newbcast:3 row_mask:0xf bank_mask:0xf
	v_mul_f32_dpp v6, v51, v6 row_newbcast:4 row_mask:0xf bank_mask:0xf
	v_mul_f32_dpp v7, v51, v7 row_newbcast:5 row_mask:0xf bank_mask:0xf
	v_mul_f32_dpp v8, v51, v8 row_newbcast:6 row_mask:0xf bank_mask:0xf
	v_mul_f32_dpp v9, v51, v9 row_newbcast:7 row_mask:0xf bank_mask:0xf
	v_mul_f32_dpp v10, v51, v10 row_newbcast:8 row_mask:0xf bank_mask:0xf
	v_mul_f32_dpp v11, v51, v11 row_newbcast:9 row_mask:0xf bank_mask:0xf
	v_mul_f32_dpp v12, v51, v12 row_newbcast:10 row_mask:0xf bank_mask:0xf
	v_mul_f32_dpp v13, v51, v13 row_newbcast:11 row_mask:0xf bank_mask:0xf
	v_mul_f32_dpp v14, v51, v14 row_newbcast:12 row_mask:0xf bank_mask:0xf
	v_mul_f32_dpp v15, v51, v15 row_newbcast:13 row_mask:0xf bank_mask:0xf
	v_mul_f32_dpp v16, v51, v16 row_newbcast:14 row_mask:0xf bank_mask:0xf
	v_mul_f32_dpp v17, v51, v17 row_newbcast:15 row_mask:0xf bank_mask:0xf
	v_add_f32_e32 v214, v214, v218
	v_add_f32_e32 v215, v215, v219
	v_add_f32_e32 v216, v216, v220
	v_add_f32_e32 v217, v217, v221
	ds_write2st64_b32 v253, v214, v215 offset0:16 offset1:17
	ds_write2st64_b32 v253, v216, v217 offset0:18 offset1:19
	s_branch .Lscan_join3

.LBB0_1331:
	s_ashr_i32 s17, s16, 31
	s_lshl_b64 s[0:1], s[16:17], 20
	s_add_u32 s17, s18, s0
	s_addc_u32 s21, s19, s1
	s_ashr_i32 s15, s14, 31
	s_lshl_b64 s[0:1], s[14:15], 18
	s_add_u32 s24, s17, s0
	s_addc_u32 s25, s21, s1
	s_and_b64 s[0:1], s[6:7], exec
	s_cselect_b32 s15, s25, s29
	s_cselect_b32 s17, s24, s28
	s_add_u32 s6, s30, 0x20080
	s_addc_u32 s7, s31, 0
	s_add_u32 s21, s28, 0x100
	s_addc_u32 s82, s29, 0
	s_mov_b32 s86, -2
	v_add_u32_e32 v142, 0x10000, v237
	ds_read_b128 v[130:133], v142
	ds_read_b128 v[134:137], v142 offset:1024
	ds_read_b128 v[138:141], v142 offset:2048
	ds_read_b128 v[142:145], v142 offset:3072
.LBB0_1332:
	s_add_u32 s0, s6, 0xfffe0080
	s_addc_u32 s1, s7, -1
	s_add_i32 s33, 0, 0x10000
	s_cmp_eq_u32 s86, 4
	s_cselect_b32 s31, s23, s1
	s_cselect_b32 s30, s22, s0
	s_cselect_b32 s29, s15, s82
	s_cselect_b32 s28, s17, s21
	v_lshl_add_u64 v[178:179], s[6:7], 0, v[214:215]
	s_add_i32 m0, s70, 0xc000
	ds_read_b128 v[146:149], v240
	ds_read_b128 v[150:153], v240 offset:1024
	ds_read_b128 v[154:157], v240 offset:2048
	ds_read_b128 v[158:161], v240 offset:3072
	ds_read_b128 v[162:165], v240 offset:4096
	ds_read_b128 v[166:169], v240 offset:5120
	ds_read_b128 v[170:173], v240 offset:6144
	ds_read_b128 v[174:177], v240 offset:7168
	global_load_lds_dwordx4 v[178:179], off
	v_lshl_add_u64 v[178:179], s[6:7], 0, v[216:217]
	s_add_i32 m0, s70, 0xe000
	s_nop 0
	global_load_lds_dwordx4 v[178:179], off
	s_waitcnt lgkmcnt(8)
	s_barrier
	s_waitcnt lgkmcnt(0)
	s_waitcnt lgkmcnt(0)
	v_mfma_f32_16x16x32_bf16 v[62:65], v[130:133], v[146:149], v[62:65]
	v_mfma_f32_16x16x32_bf16 v[58:61], v[138:141], v[146:149], v[58:61]
	v_mfma_f32_16x16x32_bf16 v[54:57], v[130:133], v[154:157], v[54:57]
	v_mfma_f32_16x16x32_bf16 v[50:53], v[138:141], v[154:157], v[50:53]
	v_mfma_f32_16x16x32_bf16 v[46:49], v[130:133], v[162:165], v[46:49]
	v_mfma_f32_16x16x32_bf16 v[42:45], v[138:141], v[162:165], v[42:45]
	v_mfma_f32_16x16x32_bf16 v[38:41], v[130:133], v[170:173], v[38:41]
	v_mfma_f32_16x16x32_bf16 v[34:37], v[138:141], v[170:173], v[34:37]
	v_mfma_f32_16x16x32_bf16 v[62:65], v[134:137], v[150:153], v[62:65]
	v_mfma_f32_16x16x32_bf16 v[58:61], v[142:145], v[150:153], v[58:61]
	v_mfma_f32_16x16x32_bf16 v[54:57], v[134:137], v[158:161], v[54:57]
	v_mfma_f32_16x16x32_bf16 v[50:53], v[142:145], v[158:161], v[50:53]
	v_mfma_f32_16x16x32_bf16 v[46:49], v[134:137], v[166:169], v[46:49]
	v_mfma_f32_16x16x32_bf16 v[42:45], v[142:145], v[166:169], v[42:45]
	v_mfma_f32_16x16x32_bf16 v[38:41], v[134:137], v[174:177], v[38:41]
	v_mfma_f32_16x16x32_bf16 v[34:37], v[142:145], v[174:177], v[34:37]
	s_barrier
	s_add_i32 s36, 0, 0x14000
	s_add_i32 s0, s33, s66
	v_add_u32_e32 v190, s36, v237
	v_lshl_add_u64 v[218:219], s[28:29], 0, v[202:203]
	s_mov_b32 m0, s0
	ds_read_b128 v[178:181], v190
	ds_read_b128 v[182:185], v190 offset:1024
	ds_read_b128 v[186:189], v190 offset:2048
	ds_read_b128 v[190:193], v190 offset:3072
	global_load_lds_dwordx4 v[218:219], off
	v_lshl_add_u64 v[220:221], s[28:29], 0, v[198:199]
	s_add_i32 m0, s0, 0x2000
	s_nop 0
	global_load_lds_dwordx4 v[220:221], off
	s_barrier
	s_waitcnt lgkmcnt(0)
	s_waitcnt lgkmcnt(0)
	v_mfma_f32_16x16x32_bf16 v[30:33], v[178:181], v[146:149], v[30:33]
	v_mfma_f32_16x16x32_bf16 v[26:29], v[186:189], v[146:149], v[26:29]
	v_mfma_f32_16x16x32_bf16 v[22:25], v[178:181], v[154:157], v[22:25]
	v_mfma_f32_16x16x32_bf16 v[18:21], v[186:189], v[154:157], v[18:21]
	v_mfma_f32_16x16x32_bf16 v[14:17], v[178:181], v[162:165], v[14:17]
	v_mfma_f32_16x16x32_bf16 v[10:13], v[186:189], v[162:165], v[10:13]
	v_mfma_f32_16x16x32_bf16 v[6:9], v[178:181], v[170:173], v[6:9]
	v_mfma_f32_16x16x32_bf16 v[2:5], v[186:189], v[170:173], v[2:5]
	v_mfma_f32_16x16x32_bf16 v[30:33], v[182:185], v[150:153], v[30:33]
	v_mfma_f32_16x16x32_bf16 v[26:29], v[190:193], v[150:153], v[26:29]
	v_mfma_f32_16x16x32_bf16 v[22:25], v[182:185], v[158:161], v[22:25]
	v_mfma_f32_16x16x32_bf16 v[18:21], v[190:193], v[158:161], v[18:21]
	v_mfma_f32_16x16x32_bf16 v[14:17], v[182:185], v[166:169], v[14:17]
	v_mfma_f32_16x16x32_bf16 v[10:13], v[190:193], v[166:169], v[10:13]
	v_mfma_f32_16x16x32_bf16 v[6:9], v[182:185], v[174:177], v[6:9]
	v_mfma_f32_16x16x32_bf16 v[2:5], v[190:193], v[174:177], v[2:5]
	s_mov_b32 m0, s70
	v_lshl_add_u64 v[224:225], s[30:31], 0, v[204:205]
	s_barrier
	ds_read_b128 v[146:149], v240 offset:16384
	ds_read_b128 v[150:153], v240 offset:17408
	ds_read_b128 v[154:157], v240 offset:18432
	ds_read_b128 v[158:161], v240 offset:19456
	ds_read_b128 v[162:165], v240 offset:20480
	ds_read_b128 v[166:169], v240 offset:21504
	ds_read_b128 v[170:173], v240 offset:22528
	ds_read_b128 v[174:177], v240 offset:23552
	global_load_lds_dwordx4 v[224:225], off
	v_lshl_add_u64 v[230:231], s[30:31], 0, v[200:201]
	s_mov_b32 m0, s71
	s_nop 0
	global_load_lds_dwordx4 v[230:231], off
	s_waitcnt vmcnt(10)
	s_barrier
	s_waitcnt lgkmcnt(0)
	s_waitcnt lgkmcnt(0)
	v_mfma_f32_16x16x32_bf16 v[66:69], v[130:133], v[146:149], v[66:69]
	v_mfma_f32_16x16x32_bf16 v[70:73], v[138:141], v[146:149], v[70:73]
	v_mfma_f32_16x16x32_bf16 v[74:77], v[130:133], v[154:157], v[74:77]
	v_mfma_f32_16x16x32_bf16 v[78:81], v[138:141], v[154:157], v[78:81]
	v_mfma_f32_16x16x32_bf16 v[82:85], v[130:133], v[162:165], v[82:85]
	v_mfma_f32_16x16x32_bf16 v[86:89], v[138:141], v[162:165], v[86:89]
	v_mfma_f32_16x16x32_bf16 v[90:93], v[130:133], v[170:173], v[90:93]
	v_mfma_f32_16x16x32_bf16 v[94:97], v[138:141], v[170:173], v[94:97]
	v_mfma_f32_16x16x32_bf16 v[66:69], v[134:137], v[150:153], v[66:69]
	v_mfma_f32_16x16x32_bf16 v[70:73], v[142:145], v[150:153], v[70:73]
	v_mfma_f32_16x16x32_bf16 v[74:77], v[134:137], v[158:161], v[74:77]
	v_mfma_f32_16x16x32_bf16 v[78:81], v[142:145], v[158:161], v[78:81]
	v_mfma_f32_16x16x32_bf16 v[82:85], v[134:137], v[166:169], v[82:85]
	v_mfma_f32_16x16x32_bf16 v[86:89], v[142:145], v[166:169], v[86:89]
	v_mfma_f32_16x16x32_bf16 v[90:93], v[134:137], v[174:177], v[90:93]
	v_mfma_f32_16x16x32_bf16 v[94:97], v[142:145], v[174:177], v[94:97]
	s_barrier
	s_add_u32 s0, s28, 0x20000
	s_addc_u32 s1, s29, 0
	s_add_i32 s33, s36, s66
	v_lshl_add_u64 v[130:131], s[0:1], 0, v[202:203]
	s_mov_b32 m0, s33
	s_nop 0
	global_load_lds_dwordx4 v[130:131], off
	v_lshl_add_u64 v[130:131], s[0:1], 0, v[198:199]
	s_add_i32 m0, s33, 0x2000
	s_nop 0
	global_load_lds_dwordx4 v[130:131], off
	v_add_u32_e32 v142, 0x18000, v237
	ds_read_b128 v[130:133], v142
	ds_read_b128 v[134:137], v142 offset:1024
	ds_read_b128 v[138:141], v142 offset:2048
	ds_read_b128 v[142:145], v142 offset:3072
	s_waitcnt vmcnt(6)
	s_barrier
	v_mfma_f32_16x16x32_bf16 v[98:101], v[178:181], v[146:149], v[98:101]
	v_mfma_f32_16x16x32_bf16 v[102:105], v[186:189], v[146:149], v[102:105]
	v_mfma_f32_16x16x32_bf16 v[106:109], v[178:181], v[154:157], v[106:109]
	v_mfma_f32_16x16x32_bf16 v[110:113], v[186:189], v[154:157], v[110:113]
	v_mfma_f32_16x16x32_bf16 v[114:117], v[178:181], v[162:165], v[114:117]
	v_mfma_f32_16x16x32_bf16 v[118:121], v[186:189], v[162:165], v[118:121]
	v_mfma_f32_16x16x32_bf16 v[122:125], v[178:181], v[170:173], v[122:125]
	v_mfma_f32_16x16x32_bf16 v[126:129], v[186:189], v[170:173], v[126:129]
	v_mfma_f32_16x16x32_bf16 v[98:101], v[182:185], v[150:153], v[98:101]
	v_mfma_f32_16x16x32_bf16 v[102:105], v[190:193], v[150:153], v[102:105]
	v_mfma_f32_16x16x32_bf16 v[106:109], v[182:185], v[158:161], v[106:109]
	v_mfma_f32_16x16x32_bf16 v[110:113], v[190:193], v[158:161], v[110:113]
	v_mfma_f32_16x16x32_bf16 v[114:117], v[182:185], v[166:169], v[114:117]
	v_mfma_f32_16x16x32_bf16 v[118:121], v[190:193], v[166:169], v[118:121]
	v_mfma_f32_16x16x32_bf16 v[122:125], v[182:185], v[174:177], v[122:125]
	v_mfma_f32_16x16x32_bf16 v[126:129], v[190:193], v[174:177], v[126:129]
	s_add_i32 s33, 0, 0x18000
	s_barrier
	s_add_u32 s0, s30, 0x20000
	s_addc_u32 s1, s31, 0
	s_mov_b32 m0, s72
	v_lshl_add_u64 v[178:179], s[0:1], 0, v[204:205]
	ds_read_b128 v[146:149], v240 offset:32768
	ds_read_b128 v[150:153], v240 offset:33792
	ds_read_b128 v[154:157], v240 offset:34816
	ds_read_b128 v[158:161], v240 offset:35840
	ds_read_b128 v[162:165], v240 offset:36864
	ds_read_b128 v[166:169], v240 offset:37888
	ds_read_b128 v[170:173], v240 offset:38912
	ds_read_b128 v[174:177], v240 offset:39936
	global_load_lds_dwordx4 v[178:179], off
	v_lshl_add_u64 v[178:179], s[0:1], 0, v[200:201]
	s_mov_b32 m0, s73
	s_nop 0
	global_load_lds_dwordx4 v[178:179], off
	s_waitcnt lgkmcnt(8)
	s_barrier
	s_waitcnt lgkmcnt(0)
	s_waitcnt lgkmcnt(0)
	v_mfma_f32_16x16x32_bf16 v[62:65], v[130:133], v[146:149], v[62:65]
	v_mfma_f32_16x16x32_bf16 v[58:61], v[138:141], v[146:149], v[58:61]
	v_mfma_f32_16x16x32_bf16 v[54:57], v[130:133], v[154:157], v[54:57]
	v_mfma_f32_16x16x32_bf16 v[50:53], v[138:141], v[154:157], v[50:53]
	v_mfma_f32_16x16x32_bf16 v[46:49], v[130:133], v[162:165], v[46:49]
	v_mfma_f32_16x16x32_bf16 v[42:45], v[138:141], v[162:165], v[42:45]
	v_mfma_f32_16x16x32_bf16 v[38:41], v[130:133], v[170:173], v[38:41]
	v_mfma_f32_16x16x32_bf16 v[34:37], v[138:141], v[170:173], v[34:37]
	v_mfma_f32_16x16x32_bf16 v[62:65], v[134:137], v[150:153], v[62:65]
	v_mfma_f32_16x16x32_bf16 v[58:61], v[142:145], v[150:153], v[58:61]
	v_mfma_f32_16x16x32_bf16 v[54:57], v[134:137], v[158:161], v[54:57]
	v_mfma_f32_16x16x32_bf16 v[50:53], v[142:145], v[158:161], v[50:53]
	v_mfma_f32_16x16x32_bf16 v[46:49], v[134:137], v[166:169], v[46:49]
	v_mfma_f32_16x16x32_bf16 v[42:45], v[142:145], v[166:169], v[42:45]
	v_mfma_f32_16x16x32_bf16 v[38:41], v[134:137], v[174:177], v[38:41]
	v_mfma_f32_16x16x32_bf16 v[34:37], v[142:145], v[174:177], v[34:37]
	s_barrier
	s_add_i32 s30, 0, 0x1c000
	s_add_i32 s0, s33, s66
	v_add_u32_e32 v190, s30, v237
	v_lshl_add_u64 v[218:219], v[218:219], 0, s[54:55]
	s_mov_b32 m0, s0
	ds_read_b128 v[178:181], v190
	ds_read_b128 v[182:185], v190 offset:1024
	ds_read_b128 v[186:189], v190 offset:2048
	ds_read_b128 v[190:193], v190 offset:3072
	global_load_lds_dwordx4 v[218:219], off
	v_lshl_add_u64 v[218:219], v[220:221], 0, s[54:55]
	s_add_i32 m0, s0, 0x2000
	s_nop 0
	global_load_lds_dwordx4 v[218:219], off
	s_barrier
	s_waitcnt lgkmcnt(0)
	s_waitcnt lgkmcnt(0)
	v_mfma_f32_16x16x32_bf16 v[30:33], v[178:181], v[146:149], v[30:33]
	v_mfma_f32_16x16x32_bf16 v[26:29], v[186:189], v[146:149], v[26:29]
	v_mfma_f32_16x16x32_bf16 v[22:25], v[178:181], v[154:157], v[22:25]
	v_mfma_f32_16x16x32_bf16 v[18:21], v[186:189], v[154:157], v[18:21]
	v_mfma_f32_16x16x32_bf16 v[14:17], v[178:181], v[162:165], v[14:17]
	v_mfma_f32_16x16x32_bf16 v[10:13], v[186:189], v[162:165], v[10:13]
	v_mfma_f32_16x16x32_bf16 v[6:9], v[178:181], v[170:173], v[6:9]
	v_mfma_f32_16x16x32_bf16 v[2:5], v[186:189], v[170:173], v[2:5]
	v_mfma_f32_16x16x32_bf16 v[30:33], v[182:185], v[150:153], v[30:33]
	v_mfma_f32_16x16x32_bf16 v[26:29], v[190:193], v[150:153], v[26:29]
	v_mfma_f32_16x16x32_bf16 v[22:25], v[182:185], v[158:161], v[22:25]
	v_mfma_f32_16x16x32_bf16 v[18:21], v[190:193], v[158:161], v[18:21]
	v_mfma_f32_16x16x32_bf16 v[14:17], v[182:185], v[166:169], v[14:17]
	v_mfma_f32_16x16x32_bf16 v[10:13], v[190:193], v[166:169], v[10:13]
	v_mfma_f32_16x16x32_bf16 v[6:9], v[182:185], v[174:177], v[6:9]
	v_mfma_f32_16x16x32_bf16 v[2:5], v[190:193], v[174:177], v[2:5]
	s_mov_b32 m0, s76
	v_lshl_add_u64 v[218:219], v[224:225], 0, s[54:55]
	s_barrier
	ds_read_b128 v[146:149], v240 offset:49152
	ds_read_b128 v[150:153], v240 offset:50176
	ds_read_b128 v[154:157], v240 offset:51200
	ds_read_b128 v[158:161], v240 offset:52224
	ds_read_b128 v[162:165], v240 offset:53248
	ds_read_b128 v[166:169], v240 offset:54272
	ds_read_b128 v[170:173], v240 offset:55296
	ds_read_b128 v[174:177], v240 offset:56320
	global_load_lds_dwordx4 v[218:219], off
	v_lshl_add_u64 v[218:219], v[230:231], 0, s[54:55]
	s_mov_b32 m0, s77
	s_nop 0
	global_load_lds_dwordx4 v[218:219], off
	s_waitcnt vmcnt(10)
	s_barrier
	s_waitcnt lgkmcnt(0)
	s_waitcnt lgkmcnt(0)
	v_mfma_f32_16x16x32_bf16 v[66:69], v[130:133], v[146:149], v[66:69]
	v_mfma_f32_16x16x32_bf16 v[70:73], v[138:141], v[146:149], v[70:73]
	v_mfma_f32_16x16x32_bf16 v[74:77], v[130:133], v[154:157], v[74:77]
	v_mfma_f32_16x16x32_bf16 v[78:81], v[138:141], v[154:157], v[78:81]
	v_mfma_f32_16x16x32_bf16 v[82:85], v[130:133], v[162:165], v[82:85]
	v_mfma_f32_16x16x32_bf16 v[86:89], v[138:141], v[162:165], v[86:89]
	v_mfma_f32_16x16x32_bf16 v[90:93], v[130:133], v[170:173], v[90:93]
	v_mfma_f32_16x16x32_bf16 v[94:97], v[138:141], v[170:173], v[94:97]
	v_mfma_f32_16x16x32_bf16 v[66:69], v[134:137], v[150:153], v[66:69]
	v_mfma_f32_16x16x32_bf16 v[70:73], v[142:145], v[150:153], v[70:73]
	v_mfma_f32_16x16x32_bf16 v[74:77], v[134:137], v[158:161], v[74:77]
	v_mfma_f32_16x16x32_bf16 v[78:81], v[142:145], v[158:161], v[78:81]
	v_mfma_f32_16x16x32_bf16 v[82:85], v[134:137], v[166:169], v[82:85]
	v_mfma_f32_16x16x32_bf16 v[86:89], v[142:145], v[166:169], v[86:89]
	v_mfma_f32_16x16x32_bf16 v[90:93], v[134:137], v[174:177], v[90:93]
	v_mfma_f32_16x16x32_bf16 v[94:97], v[142:145], v[174:177], v[94:97]
	s_barrier
	s_add_u32 s0, s28, 0x20080
	s_addc_u32 s1, s29, 0
	s_add_i32 s28, s30, s66
	v_lshl_add_u64 v[130:131], s[0:1], 0, v[202:203]
	s_mov_b32 m0, s28
	s_nop 0
	global_load_lds_dwordx4 v[130:131], off
	v_lshl_add_u64 v[130:131], s[0:1], 0, v[198:199]
	s_add_i32 m0, s28, 0x2000
	s_nop 0
	global_load_lds_dwordx4 v[130:131], off
	v_add_u32_e32 v142, 0x10000, v237
	ds_read_b128 v[130:133], v142
	ds_read_b128 v[134:137], v142 offset:1024
	ds_read_b128 v[138:141], v142 offset:2048
	ds_read_b128 v[142:145], v142 offset:3072
	s_waitcnt vmcnt(6)
	s_barrier
	v_mfma_f32_16x16x32_bf16 v[98:101], v[178:181], v[146:149], v[98:101]
	v_mfma_f32_16x16x32_bf16 v[102:105], v[186:189], v[146:149], v[102:105]
	v_mfma_f32_16x16x32_bf16 v[106:109], v[178:181], v[154:157], v[106:109]
	v_mfma_f32_16x16x32_bf16 v[110:113], v[186:189], v[154:157], v[110:113]
	v_mfma_f32_16x16x32_bf16 v[114:117], v[178:181], v[162:165], v[114:117]
	v_mfma_f32_16x16x32_bf16 v[118:121], v[186:189], v[162:165], v[118:121]
	v_mfma_f32_16x16x32_bf16 v[122:125], v[178:181], v[170:173], v[122:125]
	v_mfma_f32_16x16x32_bf16 v[126:129], v[186:189], v[170:173], v[126:129]
	v_mfma_f32_16x16x32_bf16 v[98:101], v[182:185], v[150:153], v[98:101]
	v_mfma_f32_16x16x32_bf16 v[102:105], v[190:193], v[150:153], v[102:105]
	v_mfma_f32_16x16x32_bf16 v[106:109], v[182:185], v[158:161], v[106:109]
	v_mfma_f32_16x16x32_bf16 v[110:113], v[190:193], v[158:161], v[110:113]
	v_mfma_f32_16x16x32_bf16 v[114:117], v[182:185], v[166:169], v[114:117]
	v_mfma_f32_16x16x32_bf16 v[118:121], v[190:193], v[166:169], v[118:121]
	v_mfma_f32_16x16x32_bf16 v[122:125], v[182:185], v[174:177], v[122:125]
	v_mfma_f32_16x16x32_bf16 v[126:129], v[190:193], v[174:177], v[126:129]
	s_add_i32 s86, s86, 2
	s_add_u32 s6, s6, 0x100
	s_addc_u32 s7, s7, 0
	s_add_u32 s21, s21, 0x100
	s_addc_u32 s82, s82, 0
	s_cmp_gt_u32 s86, 5
	s_barrier
	s_cbranch_scc0 .LBB0_1332
	s_waitcnt lgkmcnt(0)
	s_cmp_lg_u32 s27, 0
	s_cselect_b64 s[6:7], -1, 0
	s_cmp_eq_u32 s27, 0
	v_lshl_add_u32 v218, s26, 8, v1
	s_cselect_b32 s0, 0, 0x10000
	s_add_u32 s26, s74, s0
	v_ashrrev_i32_e32 v130, 5, v218
	s_addc_u32 s27, s75, 0
	v_and_b32_e32 v136, -8, v130
	s_lshl_b32 s0, s79, 1
	v_add_u32_e32 v130, s0, v136
	v_ashrrev_i32_e32 v131, 31, v130
	v_lshlrev_b64 v[130:131], 17, v[130:131]
	v_lshl_add_u64 v[132:133], v[206:207], 1, s[26:27]
	v_lshl_add_u64 v[134:135], v[132:133], 0, v[130:131]
	s_or_b32 s1, s0, 1
	global_load_dwordx4 v[186:189], v[134:135], off
	v_add_u32_e32 v134, s1, v136
	v_ashrrev_i32_e32 v135, 31, v134
	v_lshlrev_b64 v[134:135], 17, v[134:135]
	v_lshl_add_u64 v[132:133], v[132:133], 0, v[134:135]
	global_load_dwordx4 v[178:181], v[132:133], off
	v_lshl_add_u64 v[132:133], v[208:209], 1, s[26:27]
	v_lshl_add_u64 v[136:137], v[132:133], 0, v[130:131]
	global_load_dwordx4 v[174:177], v[136:137], off
	v_lshl_add_u64 v[132:133], v[132:133], 0, v[134:135]
	global_load_dwordx4 v[170:173], v[132:133], off
	v_lshl_add_u64 v[132:133], v[210:211], 1, s[26:27]
	v_lshl_add_u64 v[136:137], v[132:133], 0, v[130:131]
	v_lshl_add_u64 v[132:133], v[132:133], 0, v[134:135]
	global_load_dwordx4 v[162:165], v[136:137], off
	global_load_dwordx4 v[150:153], v[132:133], off
	v_lshl_add_u64 v[132:133], v[212:213], 1, s[26:27]
	v_lshl_add_u64 v[130:131], v[132:133], 0, v[130:131]
	global_load_dwordx4 v[142:145], v[130:131], off
	v_lshl_add_u64 v[130:131], v[132:133], 0, v[134:135]
	v_add_u32_e32 v220, 0x80, v218
	global_load_dwordx4 v[134:137], v[130:131], off
	v_ashrrev_i32_e32 v130, 5, v220
	v_and_b32_e32 v146, -8, v130
	v_add_u32_e32 v130, s0, v146
	v_ashrrev_i32_e32 v131, 31, v130
	v_lshlrev_b64 v[182:183], 17, v[130:131]
	v_lshlrev_b32_e32 v130, 7, v220
	s_movk_i32 s0, 0x4000
	v_and_or_b32 v130, v130, s0, v238
	v_lshlrev_b32_e32 v194, 1, v130
	v_lshl_add_u64 v[130:131], s[26:27], 0, v[194:195]
	v_lshl_add_u64 v[132:133], v[130:131], 0, v[182:183]
	global_load_dwordx4 v[138:141], v[132:133], off
	v_add_u32_e32 v132, s1, v146
	v_ashrrev_i32_e32 v133, 31, v132
	v_lshlrev_b64 v[190:191], 17, v[132:133]
	v_lshl_add_u64 v[130:131], v[130:131], 0, v[190:191]
	global_load_dwordx4 v[130:133], v[130:131], off
	v_or_b32_e32 v146, 0x2000, v194
	v_mov_b32_e32 v147, v195
	v_lshl_add_u64 v[146:147], s[26:27], 0, v[146:147]
	v_lshl_add_u64 v[148:149], v[146:147], 0, v[182:183]
	global_load_dwordx4 v[166:169], v[148:149], off
	v_lshl_add_u64 v[146:147], v[146:147], 0, v[190:191]
	global_load_dwordx4 v[154:157], v[146:147], off
	v_or_b32_e32 v146, 0x4000, v194
	v_mov_b32_e32 v147, v195
	v_lshl_add_u64 v[146:147], s[26:27], 0, v[146:147]
	v_lshl_add_u64 v[148:149], v[146:147], 0, v[182:183]
	global_load_dwordx4 v[158:161], v[148:149], off
	v_or_b32_e32 v194, 0x6000, v194
	v_lshl_add_u64 v[192:193], s[26:27], 0, v[194:195]
	v_lshl_add_u64 v[146:147], v[146:147], 0, v[190:191]
	v_lshl_add_u64 v[190:191], v[192:193], 0, v[190:191]
	v_lshl_add_u64 v[182:183], v[192:193], 0, v[182:183]
	global_load_dwordx4 v[190:193], v[190:191], off
	s_and_b64 vcc, exec, s[6:7]
	global_load_dwordx4 v[146:149], v[146:147], off
	s_waitcnt vmcnt(0)
	v_lshlrev_b32_e32 v224, 16, v186
	global_load_dwordx4 v[182:185], v[182:183], off
	v_and_b32_e32 v225, 0xffff0000, v186
	v_lshlrev_b32_e32 v186, 16, v187
	v_and_b32_e32 v187, 0xffff0000, v187
	v_pk_mul_f32 v[64:65], v[64:65], v[186:187]
	v_lshlrev_b32_e32 v186, 16, v188
	v_and_b32_e32 v187, 0xffff0000, v188
	v_pk_mul_f32 v[58:59], v[58:59], v[186:187]
	v_lshlrev_b32_e32 v186, 16, v189
	v_and_b32_e32 v187, 0xffff0000, v189
	v_pk_mul_f32 v[60:61], v[60:61], v[186:187]
	v_lshlrev_b32_e32 v186, 16, v178
	v_and_b32_e32 v187, 0xffff0000, v178
	v_lshlrev_b32_e32 v178, 16, v179
	v_and_b32_e32 v179, 0xffff0000, v179
	v_pk_mul_f32 v[32:33], v[32:33], v[178:179]
	v_lshlrev_b32_e32 v178, 16, v180
	v_and_b32_e32 v179, 0xffff0000, v180
	v_pk_mul_f32 v[26:27], v[26:27], v[178:179]
	v_lshlrev_b32_e32 v178, 16, v181
	v_and_b32_e32 v179, 0xffff0000, v181
	v_pk_mul_f32 v[28:29], v[28:29], v[178:179]
	v_lshlrev_b32_e32 v178, 16, v174
	v_and_b32_e32 v179, 0xffff0000, v174
	v_lshlrev_b32_e32 v174, 16, v175
	v_and_b32_e32 v175, 0xffff0000, v175
	v_pk_mul_f32 v[56:57], v[56:57], v[174:175]
	v_lshlrev_b32_e32 v174, 16, v176
	v_and_b32_e32 v175, 0xffff0000, v176
	v_pk_mul_f32 v[50:51], v[50:51], v[174:175]
	v_lshlrev_b32_e32 v174, 16, v177
	v_and_b32_e32 v175, 0xffff0000, v177
	v_pk_mul_f32 v[52:53], v[52:53], v[174:175]
	v_lshlrev_b32_e32 v174, 16, v170
	v_and_b32_e32 v175, 0xffff0000, v170
	v_lshlrev_b32_e32 v170, 16, v171
	v_and_b32_e32 v171, 0xffff0000, v171
	v_pk_mul_f32 v[24:25], v[24:25], v[170:171]
	v_lshlrev_b32_e32 v170, 16, v172
	v_and_b32_e32 v171, 0xffff0000, v172
	v_pk_mul_f32 v[18:19], v[18:19], v[170:171]
	v_lshlrev_b32_e32 v170, 16, v173
	v_and_b32_e32 v171, 0xffff0000, v173
	v_pk_mul_f32 v[20:21], v[20:21], v[170:171]
	v_lshlrev_b32_e32 v170, 16, v162
	v_and_b32_e32 v171, 0xffff0000, v162
	v_lshlrev_b32_e32 v162, 16, v163
	v_and_b32_e32 v163, 0xffff0000, v163
	v_pk_mul_f32 v[48:49], v[48:49], v[162:163]
	v_lshlrev_b32_e32 v162, 16, v164
	v_and_b32_e32 v163, 0xffff0000, v164
	v_pk_mul_f32 v[42:43], v[42:43], v[162:163]
	v_lshlrev_b32_e32 v162, 16, v165
	v_and_b32_e32 v163, 0xffff0000, v165
	v_pk_mul_f32 v[44:45], v[44:45], v[162:163]
	v_lshlrev_b32_e32 v162, 16, v150
	v_and_b32_e32 v163, 0xffff0000, v150
	v_lshlrev_b32_e32 v150, 16, v151
	v_and_b32_e32 v151, 0xffff0000, v151
	v_pk_mul_f32 v[16:17], v[16:17], v[150:151]
	v_lshlrev_b32_e32 v150, 16, v152
	v_and_b32_e32 v151, 0xffff0000, v152
	v_pk_mul_f32 v[10:11], v[10:11], v[150:151]
	v_lshlrev_b32_e32 v150, 16, v153
	v_and_b32_e32 v151, 0xffff0000, v153
	v_pk_mul_f32 v[12:13], v[12:13], v[150:151]
	v_lshlrev_b32_e32 v150, 16, v142
	v_and_b32_e32 v151, 0xffff0000, v142
	v_lshlrev_b32_e32 v142, 16, v143
	v_and_b32_e32 v143, 0xffff0000, v143
	v_pk_mul_f32 v[40:41], v[40:41], v[142:143]
	v_lshlrev_b32_e32 v142, 16, v144
	v_and_b32_e32 v143, 0xffff0000, v144
	v_pk_mul_f32 v[34:35], v[34:35], v[142:143]
	v_lshlrev_b32_e32 v142, 16, v145
	v_and_b32_e32 v143, 0xffff0000, v145
	v_pk_mul_f32 v[36:37], v[36:37], v[142:143]
	v_lshlrev_b32_e32 v142, 16, v134
	v_and_b32_e32 v143, 0xffff0000, v134
	v_lshlrev_b32_e32 v134, 16, v135
	v_and_b32_e32 v135, 0xffff0000, v135
	v_pk_mul_f32 v[8:9], v[8:9], v[134:135]
	v_lshlrev_b32_e32 v134, 16, v136
	v_and_b32_e32 v135, 0xffff0000, v136
	v_pk_mul_f32 v[2:3], v[2:3], v[134:135]
	v_lshlrev_b32_e32 v134, 16, v137
	v_and_b32_e32 v135, 0xffff0000, v137
	v_pk_mul_f32 v[4:5], v[4:5], v[134:135]
	v_lshlrev_b32_e32 v134, 16, v138
	v_and_b32_e32 v135, 0xffff0000, v138
	v_pk_mul_f32 v[66:67], v[66:67], v[134:135]
	v_lshlrev_b32_e32 v134, 16, v139
	v_and_b32_e32 v135, 0xffff0000, v139
	v_pk_mul_f32 v[68:69], v[68:69], v[134:135]
	v_lshlrev_b32_e32 v134, 16, v140
	v_and_b32_e32 v135, 0xffff0000, v140
	v_pk_mul_f32 v[70:71], v[70:71], v[134:135]
	v_lshlrev_b32_e32 v134, 16, v141
	v_and_b32_e32 v135, 0xffff0000, v141
	v_pk_mul_f32 v[72:73], v[72:73], v[134:135]
	v_lshlrev_b32_e32 v134, 16, v130
	v_and_b32_e32 v135, 0xffff0000, v130
	v_lshlrev_b32_e32 v130, 16, v131
	v_and_b32_e32 v131, 0xffff0000, v131
	v_pk_mul_f32 v[100:101], v[100:101], v[130:131]
	v_lshlrev_b32_e32 v130, 16, v132
	v_and_b32_e32 v131, 0xffff0000, v132
	v_pk_mul_f32 v[102:103], v[102:103], v[130:131]
	v_lshlrev_b32_e32 v130, 16, v133
	v_and_b32_e32 v131, 0xffff0000, v133
	v_pk_mul_f32 v[104:105], v[104:105], v[130:131]
	v_lshlrev_b32_e32 v130, 16, v166
	v_and_b32_e32 v131, 0xffff0000, v166
	v_pk_mul_f32 v[74:75], v[74:75], v[130:131]
	v_lshlrev_b32_e32 v130, 16, v167
	v_and_b32_e32 v131, 0xffff0000, v167
	v_pk_mul_f32 v[76:77], v[76:77], v[130:131]
	v_lshlrev_b32_e32 v130, 16, v168
	v_and_b32_e32 v131, 0xffff0000, v168
	v_pk_mul_f32 v[78:79], v[78:79], v[130:131]
	v_lshlrev_b32_e32 v130, 16, v169
	v_and_b32_e32 v131, 0xffff0000, v169
	v_pk_mul_f32 v[80:81], v[80:81], v[130:131]
	v_lshlrev_b32_e32 v130, 16, v154
	v_and_b32_e32 v131, 0xffff0000, v154
	v_pk_mul_f32 v[106:107], v[106:107], v[130:131]
	v_lshlrev_b32_e32 v130, 16, v155
	v_and_b32_e32 v131, 0xffff0000, v155
	v_pk_mul_f32 v[108:109], v[108:109], v[130:131]
	v_lshlrev_b32_e32 v130, 16, v156
	v_and_b32_e32 v131, 0xffff0000, v156
	v_pk_mul_f32 v[110:111], v[110:111], v[130:131]
	v_lshlrev_b32_e32 v130, 16, v157
	v_and_b32_e32 v131, 0xffff0000, v157
	v_pk_mul_f32 v[112:113], v[112:113], v[130:131]
	v_lshlrev_b32_e32 v130, 16, v158
	v_and_b32_e32 v131, 0xffff0000, v158
	v_pk_mul_f32 v[82:83], v[82:83], v[130:131]
	v_lshlrev_b32_e32 v130, 16, v159
	v_and_b32_e32 v131, 0xffff0000, v159
	v_pk_mul_f32 v[84:85], v[84:85], v[130:131]
	v_lshlrev_b32_e32 v130, 16, v160
	v_and_b32_e32 v131, 0xffff0000, v160
	v_pk_mul_f32 v[86:87], v[86:87], v[130:131]
	v_lshlrev_b32_e32 v130, 16, v161
	v_and_b32_e32 v131, 0xffff0000, v161
	v_pk_mul_f32 v[88:89], v[88:89], v[130:131]
	v_lshlrev_b32_e32 v130, 16, v146
	v_and_b32_e32 v131, 0xffff0000, v146
	v_pk_mul_f32 v[114:115], v[114:115], v[130:131]
	v_lshlrev_b32_e32 v130, 16, v147
	v_and_b32_e32 v131, 0xffff0000, v147
	v_pk_mul_f32 v[116:117], v[116:117], v[130:131]
	v_lshlrev_b32_e32 v130, 16, v148
	v_and_b32_e32 v131, 0xffff0000, v148
	v_pk_mul_f32 v[118:119], v[118:119], v[130:131]
	v_lshlrev_b32_e32 v130, 16, v149
	v_and_b32_e32 v131, 0xffff0000, v149
	v_pk_mul_f32 v[120:121], v[120:121], v[130:131]
	s_waitcnt vmcnt(0)
	v_lshlrev_b32_e32 v130, 16, v182
	v_and_b32_e32 v131, 0xffff0000, v182
	v_pk_mul_f32 v[90:91], v[90:91], v[130:131]
	v_lshlrev_b32_e32 v130, 16, v183
	v_and_b32_e32 v131, 0xffff0000, v183
	v_pk_mul_f32 v[92:93], v[92:93], v[130:131]
	v_lshlrev_b32_e32 v130, 16, v184
	v_and_b32_e32 v131, 0xffff0000, v184
	v_pk_mul_f32 v[94:95], v[94:95], v[130:131]
	v_lshlrev_b32_e32 v130, 16, v185
	v_and_b32_e32 v131, 0xffff0000, v185
	v_pk_mul_f32 v[96:97], v[96:97], v[130:131]
	v_lshlrev_b32_e32 v130, 16, v190
	v_and_b32_e32 v131, 0xffff0000, v190
	v_pk_mul_f32 v[122:123], v[122:123], v[130:131]
	v_lshlrev_b32_e32 v130, 16, v191
	v_and_b32_e32 v131, 0xffff0000, v191
	v_pk_mul_f32 v[124:125], v[124:125], v[130:131]
	v_lshlrev_b32_e32 v130, 16, v192
	v_and_b32_e32 v131, 0xffff0000, v192
	v_pk_mul_f32 v[126:127], v[126:127], v[130:131]
	v_lshlrev_b32_e32 v130, 16, v193
	v_and_b32_e32 v131, 0xffff0000, v193
	v_pk_mul_f32 v[62:63], v[62:63], v[224:225]
	v_pk_mul_f32 v[30:31], v[30:31], v[186:187]
	v_pk_mul_f32 v[54:55], v[54:55], v[178:179]
	v_pk_mul_f32 v[22:23], v[22:23], v[174:175]
	v_pk_mul_f32 v[46:47], v[46:47], v[170:171]
	v_pk_mul_f32 v[14:15], v[14:15], v[162:163]
	v_pk_mul_f32 v[38:39], v[38:39], v[150:151]
	v_pk_mul_f32 v[6:7], v[6:7], v[142:143]
	v_pk_mul_f32 v[98:99], v[98:99], v[134:135]
	v_pk_mul_f32 v[128:129], v[128:129], v[130:131]
	s_cbranch_vccz .LBB0_1335
	v_lshl_or_b32 v134, s79, 8, v239
	v_ashrrev_i32_e32 v219, 31, v218
	v_lshlrev_b64 v[130:131], 11, v[218:219]
	v_ashrrev_i32_e32 v135, 31, v134
	v_lshl_add_u64 v[136:137], s[8:9], 0, v[130:131]
	v_lshlrev_b64 v[134:135], 1, v[134:135]
	v_cvt_pk_bf16_f32 v130, v62, v63
	v_cvt_pk_bf16_f32 v131, v64, v65
	v_cvt_pk_bf16_f32 v132, v58, v59
	v_cvt_pk_bf16_f32 v133, v60, v61
	v_lshl_add_u64 v[136:137], v[136:137], 0, v[134:135]
	global_store_dwordx4 v[136:137], v[130:133], off
	v_ashrrev_i32_e32 v221, 31, v220
	s_mov_b64 s[0:1], 0x48000
	v_cvt_pk_bf16_f32 v130, v30, v31
	v_cvt_pk_bf16_f32 v131, v32, v33
	v_cvt_pk_bf16_f32 v132, v26, v27
	v_cvt_pk_bf16_f32 v133, v28, v29
	global_store_dwordx4 v[136:137], v[130:133], off offset:256
	s_nop 1
	v_or_b32_e32 v130, 16, v218
	v_ashrrev_i32_e32 v131, 31, v130
	v_lshlrev_b64 v[130:131], 11, v[130:131]
	v_lshl_add_u64 v[138:139], s[8:9], 0, v[130:131]
	v_cvt_pk_bf16_f32 v130, v54, v55
	v_cvt_pk_bf16_f32 v131, v56, v57
	v_cvt_pk_bf16_f32 v132, v50, v51
	v_cvt_pk_bf16_f32 v133, v52, v53
	v_lshl_add_u64 v[138:139], v[138:139], 0, v[134:135]
	global_store_dwordx4 v[138:139], v[130:133], off
	s_nop 1
	v_cvt_pk_bf16_f32 v130, v22, v23
	v_cvt_pk_bf16_f32 v131, v24, v25
	v_cvt_pk_bf16_f32 v132, v18, v19
	v_cvt_pk_bf16_f32 v133, v20, v21
	global_store_dwordx4 v[138:139], v[130:133], off offset:256
	s_nop 1
	v_or_b32_e32 v130, 32, v218
	v_ashrrev_i32_e32 v131, 31, v130
	v_lshlrev_b64 v[130:131], 11, v[130:131]
	v_lshl_add_u64 v[138:139], s[8:9], 0, v[130:131]
	v_cvt_pk_bf16_f32 v130, v46, v47
	v_cvt_pk_bf16_f32 v131, v48, v49
	v_cvt_pk_bf16_f32 v132, v42, v43
	v_cvt_pk_bf16_f32 v133, v44, v45
	v_lshl_add_u64 v[138:139], v[138:139], 0, v[134:135]
	global_store_dwordx4 v[138:139], v[130:133], off
	s_nop 1
	v_cvt_pk_bf16_f32 v130, v14, v15
	v_cvt_pk_bf16_f32 v131, v16, v17
	v_cvt_pk_bf16_f32 v132, v10, v11
	v_cvt_pk_bf16_f32 v133, v12, v13
	global_store_dwordx4 v[138:139], v[130:133], off offset:256
	s_nop 1
	v_or_b32_e32 v130, 48, v218
	v_ashrrev_i32_e32 v131, 31, v130
	v_lshlrev_b64 v[130:131], 11, v[130:131]
	v_lshl_add_u64 v[138:139], s[8:9], 0, v[130:131]
	v_cvt_pk_bf16_f32 v130, v38, v39
	v_cvt_pk_bf16_f32 v131, v40, v41
	v_cvt_pk_bf16_f32 v132, v34, v35
	v_cvt_pk_bf16_f32 v133, v36, v37
	v_lshl_add_u64 v[138:139], v[138:139], 0, v[134:135]
	global_store_dwordx4 v[138:139], v[130:133], off
	s_nop 1
	v_cvt_pk_bf16_f32 v130, v6, v7
	v_cvt_pk_bf16_f32 v131, v8, v9
	v_cvt_pk_bf16_f32 v132, v2, v3
	v_cvt_pk_bf16_f32 v133, v4, v5
	global_store_dwordx4 v[138:139], v[130:133], off offset:256
	s_nop 1
	v_lshlrev_b64 v[130:131], 11, v[220:221]
	v_lshl_add_u64 v[138:139], s[8:9], 0, v[130:131]
	v_cvt_pk_bf16_f32 v130, v66, v67
	v_cvt_pk_bf16_f32 v131, v68, v69
	v_cvt_pk_bf16_f32 v132, v70, v71
	v_cvt_pk_bf16_f32 v133, v72, v73
	v_lshl_add_u64 v[134:135], v[138:139], 0, v[134:135]
	global_store_dwordx4 v[134:135], v[130:133], off
	s_nop 1
	v_cvt_pk_bf16_f32 v130, v98, v99
	v_cvt_pk_bf16_f32 v131, v100, v101
	v_cvt_pk_bf16_f32 v132, v102, v103
	v_cvt_pk_bf16_f32 v133, v104, v105
	global_store_dwordx4 v[134:135], v[130:133], off offset:256
	v_lshl_add_u64 v[134:135], v[136:137], 0, s[0:1]
	s_mov_b32 s0, 0x48000
	v_add_co_u32_e32 v138, vcc, s0, v136
	v_cvt_pk_bf16_f32 v130, v74, v75
	v_cvt_pk_bf16_f32 v131, v76, v77
	v_cvt_pk_bf16_f32 v132, v78, v79
	v_cvt_pk_bf16_f32 v133, v80, v81
	v_addc_co_u32_e32 v139, vcc, 0, v137, vcc
	global_store_dwordx4 v[138:139], v[130:133], off
	s_mov_b64 s[0:1], 0x50000
	s_nop 0
	v_cvt_pk_bf16_f32 v130, v106, v107
	v_cvt_pk_bf16_f32 v131, v108, v109
	v_cvt_pk_bf16_f32 v132, v110, v111
	v_cvt_pk_bf16_f32 v133, v112, v113
	global_store_dwordx4 v[134:135], v[130:133], off offset:256
	v_lshl_add_u64 v[134:135], v[136:137], 0, s[0:1]
	s_mov_b32 s0, 0x50000
	v_add_co_u32_e32 v138, vcc, s0, v136
	v_cvt_pk_bf16_f32 v130, v82, v83
	v_cvt_pk_bf16_f32 v131, v84, v85
	v_cvt_pk_bf16_f32 v132, v86, v87
	v_cvt_pk_bf16_f32 v133, v88, v89
	v_addc_co_u32_e32 v139, vcc, 0, v137, vcc
	global_store_dwordx4 v[138:139], v[130:133], off
	s_mov_b64 s[0:1], 0x58000
	s_nop 0
	v_cvt_pk_bf16_f32 v130, v114, v115
	v_cvt_pk_bf16_f32 v131, v116, v117
	v_cvt_pk_bf16_f32 v132, v118, v119
	v_cvt_pk_bf16_f32 v133, v120, v121
	global_store_dwordx4 v[134:135], v[130:133], off offset:256
	v_lshl_add_u64 v[134:135], v[136:137], 0, s[0:1]
	s_mov_b32 s0, 0x58000
	v_add_co_u32_e32 v136, vcc, s0, v136
	v_cvt_pk_bf16_f32 v130, v90, v91
	v_cvt_pk_bf16_f32 v131, v92, v93
	v_cvt_pk_bf16_f32 v132, v94, v95
	v_cvt_pk_bf16_f32 v133, v96, v97
	v_addc_co_u32_e32 v137, vcc, 0, v137, vcc
	global_store_dwordx4 v[136:137], v[130:133], off
	s_nop 1
	v_cvt_pk_bf16_f32 v130, v122, v123
	v_cvt_pk_bf16_f32 v131, v124, v125
	v_cvt_pk_bf16_f32 v132, v126, v127
	v_cvt_pk_bf16_f32 v133, v128, v129
	global_store_dwordx4 v[134:135], v[130:133], off offset:256

.LBB0_1764:
	s_ashr_i32 s19, s18, 31
	v_mov_b64_e32 v[2:3], s[48:49]
	s_lshl_b64 s[0:1], s[18:19], 19
	v_cmp_lt_i64_e32 vcc, s[20:21], v[2:3]
	s_add_u32 s20, s35, s0
	s_addc_u32 s21, s40, s1
	s_and_b64 s[0:1], vcc, exec
	s_cselect_b32 s19, s21, s25
	s_cselect_b32 s76, s20, s24
	s_ashr_i32 s15, s14, 31
	s_lshl_b64 s[0:1], s[14:15], 19
	s_add_u32 s22, s16, s0
	s_addc_u32 s23, s17, s1
	s_and_b64 s[0:1], vcc, exec
	s_cselect_b32 s15, s23, s27
	s_cselect_b32 s77, s22, s26
	s_add_u32 s24, s24, 0x40080
	s_addc_u32 s25, s25, 0
	s_add_u32 s78, s26, 0x100
	v_mov_b32_e32 v2, 0
	s_addc_u32 s79, s27, 0
	s_mov_b32 s82, -2
	v_mov_b32_e32 v3, v2
	v_mov_b32_e32 v4, v2
	v_mov_b32_e32 v5, v2
	v_mov_b32_e32 v6, v2
	v_mov_b32_e32 v7, v2
	v_mov_b32_e32 v8, v2
	v_mov_b32_e32 v9, v2
	v_mov_b32_e32 v10, v2
	v_mov_b32_e32 v11, v2
	v_mov_b32_e32 v12, v2
	v_mov_b32_e32 v13, v2
	v_mov_b32_e32 v14, v2
	v_mov_b32_e32 v15, v2
	v_mov_b32_e32 v16, v2
	v_mov_b32_e32 v17, v2
	v_mov_b32_e32 v26, v2
	v_mov_b32_e32 v27, v2
	v_mov_b32_e32 v28, v2
	v_mov_b32_e32 v29, v2
	v_mov_b32_e32 v30, v2
	v_mov_b32_e32 v31, v2
	v_mov_b32_e32 v32, v2
	v_mov_b32_e32 v33, v2
	v_mov_b32_e32 v42, v2
	v_mov_b32_e32 v43, v2
	v_mov_b32_e32 v44, v2
	v_mov_b32_e32 v45, v2
	v_mov_b32_e32 v46, v2
	v_mov_b32_e32 v47, v2
	v_mov_b32_e32 v48, v2
	v_mov_b32_e32 v49, v2
	v_mov_b32_e32 v18, v2
	v_mov_b32_e32 v19, v2
	v_mov_b32_e32 v20, v2
	v_mov_b32_e32 v21, v2
	v_mov_b32_e32 v22, v2
	v_mov_b32_e32 v23, v2
	v_mov_b32_e32 v24, v2
	v_mov_b32_e32 v25, v2
	v_mov_b32_e32 v34, v2
	v_mov_b32_e32 v35, v2
	v_mov_b32_e32 v36, v2
	v_mov_b32_e32 v37, v2
	v_mov_b32_e32 v38, v2
	v_mov_b32_e32 v39, v2
	v_mov_b32_e32 v40, v2
	v_mov_b32_e32 v41, v2
	v_mov_b32_e32 v50, v2
	v_mov_b32_e32 v51, v2
	v_mov_b32_e32 v52, v2
	v_mov_b32_e32 v53, v2
	v_mov_b32_e32 v54, v2
	v_mov_b32_e32 v55, v2
	v_mov_b32_e32 v56, v2
	v_mov_b32_e32 v57, v2
	v_mov_b32_e32 v58, v2
	v_mov_b32_e32 v59, v2
	v_mov_b32_e32 v60, v2
	v_mov_b32_e32 v61, v2
	v_mov_b32_e32 v62, v2
	v_mov_b32_e32 v63, v2
	v_mov_b32_e32 v64, v2
	v_mov_b32_e32 v65, v2
	v_mov_b32_e32 v66, v2
	v_mov_b32_e32 v67, v2
	v_mov_b32_e32 v68, v2
	v_mov_b32_e32 v69, v2
	v_mov_b32_e32 v70, v2
	v_mov_b32_e32 v71, v2
	v_mov_b32_e32 v72, v2
	v_mov_b32_e32 v73, v2
	v_mov_b32_e32 v74, v2
	v_mov_b32_e32 v75, v2
	v_mov_b32_e32 v76, v2
	v_mov_b32_e32 v77, v2
	v_mov_b32_e32 v78, v2
	v_mov_b32_e32 v79, v2
	v_mov_b32_e32 v80, v2
	v_mov_b32_e32 v81, v2
	v_mov_b32_e32 v90, v2
	v_mov_b32_e32 v91, v2
	v_mov_b32_e32 v92, v2
	v_mov_b32_e32 v93, v2
	v_mov_b32_e32 v94, v2
	v_mov_b32_e32 v95, v2
	v_mov_b32_e32 v96, v2
	v_mov_b32_e32 v97, v2
	v_mov_b32_e32 v106, v2
	v_mov_b32_e32 v107, v2
	v_mov_b32_e32 v108, v2
	v_mov_b32_e32 v109, v2
	v_mov_b32_e32 v110, v2
	v_mov_b32_e32 v111, v2
	v_mov_b32_e32 v112, v2
	v_mov_b32_e32 v113, v2
	v_mov_b32_e32 v82, v2
	v_mov_b32_e32 v83, v2
	v_mov_b32_e32 v84, v2
	v_mov_b32_e32 v85, v2
	v_mov_b32_e32 v86, v2
	v_mov_b32_e32 v87, v2
	v_mov_b32_e32 v88, v2
	v_mov_b32_e32 v89, v2
	v_mov_b32_e32 v98, v2
	v_mov_b32_e32 v99, v2
	v_mov_b32_e32 v100, v2
	v_mov_b32_e32 v101, v2
	v_mov_b32_e32 v102, v2
	v_mov_b32_e32 v103, v2
	v_mov_b32_e32 v104, v2
	v_mov_b32_e32 v105, v2
	v_mov_b32_e32 v114, v2
	v_mov_b32_e32 v115, v2
	v_mov_b32_e32 v116, v2
	v_mov_b32_e32 v117, v2
	v_mov_b32_e32 v118, v2
	v_mov_b32_e32 v119, v2
	v_mov_b32_e32 v120, v2
	v_mov_b32_e32 v121, v2
	v_mov_b32_e32 v122, v2
	v_mov_b32_e32 v123, v2
	v_mov_b32_e32 v124, v2
	v_mov_b32_e32 v125, v2
	v_mov_b32_e32 v126, v2
	v_mov_b32_e32 v127, v2
	v_mov_b32_e32 v128, v2
	v_mov_b32_e32 v129, v2
	v_add_u32_e32 v156, 0x10000, v141
	ds_read_b128 v[144:147], v156
	ds_read_b128 v[148:151], v156 offset:1024
	ds_read_b128 v[152:155], v156 offset:2048
	ds_read_b128 v[156:159], v156 offset:3072
.LBB0_1765:
	s_add_u32 s0, s24, 0xfffc0080
	s_addc_u32 s1, s25, -1
	s_add_i32 s33, 0, 0x10000
	s_cmp_eq_u32 s82, 12
	s_cselect_b32 s29, s19, s1
	s_cselect_b32 s28, s76, s0
	s_cselect_b32 s27, s15, s79
	s_cselect_b32 s26, s77, s78
	v_lshl_add_u64 v[192:193], s[24:25], 0, v[136:137]
	s_add_i32 m0, s13, 0xc000
	ds_read_b128 v[160:163], v143
	ds_read_b128 v[164:167], v143 offset:1024
	ds_read_b128 v[168:171], v143 offset:2048
	ds_read_b128 v[172:175], v143 offset:3072
	ds_read_b128 v[176:179], v143 offset:4096
	ds_read_b128 v[180:183], v143 offset:5120
	ds_read_b128 v[184:187], v143 offset:6144
	ds_read_b128 v[188:191], v143 offset:7168
	global_load_lds_dwordx4 v[192:193], off
	v_lshl_add_u64 v[192:193], s[24:25], 0, v[138:139]
	s_add_i32 m0, s13, 0xe000
	s_nop 0
	global_load_lds_dwordx4 v[192:193], off
	s_waitcnt lgkmcnt(8)
	s_barrier
	s_waitcnt lgkmcnt(0)
	s_waitcnt lgkmcnt(0)
	v_mfma_f32_16x16x32_bf16 v[126:129], v[144:147], v[160:163], v[126:129]
	v_mfma_f32_16x16x32_bf16 v[122:125], v[152:155], v[160:163], v[122:125]
	v_mfma_f32_16x16x32_bf16 v[118:121], v[144:147], v[168:171], v[118:121]
	v_mfma_f32_16x16x32_bf16 v[114:117], v[152:155], v[168:171], v[114:117]
	v_mfma_f32_16x16x32_bf16 v[102:105], v[144:147], v[176:179], v[102:105]
	v_mfma_f32_16x16x32_bf16 v[98:101], v[152:155], v[176:179], v[98:101]
	v_mfma_f32_16x16x32_bf16 v[86:89], v[144:147], v[184:187], v[86:89]
	v_mfma_f32_16x16x32_bf16 v[82:85], v[152:155], v[184:187], v[82:85]
	v_mfma_f32_16x16x32_bf16 v[126:129], v[148:151], v[164:167], v[126:129]
	v_mfma_f32_16x16x32_bf16 v[122:125], v[156:159], v[164:167], v[122:125]
	v_mfma_f32_16x16x32_bf16 v[118:121], v[148:151], v[172:175], v[118:121]
	v_mfma_f32_16x16x32_bf16 v[114:117], v[156:159], v[172:175], v[114:117]
	v_mfma_f32_16x16x32_bf16 v[102:105], v[148:151], v[180:183], v[102:105]
	v_mfma_f32_16x16x32_bf16 v[98:101], v[156:159], v[180:183], v[98:101]
	v_mfma_f32_16x16x32_bf16 v[86:89], v[148:151], v[188:191], v[86:89]
	v_mfma_f32_16x16x32_bf16 v[82:85], v[156:159], v[188:191], v[82:85]
	s_barrier
	s_add_i32 s36, 0, 0x14000
	v_add_u32_e32 v192, s36, v141
	s_add_i32 s0, s33, s64
	ds_read_b128 v[198:201], v192
	ds_read_b128 v[202:205], v192 offset:1024
	ds_read_b128 v[206:209], v192 offset:2048
	ds_read_b128 v[210:213], v192 offset:3072
	v_lshl_add_u64 v[192:193], s[26:27], 0, v[194:195]
	s_mov_b32 m0, s0
	v_lshl_add_u64 v[214:215], s[26:27], 0, v[130:131]
	global_load_lds_dwordx4 v[192:193], off
	s_add_i32 m0, s0, 0x2000
	s_nop 0
	global_load_lds_dwordx4 v[214:215], off
	s_barrier
	s_waitcnt lgkmcnt(0)
	s_waitcnt lgkmcnt(0)
	v_mfma_f32_16x16x32_bf16 v[110:113], v[198:201], v[160:163], v[110:113]
	v_mfma_f32_16x16x32_bf16 v[106:109], v[206:209], v[160:163], v[106:109]
	v_mfma_f32_16x16x32_bf16 v[94:97], v[198:201], v[168:171], v[94:97]
	v_mfma_f32_16x16x32_bf16 v[90:93], v[206:209], v[168:171], v[90:93]
	v_mfma_f32_16x16x32_bf16 v[78:81], v[198:201], v[176:179], v[78:81]
	v_mfma_f32_16x16x32_bf16 v[74:77], v[206:209], v[176:179], v[74:77]
	v_mfma_f32_16x16x32_bf16 v[70:73], v[198:201], v[184:187], v[70:73]
	v_mfma_f32_16x16x32_bf16 v[66:69], v[206:209], v[184:187], v[66:69]
	v_mfma_f32_16x16x32_bf16 v[110:113], v[202:205], v[164:167], v[110:113]
	v_mfma_f32_16x16x32_bf16 v[106:109], v[210:213], v[164:167], v[106:109]
	v_mfma_f32_16x16x32_bf16 v[94:97], v[202:205], v[172:175], v[94:97]
	v_mfma_f32_16x16x32_bf16 v[90:93], v[210:213], v[172:175], v[90:93]
	v_mfma_f32_16x16x32_bf16 v[78:81], v[202:205], v[180:183], v[78:81]
	v_mfma_f32_16x16x32_bf16 v[74:77], v[210:213], v[180:183], v[74:77]
	v_mfma_f32_16x16x32_bf16 v[70:73], v[202:205], v[188:191], v[70:73]
	v_mfma_f32_16x16x32_bf16 v[66:69], v[210:213], v[188:191], v[66:69]
	s_mov_b32 m0, s13
	v_lshl_add_u64 v[216:217], s[28:29], 0, v[134:135]
	s_barrier
	ds_read_b128 v[160:163], v143 offset:16384
	ds_read_b128 v[164:167], v143 offset:17408
	ds_read_b128 v[168:171], v143 offset:18432
	ds_read_b128 v[172:175], v143 offset:19456
	ds_read_b128 v[176:179], v143 offset:20480
	ds_read_b128 v[180:183], v143 offset:21504
	ds_read_b128 v[184:187], v143 offset:22528
	ds_read_b128 v[188:191], v143 offset:23552
	global_load_lds_dwordx4 v[216:217], off
	v_lshl_add_u64 v[218:219], s[28:29], 0, v[132:133]
	s_mov_b32 m0, s68
	s_nop 0
	global_load_lds_dwordx4 v[218:219], off
	s_waitcnt vmcnt(10)
	s_barrier
	s_waitcnt lgkmcnt(0)
	s_waitcnt lgkmcnt(0)
	v_mfma_f32_16x16x32_bf16 v[62:65], v[144:147], v[160:163], v[62:65]
	v_mfma_f32_16x16x32_bf16 v[58:61], v[152:155], v[160:163], v[58:61]
	v_mfma_f32_16x16x32_bf16 v[54:57], v[144:147], v[168:171], v[54:57]
	v_mfma_f32_16x16x32_bf16 v[50:53], v[152:155], v[168:171], v[50:53]
	v_mfma_f32_16x16x32_bf16 v[38:41], v[144:147], v[176:179], v[38:41]
	v_mfma_f32_16x16x32_bf16 v[34:37], v[152:155], v[176:179], v[34:37]
	v_mfma_f32_16x16x32_bf16 v[22:25], v[144:147], v[184:187], v[22:25]
	v_mfma_f32_16x16x32_bf16 v[18:21], v[152:155], v[184:187], v[18:21]
	v_mfma_f32_16x16x32_bf16 v[62:65], v[148:151], v[164:167], v[62:65]
	v_mfma_f32_16x16x32_bf16 v[58:61], v[156:159], v[164:167], v[58:61]
	v_mfma_f32_16x16x32_bf16 v[54:57], v[148:151], v[172:175], v[54:57]
	v_mfma_f32_16x16x32_bf16 v[50:53], v[156:159], v[172:175], v[50:53]
	v_mfma_f32_16x16x32_bf16 v[38:41], v[148:151], v[180:183], v[38:41]
	v_mfma_f32_16x16x32_bf16 v[34:37], v[156:159], v[180:183], v[34:37]
	v_mfma_f32_16x16x32_bf16 v[22:25], v[148:151], v[188:191], v[22:25]
	v_mfma_f32_16x16x32_bf16 v[18:21], v[156:159], v[188:191], v[18:21]
	s_barrier
	s_add_u32 s0, s26, 0x40000
	s_addc_u32 s1, s27, 0
	s_add_i32 s33, s36, s64
	v_lshl_add_u64 v[144:145], s[0:1], 0, v[194:195]
	s_mov_b32 m0, s33
	s_nop 0
	global_load_lds_dwordx4 v[144:145], off
	v_lshl_add_u64 v[144:145], s[0:1], 0, v[130:131]
	s_add_i32 m0, s33, 0x2000
	s_nop 0
	global_load_lds_dwordx4 v[144:145], off
	v_add_u32_e32 v156, 0x18000, v141
	ds_read_b128 v[144:147], v156
	ds_read_b128 v[148:151], v156 offset:1024
	ds_read_b128 v[152:155], v156 offset:2048
	ds_read_b128 v[156:159], v156 offset:3072
	s_waitcnt vmcnt(6)
	s_barrier
	v_mfma_f32_16x16x32_bf16 v[46:49], v[198:201], v[160:163], v[46:49]
	v_mfma_f32_16x16x32_bf16 v[42:45], v[206:209], v[160:163], v[42:45]
	v_mfma_f32_16x16x32_bf16 v[30:33], v[198:201], v[168:171], v[30:33]
	v_mfma_f32_16x16x32_bf16 v[26:29], v[206:209], v[168:171], v[26:29]
	v_mfma_f32_16x16x32_bf16 v[14:17], v[198:201], v[176:179], v[14:17]
	v_mfma_f32_16x16x32_bf16 v[10:13], v[206:209], v[176:179], v[10:13]
	v_mfma_f32_16x16x32_bf16 v[6:9], v[198:201], v[184:187], v[6:9]
	v_mfma_f32_16x16x32_bf16 v[2:5], v[206:209], v[184:187], v[2:5]
	v_mfma_f32_16x16x32_bf16 v[46:49], v[202:205], v[164:167], v[46:49]
	v_mfma_f32_16x16x32_bf16 v[42:45], v[210:213], v[164:167], v[42:45]
	v_mfma_f32_16x16x32_bf16 v[30:33], v[202:205], v[172:175], v[30:33]
	v_mfma_f32_16x16x32_bf16 v[26:29], v[210:213], v[172:175], v[26:29]
	v_mfma_f32_16x16x32_bf16 v[14:17], v[202:205], v[180:183], v[14:17]
	v_mfma_f32_16x16x32_bf16 v[10:13], v[210:213], v[180:183], v[10:13]
	v_mfma_f32_16x16x32_bf16 v[6:9], v[202:205], v[188:191], v[6:9]
	v_mfma_f32_16x16x32_bf16 v[2:5], v[210:213], v[188:191], v[2:5]
	s_add_i32 s33, 0, 0x18000
	s_barrier
	s_add_u32 s0, s28, 0x40000
	s_addc_u32 s1, s29, 0
	s_mov_b32 m0, s69
	v_lshl_add_u64 v[198:199], s[0:1], 0, v[134:135]
	ds_read_b128 v[160:163], v143 offset:32768
	ds_read_b128 v[164:167], v143 offset:33792
	ds_read_b128 v[168:171], v143 offset:34816
	ds_read_b128 v[172:175], v143 offset:35840
	ds_read_b128 v[176:179], v143 offset:36864
	ds_read_b128 v[180:183], v143 offset:37888
	ds_read_b128 v[184:187], v143 offset:38912
	ds_read_b128 v[188:191], v143 offset:39936
	global_load_lds_dwordx4 v[198:199], off
	v_lshl_add_u64 v[198:199], s[0:1], 0, v[132:133]
	s_mov_b32 m0, s70
	s_nop 0
	global_load_lds_dwordx4 v[198:199], off
	s_waitcnt lgkmcnt(8)
	s_barrier
	s_waitcnt lgkmcnt(0)
	s_waitcnt lgkmcnt(0)
	v_mfma_f32_16x16x32_bf16 v[126:129], v[144:147], v[160:163], v[126:129]
	v_mfma_f32_16x16x32_bf16 v[122:125], v[152:155], v[160:163], v[122:125]
	v_mfma_f32_16x16x32_bf16 v[118:121], v[144:147], v[168:171], v[118:121]
	v_mfma_f32_16x16x32_bf16 v[114:117], v[152:155], v[168:171], v[114:117]
	v_mfma_f32_16x16x32_bf16 v[102:105], v[144:147], v[176:179], v[102:105]
	v_mfma_f32_16x16x32_bf16 v[98:101], v[152:155], v[176:179], v[98:101]
	v_mfma_f32_16x16x32_bf16 v[86:89], v[144:147], v[184:187], v[86:89]
	v_mfma_f32_16x16x32_bf16 v[82:85], v[152:155], v[184:187], v[82:85]
	v_mfma_f32_16x16x32_bf16 v[126:129], v[148:151], v[164:167], v[126:129]
	v_mfma_f32_16x16x32_bf16 v[122:125], v[156:159], v[164:167], v[122:125]
	v_mfma_f32_16x16x32_bf16 v[118:121], v[148:151], v[172:175], v[118:121]
	v_mfma_f32_16x16x32_bf16 v[114:117], v[156:159], v[172:175], v[114:117]
	v_mfma_f32_16x16x32_bf16 v[102:105], v[148:151], v[180:183], v[102:105]
	v_mfma_f32_16x16x32_bf16 v[98:101], v[156:159], v[180:183], v[98:101]
	v_mfma_f32_16x16x32_bf16 v[86:89], v[148:151], v[188:191], v[86:89]
	v_mfma_f32_16x16x32_bf16 v[82:85], v[156:159], v[188:191], v[82:85]
	s_barrier
	s_add_i32 s28, 0, 0x1c000
	s_add_i32 s0, s33, s64
	v_add_u32_e32 v196, s28, v141
	v_lshl_add_u64 v[192:193], v[192:193], 0, s[54:55]
	s_mov_b32 m0, s0
	ds_read_b128 v[198:201], v196
	ds_read_b128 v[202:205], v196 offset:1024
	ds_read_b128 v[206:209], v196 offset:2048
	ds_read_b128 v[210:213], v196 offset:3072
	global_load_lds_dwordx4 v[192:193], off
	v_lshl_add_u64 v[192:193], v[214:215], 0, s[54:55]
	s_add_i32 m0, s0, 0x2000
	s_nop 0
	global_load_lds_dwordx4 v[192:193], off
	s_barrier
	s_waitcnt lgkmcnt(0)
	s_waitcnt lgkmcnt(0)
	v_mfma_f32_16x16x32_bf16 v[110:113], v[198:201], v[160:163], v[110:113]
	v_mfma_f32_16x16x32_bf16 v[106:109], v[206:209], v[160:163], v[106:109]
	v_mfma_f32_16x16x32_bf16 v[94:97], v[198:201], v[168:171], v[94:97]
	v_mfma_f32_16x16x32_bf16 v[90:93], v[206:209], v[168:171], v[90:93]
	v_mfma_f32_16x16x32_bf16 v[78:81], v[198:201], v[176:179], v[78:81]
	v_mfma_f32_16x16x32_bf16 v[74:77], v[206:209], v[176:179], v[74:77]
	v_mfma_f32_16x16x32_bf16 v[70:73], v[198:201], v[184:187], v[70:73]
	v_mfma_f32_16x16x32_bf16 v[66:69], v[206:209], v[184:187], v[66:69]
	v_mfma_f32_16x16x32_bf16 v[110:113], v[202:205], v[164:167], v[110:113]
	v_mfma_f32_16x16x32_bf16 v[106:109], v[210:213], v[164:167], v[106:109]
	v_mfma_f32_16x16x32_bf16 v[94:97], v[202:205], v[172:175], v[94:97]
	v_mfma_f32_16x16x32_bf16 v[90:93], v[210:213], v[172:175], v[90:93]
	v_mfma_f32_16x16x32_bf16 v[78:81], v[202:205], v[180:183], v[78:81]
	v_mfma_f32_16x16x32_bf16 v[74:77], v[210:213], v[180:183], v[74:77]
	v_mfma_f32_16x16x32_bf16 v[70:73], v[202:205], v[188:191], v[70:73]
	v_mfma_f32_16x16x32_bf16 v[66:69], v[210:213], v[188:191], v[66:69]
	s_mov_b32 m0, s71
	v_lshl_add_u64 v[192:193], v[216:217], 0, s[54:55]
	s_barrier
	ds_read_b128 v[160:163], v143 offset:49152
	ds_read_b128 v[164:167], v143 offset:50176
	ds_read_b128 v[168:171], v143 offset:51200
	ds_read_b128 v[172:175], v143 offset:52224
	ds_read_b128 v[176:179], v143 offset:53248
	ds_read_b128 v[180:183], v143 offset:54272
	ds_read_b128 v[184:187], v143 offset:55296
	ds_read_b128 v[188:191], v143 offset:56320
	global_load_lds_dwordx4 v[192:193], off
	v_lshl_add_u64 v[192:193], v[218:219], 0, s[54:55]
	s_mov_b32 m0, s72
	s_nop 0
	global_load_lds_dwordx4 v[192:193], off
	s_waitcnt vmcnt(10)
	s_barrier
	s_waitcnt lgkmcnt(0)
	s_waitcnt lgkmcnt(0)
	v_mfma_f32_16x16x32_bf16 v[62:65], v[144:147], v[160:163], v[62:65]
	v_mfma_f32_16x16x32_bf16 v[58:61], v[152:155], v[160:163], v[58:61]
	v_mfma_f32_16x16x32_bf16 v[54:57], v[144:147], v[168:171], v[54:57]
	v_mfma_f32_16x16x32_bf16 v[50:53], v[152:155], v[168:171], v[50:53]
	v_mfma_f32_16x16x32_bf16 v[38:41], v[144:147], v[176:179], v[38:41]
	v_mfma_f32_16x16x32_bf16 v[34:37], v[152:155], v[176:179], v[34:37]
	v_mfma_f32_16x16x32_bf16 v[22:25], v[144:147], v[184:187], v[22:25]
	v_mfma_f32_16x16x32_bf16 v[18:21], v[152:155], v[184:187], v[18:21]
	v_mfma_f32_16x16x32_bf16 v[62:65], v[148:151], v[164:167], v[62:65]
	v_mfma_f32_16x16x32_bf16 v[58:61], v[156:159], v[164:167], v[58:61]
	v_mfma_f32_16x16x32_bf16 v[54:57], v[148:151], v[172:175], v[54:57]
	v_mfma_f32_16x16x32_bf16 v[50:53], v[156:159], v[172:175], v[50:53]
	v_mfma_f32_16x16x32_bf16 v[38:41], v[148:151], v[180:183], v[38:41]
	v_mfma_f32_16x16x32_bf16 v[34:37], v[156:159], v[180:183], v[34:37]
	v_mfma_f32_16x16x32_bf16 v[22:25], v[148:151], v[188:191], v[22:25]
	v_mfma_f32_16x16x32_bf16 v[18:21], v[156:159], v[188:191], v[18:21]
	s_barrier
	s_add_u32 s0, s26, 0x40080
	s_addc_u32 s1, s27, 0
	s_add_i32 s26, s28, s64
	v_lshl_add_u64 v[144:145], s[0:1], 0, v[194:195]
	s_mov_b32 m0, s26
	s_nop 0
	global_load_lds_dwordx4 v[144:145], off
	v_lshl_add_u64 v[144:145], s[0:1], 0, v[130:131]
	s_add_i32 m0, s26, 0x2000
	s_nop 0
	global_load_lds_dwordx4 v[144:145], off
	v_add_u32_e32 v156, 0x10000, v141
	ds_read_b128 v[144:147], v156
	ds_read_b128 v[148:151], v156 offset:1024
	ds_read_b128 v[152:155], v156 offset:2048
	ds_read_b128 v[156:159], v156 offset:3072
	s_waitcnt vmcnt(6)
	s_barrier
	v_mfma_f32_16x16x32_bf16 v[46:49], v[198:201], v[160:163], v[46:49]
	v_mfma_f32_16x16x32_bf16 v[42:45], v[206:209], v[160:163], v[42:45]
	v_mfma_f32_16x16x32_bf16 v[30:33], v[198:201], v[168:171], v[30:33]
	v_mfma_f32_16x16x32_bf16 v[26:29], v[206:209], v[168:171], v[26:29]
	v_mfma_f32_16x16x32_bf16 v[14:17], v[198:201], v[176:179], v[14:17]
	v_mfma_f32_16x16x32_bf16 v[10:13], v[206:209], v[176:179], v[10:13]
	v_mfma_f32_16x16x32_bf16 v[6:9], v[198:201], v[184:187], v[6:9]
	v_mfma_f32_16x16x32_bf16 v[2:5], v[206:209], v[184:187], v[2:5]
	v_mfma_f32_16x16x32_bf16 v[46:49], v[202:205], v[164:167], v[46:49]
	v_mfma_f32_16x16x32_bf16 v[42:45], v[210:213], v[164:167], v[42:45]
	v_mfma_f32_16x16x32_bf16 v[30:33], v[202:205], v[172:175], v[30:33]
	v_mfma_f32_16x16x32_bf16 v[26:29], v[210:213], v[172:175], v[26:29]
	v_mfma_f32_16x16x32_bf16 v[14:17], v[202:205], v[180:183], v[14:17]
	v_mfma_f32_16x16x32_bf16 v[10:13], v[210:213], v[180:183], v[10:13]
	v_mfma_f32_16x16x32_bf16 v[6:9], v[202:205], v[188:191], v[6:9]
	v_mfma_f32_16x16x32_bf16 v[2:5], v[210:213], v[188:191], v[2:5]
	s_add_i32 s82, s82, 2
	s_add_u32 s24, s24, 0x100
	s_addc_u32 s25, s25, 0
	s_add_u32 s78, s78, 0x100
	s_addc_u32 s79, s79, 0
	s_cmp_gt_u32 s82, 13
	s_barrier
	s_cbranch_scc0 .LBB0_1765
	s_waitcnt lgkmcnt(0)
	v_lshl_add_u32 v144, s12, 8, v1
	v_lshl_or_b32 v146, s75, 8, v142
	v_ashrrev_i32_e32 v145, 31, v144
	v_lshlrev_b64 v[148:149], 11, v[144:145]
	v_ashrrev_i32_e32 v147, 31, v146
	v_lshl_add_u64 v[148:149], s[10:11], 0, v[148:149]
	v_cvt_pk_bf16_f32 v126, v126, v127
	v_cvt_pk_bf16_f32 v127, v128, v129
	v_cvt_pk_bf16_f32 v128, v122, v123
	v_lshlrev_b64 v[122:123], 1, v[146:147]
	v_cvt_pk_bf16_f32 v129, v124, v125
	v_lshl_add_u64 v[124:125], v[148:149], 0, v[122:123]
	s_mov_b64 s[0:1], 0x40000
	v_cvt_pk_bf16_f32 v62, v62, v63
	v_cvt_pk_bf16_f32 v63, v64, v65
	v_cvt_pk_bf16_f32 v64, v58, v59
	v_lshl_add_u64 v[58:59], v[124:125], 0, s[0:1]
	s_mov_b32 s0, 0x40000
	v_cvt_pk_bf16_f32 v110, v110, v111
	v_cvt_pk_bf16_f32 v111, v112, v113
	v_cvt_pk_bf16_f32 v112, v106, v107
	v_or_b32_e32 v106, 16, v144
	v_cvt_pk_bf16_f32 v65, v60, v61
	v_add_co_u32_e32 v60, vcc, s0, v124
	v_cvt_pk_bf16_f32 v46, v46, v47
	v_cvt_pk_bf16_f32 v47, v48, v49
	v_cvt_pk_bf16_f32 v48, v42, v43
	v_cvt_pk_bf16_f32 v49, v44, v45
	s_mov_b64 s[0:1], 0x48000
	v_ashrrev_i32_e32 v107, 31, v106
	v_addc_co_u32_e32 v61, vcc, 0, v125, vcc
	global_store_dwordx4 v[58:59], v[46:49], off offset:256
	v_cvt_pk_bf16_f32 v113, v108, v109
	v_lshlrev_b64 v[106:107], 11, v[106:107]
	v_lshl_add_u64 v[46:47], v[124:125], 0, s[0:1]
	s_mov_b32 s0, 0x48000
	v_cvt_pk_bf16_f32 v94, v94, v95
	v_cvt_pk_bf16_f32 v95, v96, v97
	v_cvt_pk_bf16_f32 v96, v90, v91
	v_or_b32_e32 v90, 32, v144
	v_add_co_u32_e32 v48, vcc, s0, v124
	v_cvt_pk_bf16_f32 v30, v30, v31
	v_cvt_pk_bf16_f32 v31, v32, v33
	v_cvt_pk_bf16_f32 v32, v26, v27
	v_cvt_pk_bf16_f32 v33, v28, v29
	s_mov_b64 s[0:1], 0x50000
	global_store_dwordx4 v[124:125], v[110:113], off offset:256
	v_ashrrev_i32_e32 v91, 31, v90
	v_addc_co_u32_e32 v49, vcc, 0, v125, vcc
	v_lshl_add_u64 v[110:111], s[10:11], 0, v[106:107]
	global_store_dwordx4 v[46:47], v[30:33], off offset:256
	v_lshl_add_u64 v[110:111], v[110:111], 0, v[122:123]
	v_cvt_pk_bf16_f32 v97, v92, v93
	v_lshl_add_u64 v[30:31], v[124:125], 0, s[0:1]
	s_mov_b32 s0, 0x50000
	v_lshlrev_b64 v[90:91], 11, v[90:91]
	v_cvt_pk_bf16_f32 v78, v78, v79
	v_cvt_pk_bf16_f32 v79, v80, v81
	v_cvt_pk_bf16_f32 v80, v74, v75
	v_or_b32_e32 v74, 48, v144
	v_add_co_u32_e32 v32, vcc, s0, v124
	v_cvt_pk_bf16_f32 v14, v14, v15
	v_cvt_pk_bf16_f32 v15, v16, v17
	v_cvt_pk_bf16_f32 v16, v10, v11
	v_cvt_pk_bf16_f32 v17, v12, v13
	s_mov_b64 s[0:1], 0x58000
	global_store_dwordx4 v[110:111], v[94:97], off offset:256
	v_ashrrev_i32_e32 v75, 31, v74
	v_addc_co_u32_e32 v33, vcc, 0, v125, vcc
	v_lshl_add_u64 v[94:95], s[10:11], 0, v[90:91]
	global_store_dwordx4 v[30:31], v[14:17], off offset:256
	v_lshl_add_u64 v[94:95], v[94:95], 0, v[122:123]
	v_cvt_pk_bf16_f32 v81, v76, v77
	v_lshl_add_u64 v[14:15], v[124:125], 0, s[0:1]
	s_mov_b32 s0, 0x58000
	v_lshlrev_b64 v[74:75], 11, v[74:75]
	v_add_co_u32_e32 v16, vcc, s0, v124
	global_store_dwordx4 v[94:95], v[78:81], off offset:256
	s_nop 0
	v_addc_co_u32_e32 v17, vcc, 0, v125, vcc
	v_lshl_add_u64 v[78:79], s[10:11], 0, v[74:75]
	v_cvt_pk_bf16_f32 v106, v118, v119
	v_cvt_pk_bf16_f32 v107, v120, v121
	v_cvt_pk_bf16_f32 v108, v114, v115
	v_cvt_pk_bf16_f32 v109, v116, v117
	v_cvt_pk_bf16_f32 v90, v102, v103
	v_cvt_pk_bf16_f32 v91, v104, v105
	v_cvt_pk_bf16_f32 v92, v98, v99
	v_cvt_pk_bf16_f32 v93, v100, v101
	v_cvt_pk_bf16_f32 v74, v86, v87
	v_cvt_pk_bf16_f32 v75, v88, v89
	v_cvt_pk_bf16_f32 v76, v82, v83
	v_cvt_pk_bf16_f32 v77, v84, v85
	v_lshl_add_u64 v[78:79], v[78:79], 0, v[122:123]
	v_cvt_pk_bf16_f32 v70, v70, v71
	v_cvt_pk_bf16_f32 v71, v72, v73
	v_cvt_pk_bf16_f32 v72, v66, v67
	v_cvt_pk_bf16_f32 v73, v68, v69
	v_cvt_pk_bf16_f32 v42, v54, v55
	v_cvt_pk_bf16_f32 v43, v56, v57
	v_cvt_pk_bf16_f32 v44, v50, v51
	v_cvt_pk_bf16_f32 v45, v52, v53
	v_cvt_pk_bf16_f32 v26, v38, v39
	v_cvt_pk_bf16_f32 v27, v40, v41
	v_cvt_pk_bf16_f32 v28, v34, v35
	v_cvt_pk_bf16_f32 v29, v36, v37
	v_cvt_pk_bf16_f32 v10, v22, v23
	v_cvt_pk_bf16_f32 v11, v24, v25
	v_cvt_pk_bf16_f32 v12, v18, v19
	v_cvt_pk_bf16_f32 v13, v20, v21
	v_cvt_pk_bf16_f32 v6, v6, v7
	v_cvt_pk_bf16_f32 v7, v8, v9
	v_cvt_pk_bf16_f32 v8, v2, v3
	v_cvt_pk_bf16_f32 v9, v4, v5
	s_and_b64 vcc, exec, s[4:5]
	s_mov_b32 s75, s14
	s_mov_b32 s12, s18
	s_mov_b64 s[26:27], s[22:23]
	s_mov_b64 s[24:25], s[20:21]
	global_store_dwordx4 v[124:125], v[126:129], off
	global_store_dwordx4 v[110:111], v[106:109], off
	global_store_dwordx4 v[94:95], v[90:93], off
	global_store_dwordx4 v[78:79], v[74:77], off
	global_store_dwordx4 v[78:79], v[70:73], off offset:256
	global_store_dwordx4 v[60:61], v[62:65], off
	global_store_dwordx4 v[48:49], v[42:45], off
	global_store_dwordx4 v[32:33], v[26:29], off
	global_store_dwordx4 v[16:17], v[10:13], off
	global_store_dwordx4 v[14:15], v[6:9], off offset:256
	s_cbranch_vccz .LBB0_1762
	s_waitcnt vmcnt(0)
	s_cmpk_gt_u32 s34, 0xff
	s_cbranch_scc1 .LBB0_1769
	s_barrier

.LBB0_2474:
	s_ashr_i32 s13, s12, 31
	s_lshl_b64 s[0:1], s[12:13], 21
	s_add_u32 s13, s31, s0
	s_addc_u32 s19, s34, s1
	s_ashr_i32 s15, s14, 31
	s_lshl_b64 s[0:1], s[14:15], 19
	s_add_u32 s18, s13, s0
	s_addc_u32 s19, s19, s1
	s_and_b64 s[0:1], s[22:23], exec
	s_cselect_b32 s13, s19, s21
	s_cselect_b32 s15, s18, s20
	v_mov_b32_e32 v141, v195
	v_mov_b32_e32 v143, v195
	s_add_u32 s75, s20, 0x100
	v_mov_b32_e32 v2, 0
	s_addc_u32 s76, s21, 0
	v_lshl_add_u64 v[144:145], s[6:7], 0, v[142:143]
	v_lshl_add_u64 v[146:147], s[6:7], 0, v[140:141]
	s_mov_b32 s77, -2
	s_mov_b64 s[20:21], 0
	v_mov_b32_e32 v3, v2
	v_mov_b32_e32 v4, v2
	v_mov_b32_e32 v5, v2
	v_mov_b32_e32 v6, v2
	v_mov_b32_e32 v7, v2
	v_mov_b32_e32 v8, v2
	v_mov_b32_e32 v9, v2
	v_mov_b32_e32 v10, v2
	v_mov_b32_e32 v11, v2
	v_mov_b32_e32 v12, v2
	v_mov_b32_e32 v13, v2
	v_mov_b32_e32 v14, v2
	v_mov_b32_e32 v15, v2
	v_mov_b32_e32 v16, v2
	v_mov_b32_e32 v17, v2
	v_mov_b32_e32 v34, v2
	v_mov_b32_e32 v35, v2
	v_mov_b32_e32 v36, v2
	v_mov_b32_e32 v37, v2
	v_mov_b32_e32 v38, v2
	v_mov_b32_e32 v39, v2
	v_mov_b32_e32 v40, v2
	v_mov_b32_e32 v41, v2
	v_mov_b32_e32 v42, v2
	v_mov_b32_e32 v43, v2
	v_mov_b32_e32 v44, v2
	v_mov_b32_e32 v45, v2
	v_mov_b32_e32 v46, v2
	v_mov_b32_e32 v47, v2
	v_mov_b32_e32 v48, v2
	v_mov_b32_e32 v49, v2
	v_mov_b32_e32 v18, v2
	v_mov_b32_e32 v19, v2
	v_mov_b32_e32 v20, v2
	v_mov_b32_e32 v21, v2
	v_mov_b32_e32 v22, v2
	v_mov_b32_e32 v23, v2
	v_mov_b32_e32 v24, v2
	v_mov_b32_e32 v25, v2
	v_mov_b32_e32 v26, v2
	v_mov_b32_e32 v27, v2
	v_mov_b32_e32 v28, v2
	v_mov_b32_e32 v29, v2
	v_mov_b32_e32 v30, v2
	v_mov_b32_e32 v31, v2
	v_mov_b32_e32 v32, v2
	v_mov_b32_e32 v33, v2
	v_mov_b32_e32 v50, v2
	v_mov_b32_e32 v51, v2
	v_mov_b32_e32 v52, v2
	v_mov_b32_e32 v53, v2
	v_mov_b32_e32 v54, v2
	v_mov_b32_e32 v55, v2
	v_mov_b32_e32 v56, v2
	v_mov_b32_e32 v57, v2
	v_mov_b32_e32 v58, v2
	v_mov_b32_e32 v59, v2
	v_mov_b32_e32 v60, v2
	v_mov_b32_e32 v61, v2
	v_mov_b32_e32 v62, v2
	v_mov_b32_e32 v63, v2
	v_mov_b32_e32 v64, v2
	v_mov_b32_e32 v65, v2
	v_mov_b32_e32 v66, v2
	v_mov_b32_e32 v67, v2
	v_mov_b32_e32 v68, v2
	v_mov_b32_e32 v69, v2
	v_mov_b32_e32 v70, v2
	v_mov_b32_e32 v71, v2
	v_mov_b32_e32 v72, v2
	v_mov_b32_e32 v73, v2
	v_mov_b32_e32 v74, v2
	v_mov_b32_e32 v75, v2
	v_mov_b32_e32 v76, v2
	v_mov_b32_e32 v77, v2
	v_mov_b32_e32 v78, v2
	v_mov_b32_e32 v79, v2
	v_mov_b32_e32 v80, v2
	v_mov_b32_e32 v81, v2
	v_mov_b32_e32 v98, v2
	v_mov_b32_e32 v99, v2
	v_mov_b32_e32 v100, v2
	v_mov_b32_e32 v101, v2
	v_mov_b32_e32 v102, v2
	v_mov_b32_e32 v103, v2
	v_mov_b32_e32 v104, v2
	v_mov_b32_e32 v105, v2
	v_mov_b32_e32 v106, v2
	v_mov_b32_e32 v107, v2
	v_mov_b32_e32 v108, v2
	v_mov_b32_e32 v109, v2
	v_mov_b32_e32 v110, v2
	v_mov_b32_e32 v111, v2
	v_mov_b32_e32 v112, v2
	v_mov_b32_e32 v113, v2
	v_mov_b32_e32 v82, v2
	v_mov_b32_e32 v83, v2
	v_mov_b32_e32 v84, v2
	v_mov_b32_e32 v85, v2
	v_mov_b32_e32 v86, v2
	v_mov_b32_e32 v87, v2
	v_mov_b32_e32 v88, v2
	v_mov_b32_e32 v89, v2
	v_mov_b32_e32 v90, v2
	v_mov_b32_e32 v91, v2
	v_mov_b32_e32 v92, v2
	v_mov_b32_e32 v93, v2
	v_mov_b32_e32 v94, v2
	v_mov_b32_e32 v95, v2
	v_mov_b32_e32 v96, v2
	v_mov_b32_e32 v97, v2
	v_mov_b32_e32 v114, v2
	v_mov_b32_e32 v115, v2
	v_mov_b32_e32 v116, v2
	v_mov_b32_e32 v117, v2
	v_mov_b32_e32 v118, v2
	v_mov_b32_e32 v119, v2
	v_mov_b32_e32 v120, v2
	v_mov_b32_e32 v121, v2
	v_mov_b32_e32 v122, v2
	v_mov_b32_e32 v123, v2
	v_mov_b32_e32 v124, v2
	v_mov_b32_e32 v125, v2
	v_mov_b32_e32 v126, v2
	v_mov_b32_e32 v127, v2
	v_mov_b32_e32 v128, v2
	v_mov_b32_e32 v129, v2
	v_add_u32_e32 v172, 0x10000, v139
	ds_read_b128 v[160:163], v172
	ds_read_b128 v[164:167], v172 offset:1024
	ds_read_b128 v[168:171], v172 offset:2048
	ds_read_b128 v[172:175], v172 offset:3072
.LBB0_2475:
	s_add_u32 s22, s20, 0x100
	s_addc_u32 s23, s21, 0
	s_add_u32 s24, s75, s20
	s_addc_u32 s25, s76, s21
	s_cmpk_eq_i32 s20, 0x700
	s_cselect_b64 vcc, -1, 0
	s_and_b64 s[0:1], vcc, exec
	s_cselect_b32 s0, 0, s22
	s_cselect_b32 s25, s13, s25
	s_cselect_b32 s24, s15, s24
	s_add_i32 s1, 0, 0x10000
	s_add_u32 s26, s4, s0
	v_cndmask_b32_e32 v194, v136, v155, vcc
	v_cndmask_b32_e32 v192, v138, v156, vcc
	v_cndmask_b32_e32 v141, v140, v157, vcc
	v_cndmask_b32_e32 v143, v142, v158, vcc
	s_addc_u32 s27, s5, 0
	v_lshl_add_u64 v[214:215], v[146:147], 0, s[20:21]
	s_add_i32 m0, s38, 0xc000
	ds_read_b128 v[176:179], v154
	ds_read_b128 v[180:183], v154 offset:1024
	ds_read_b128 v[184:187], v154 offset:2048
	ds_read_b128 v[188:191], v154 offset:3072
	ds_read_b128 v[198:201], v154 offset:4096
	ds_read_b128 v[202:205], v154 offset:5120
	ds_read_b128 v[206:209], v154 offset:6144
	ds_read_b128 v[210:213], v154 offset:7168
	global_load_lds_dwordx4 v[214:215], off
	v_lshl_add_u64 v[214:215], v[144:145], 0, s[20:21]
	s_add_i32 m0, s38, 0xe000
	s_nop 0
	global_load_lds_dwordx4 v[214:215], off
	s_waitcnt lgkmcnt(8)
	s_barrier
	s_waitcnt lgkmcnt(0)
	s_waitcnt lgkmcnt(0)
	v_mfma_f32_16x16x32_bf16 v[126:129], v[160:163], v[176:179], v[126:129]
	v_mfma_f32_16x16x32_bf16 v[122:125], v[168:171], v[176:179], v[122:125]
	v_mfma_f32_16x16x32_bf16 v[118:121], v[160:163], v[184:187], v[118:121]
	v_mfma_f32_16x16x32_bf16 v[114:117], v[168:171], v[184:187], v[114:117]
	v_mfma_f32_16x16x32_bf16 v[94:97], v[160:163], v[198:201], v[94:97]
	v_mfma_f32_16x16x32_bf16 v[90:93], v[168:171], v[198:201], v[90:93]
	v_mfma_f32_16x16x32_bf16 v[86:89], v[160:163], v[206:209], v[86:89]
	v_mfma_f32_16x16x32_bf16 v[82:85], v[168:171], v[206:209], v[82:85]
	v_mfma_f32_16x16x32_bf16 v[126:129], v[164:167], v[180:183], v[126:129]
	v_mfma_f32_16x16x32_bf16 v[122:125], v[172:175], v[180:183], v[122:125]
	v_mfma_f32_16x16x32_bf16 v[118:121], v[164:167], v[188:191], v[118:121]
	v_mfma_f32_16x16x32_bf16 v[114:117], v[172:175], v[188:191], v[114:117]
	v_mfma_f32_16x16x32_bf16 v[94:97], v[164:167], v[202:205], v[94:97]
	v_mfma_f32_16x16x32_bf16 v[90:93], v[172:175], v[202:205], v[90:93]
	v_mfma_f32_16x16x32_bf16 v[86:89], v[164:167], v[210:213], v[86:89]
	v_mfma_f32_16x16x32_bf16 v[82:85], v[172:175], v[210:213], v[82:85]
	s_barrier
	s_add_i32 s20, 0, 0x14000
	s_add_i32 s0, s1, s35
	v_add_u32_e32 v159, s20, v139
	v_lshl_add_u64 v[224:225], s[24:25], 0, v[130:131]
	s_mov_b32 m0, s0
	ds_read_b128 v[214:217], v159
	ds_read_b128 v[218:221], v159 offset:1024
	ds_read_b128 v[238:241], v159 offset:2048
	ds_read_b128 v[242:245], v159 offset:3072
	global_load_lds_dwordx4 v[224:225], off
	v_lshl_add_u64 v[230:231], s[24:25], 0, v[132:133]
	s_add_i32 m0, s0, 0x2000
	s_nop 0
	global_load_lds_dwordx4 v[230:231], off
	s_barrier
	s_waitcnt lgkmcnt(0)
	s_waitcnt lgkmcnt(0)
	v_mfma_f32_16x16x32_bf16 v[110:113], v[214:217], v[176:179], v[110:113]
	v_mfma_f32_16x16x32_bf16 v[106:109], v[238:241], v[176:179], v[106:109]
	v_mfma_f32_16x16x32_bf16 v[102:105], v[214:217], v[184:187], v[102:105]
	v_mfma_f32_16x16x32_bf16 v[98:101], v[238:241], v[184:187], v[98:101]
	v_mfma_f32_16x16x32_bf16 v[78:81], v[214:217], v[198:201], v[78:81]
	v_mfma_f32_16x16x32_bf16 v[74:77], v[238:241], v[198:201], v[74:77]
	v_mfma_f32_16x16x32_bf16 v[70:73], v[214:217], v[206:209], v[70:73]
	v_mfma_f32_16x16x32_bf16 v[66:69], v[238:241], v[206:209], v[66:69]
	v_mfma_f32_16x16x32_bf16 v[110:113], v[218:221], v[180:183], v[110:113]
	v_mfma_f32_16x16x32_bf16 v[106:109], v[242:245], v[180:183], v[106:109]
	v_mfma_f32_16x16x32_bf16 v[102:105], v[218:221], v[188:191], v[102:105]
	v_mfma_f32_16x16x32_bf16 v[98:101], v[242:245], v[188:191], v[98:101]
	v_mfma_f32_16x16x32_bf16 v[78:81], v[218:221], v[202:205], v[78:81]
	v_mfma_f32_16x16x32_bf16 v[74:77], v[242:245], v[202:205], v[74:77]
	v_mfma_f32_16x16x32_bf16 v[70:73], v[218:221], v[210:213], v[70:73]
	v_mfma_f32_16x16x32_bf16 v[66:69], v[242:245], v[210:213], v[66:69]
	s_mov_b32 m0, s38
	s_barrier
	ds_read_b128 v[176:179], v154 offset:16384
	ds_read_b128 v[180:183], v154 offset:17408
	ds_read_b128 v[184:187], v154 offset:18432
	ds_read_b128 v[188:191], v154 offset:19456
	ds_read_b128 v[198:201], v154 offset:20480
	ds_read_b128 v[202:205], v154 offset:21504
	ds_read_b128 v[206:209], v154 offset:22528
	ds_read_b128 v[210:213], v154 offset:23552
	global_load_lds_dwordx4 v194, s[26:27]
	s_mov_b32 m0, s40
	v_mov_b32_e32 v193, v195
	global_load_lds_dwordx4 v192, s[26:27]
	s_waitcnt vmcnt(10)
	s_barrier
	s_waitcnt lgkmcnt(0)
	v_lshl_add_u64 v[232:233], s[26:27], 0, v[194:195]
	v_lshl_add_u64 v[192:193], s[26:27], 0, v[192:193]
	s_waitcnt lgkmcnt(0)
	v_mfma_f32_16x16x32_bf16 v[62:65], v[160:163], v[176:179], v[62:65]
	v_mfma_f32_16x16x32_bf16 v[58:61], v[168:171], v[176:179], v[58:61]
	v_mfma_f32_16x16x32_bf16 v[54:57], v[160:163], v[184:187], v[54:57]
	v_mfma_f32_16x16x32_bf16 v[50:53], v[168:171], v[184:187], v[50:53]
	v_mfma_f32_16x16x32_bf16 v[30:33], v[160:163], v[198:201], v[30:33]
	v_mfma_f32_16x16x32_bf16 v[26:29], v[168:171], v[198:201], v[26:29]
	v_mfma_f32_16x16x32_bf16 v[22:25], v[160:163], v[206:209], v[22:25]
	v_mfma_f32_16x16x32_bf16 v[18:21], v[168:171], v[206:209], v[18:21]
	v_mfma_f32_16x16x32_bf16 v[62:65], v[164:167], v[180:183], v[62:65]
	v_mfma_f32_16x16x32_bf16 v[58:61], v[172:175], v[180:183], v[58:61]
	v_mfma_f32_16x16x32_bf16 v[54:57], v[164:167], v[188:191], v[54:57]
	v_mfma_f32_16x16x32_bf16 v[50:53], v[172:175], v[188:191], v[50:53]
	v_mfma_f32_16x16x32_bf16 v[30:33], v[164:167], v[202:205], v[30:33]
	v_mfma_f32_16x16x32_bf16 v[26:29], v[172:175], v[202:205], v[26:29]
	v_mfma_f32_16x16x32_bf16 v[22:25], v[164:167], v[210:213], v[22:25]
	v_mfma_f32_16x16x32_bf16 v[18:21], v[172:175], v[210:213], v[18:21]
	s_barrier
	s_add_u32 s0, s24, 0x40000
	s_addc_u32 s1, s25, 0
	s_add_i32 s20, s20, s35
	v_lshl_add_u64 v[160:161], s[0:1], 0, v[130:131]
	s_mov_b32 m0, s20
	s_nop 0
	global_load_lds_dwordx4 v[160:161], off
	v_lshl_add_u64 v[160:161], s[0:1], 0, v[132:133]
	s_add_i32 m0, s20, 0x2000
	s_nop 0
	global_load_lds_dwordx4 v[160:161], off
	v_add_u32_e32 v172, 0x18000, v139
	ds_read_b128 v[160:163], v172
	ds_read_b128 v[164:167], v172 offset:1024
	ds_read_b128 v[168:171], v172 offset:2048
	ds_read_b128 v[172:175], v172 offset:3072
	s_waitcnt vmcnt(6)
	s_barrier
	v_mfma_f32_16x16x32_bf16 v[46:49], v[214:217], v[176:179], v[46:49]
	v_mfma_f32_16x16x32_bf16 v[42:45], v[238:241], v[176:179], v[42:45]
	v_mfma_f32_16x16x32_bf16 v[38:41], v[214:217], v[184:187], v[38:41]
	v_mfma_f32_16x16x32_bf16 v[34:37], v[238:241], v[184:187], v[34:37]
	v_mfma_f32_16x16x32_bf16 v[14:17], v[214:217], v[198:201], v[14:17]
	v_mfma_f32_16x16x32_bf16 v[10:13], v[238:241], v[198:201], v[10:13]
	v_mfma_f32_16x16x32_bf16 v[6:9], v[214:217], v[206:209], v[6:9]
	v_mfma_f32_16x16x32_bf16 v[2:5], v[238:241], v[206:209], v[2:5]
	v_mfma_f32_16x16x32_bf16 v[46:49], v[218:221], v[180:183], v[46:49]
	v_mfma_f32_16x16x32_bf16 v[42:45], v[242:245], v[180:183], v[42:45]
	v_mfma_f32_16x16x32_bf16 v[38:41], v[218:221], v[188:191], v[38:41]
	v_mfma_f32_16x16x32_bf16 v[34:37], v[242:245], v[188:191], v[34:37]
	v_mfma_f32_16x16x32_bf16 v[14:17], v[218:221], v[202:205], v[14:17]
	v_mfma_f32_16x16x32_bf16 v[10:13], v[242:245], v[202:205], v[10:13]
	v_mfma_f32_16x16x32_bf16 v[6:9], v[218:221], v[210:213], v[6:9]
	v_mfma_f32_16x16x32_bf16 v[2:5], v[242:245], v[210:213], v[2:5]
	s_add_i32 s0, 0, 0x18000
	s_barrier
	s_mov_b32 m0, s43
	ds_read_b128 v[176:179], v154 offset:32768
	ds_read_b128 v[180:183], v154 offset:33792
	ds_read_b128 v[184:187], v154 offset:34816
	ds_read_b128 v[188:191], v154 offset:35840
	ds_read_b128 v[198:201], v154 offset:36864
	ds_read_b128 v[202:205], v154 offset:37888
	ds_read_b128 v[206:209], v154 offset:38912
	ds_read_b128 v[210:213], v154 offset:39936
	global_load_lds_dwordx4 v141, s[26:27]
	s_mov_b32 m0, s64
	s_nop 0
	global_load_lds_dwordx4 v143, s[26:27]
	s_waitcnt lgkmcnt(8)
	s_barrier
	s_waitcnt lgkmcnt(0)
	s_waitcnt lgkmcnt(0)
	v_mfma_f32_16x16x32_bf16 v[126:129], v[160:163], v[176:179], v[126:129]
	v_mfma_f32_16x16x32_bf16 v[122:125], v[168:171], v[176:179], v[122:125]
	v_mfma_f32_16x16x32_bf16 v[118:121], v[160:163], v[184:187], v[118:121]
	v_mfma_f32_16x16x32_bf16 v[114:117], v[168:171], v[184:187], v[114:117]
	v_mfma_f32_16x16x32_bf16 v[94:97], v[160:163], v[198:201], v[94:97]
	v_mfma_f32_16x16x32_bf16 v[90:93], v[168:171], v[198:201], v[90:93]
	v_mfma_f32_16x16x32_bf16 v[86:89], v[160:163], v[206:209], v[86:89]
	v_mfma_f32_16x16x32_bf16 v[82:85], v[168:171], v[206:209], v[82:85]
	v_mfma_f32_16x16x32_bf16 v[126:129], v[164:167], v[180:183], v[126:129]
	v_mfma_f32_16x16x32_bf16 v[122:125], v[172:175], v[180:183], v[122:125]
	v_mfma_f32_16x16x32_bf16 v[118:121], v[164:167], v[188:191], v[118:121]
	v_mfma_f32_16x16x32_bf16 v[114:117], v[172:175], v[188:191], v[114:117]
	v_mfma_f32_16x16x32_bf16 v[94:97], v[164:167], v[202:205], v[94:97]
	v_mfma_f32_16x16x32_bf16 v[90:93], v[172:175], v[202:205], v[90:93]
	v_mfma_f32_16x16x32_bf16 v[86:89], v[164:167], v[210:213], v[86:89]
	v_mfma_f32_16x16x32_bf16 v[82:85], v[172:175], v[210:213], v[82:85]
	s_barrier
	s_add_i32 s20, 0, 0x1c000
	s_add_i32 s0, s0, s35
	v_add_u32_e32 v141, s20, v139
	v_lshl_add_u64 v[224:225], v[224:225], 0, s[54:55]
	s_mov_b32 m0, s0
	ds_read_b128 v[214:217], v141
	ds_read_b128 v[218:221], v141 offset:1024
	ds_read_b128 v[238:241], v141 offset:2048
	ds_read_b128 v[242:245], v141 offset:3072
	global_load_lds_dwordx4 v[224:225], off
	v_lshl_add_u64 v[224:225], v[230:231], 0, s[54:55]
	s_add_i32 m0, s0, 0x2000
	s_nop 0
	global_load_lds_dwordx4 v[224:225], off
	s_barrier
	s_waitcnt lgkmcnt(0)
	s_waitcnt lgkmcnt(0)
	v_mfma_f32_16x16x32_bf16 v[110:113], v[214:217], v[176:179], v[110:113]
	v_mfma_f32_16x16x32_bf16 v[106:109], v[238:241], v[176:179], v[106:109]
	v_mfma_f32_16x16x32_bf16 v[102:105], v[214:217], v[184:187], v[102:105]
	v_mfma_f32_16x16x32_bf16 v[98:101], v[238:241], v[184:187], v[98:101]
	v_mfma_f32_16x16x32_bf16 v[78:81], v[214:217], v[198:201], v[78:81]
	v_mfma_f32_16x16x32_bf16 v[74:77], v[238:241], v[198:201], v[74:77]
	v_mfma_f32_16x16x32_bf16 v[70:73], v[214:217], v[206:209], v[70:73]
	v_mfma_f32_16x16x32_bf16 v[66:69], v[238:241], v[206:209], v[66:69]
	v_mfma_f32_16x16x32_bf16 v[110:113], v[218:221], v[180:183], v[110:113]
	v_mfma_f32_16x16x32_bf16 v[106:109], v[242:245], v[180:183], v[106:109]
	v_mfma_f32_16x16x32_bf16 v[102:105], v[218:221], v[188:191], v[102:105]
	v_mfma_f32_16x16x32_bf16 v[98:101], v[242:245], v[188:191], v[98:101]
	v_mfma_f32_16x16x32_bf16 v[78:81], v[218:221], v[202:205], v[78:81]
	v_mfma_f32_16x16x32_bf16 v[74:77], v[242:245], v[202:205], v[74:77]
	v_mfma_f32_16x16x32_bf16 v[70:73], v[218:221], v[210:213], v[70:73]
	v_mfma_f32_16x16x32_bf16 v[66:69], v[242:245], v[210:213], v[66:69]
	s_mov_b32 m0, s65
	v_lshl_add_u64 v[224:225], v[232:233], 0, s[54:55]
	s_barrier
	ds_read_b128 v[176:179], v154 offset:49152
	ds_read_b128 v[180:183], v154 offset:50176
	ds_read_b128 v[184:187], v154 offset:51200
	ds_read_b128 v[188:191], v154 offset:52224
	ds_read_b128 v[198:201], v154 offset:53248
	ds_read_b128 v[202:205], v154 offset:54272
	ds_read_b128 v[206:209], v154 offset:55296
	ds_read_b128 v[210:213], v154 offset:56320
	global_load_lds_dwordx4 v[224:225], off
	v_lshl_add_u64 v[192:193], v[192:193], 0, s[54:55]
	s_mov_b32 m0, s66
	s_nop 0
	global_load_lds_dwordx4 v[192:193], off
	s_waitcnt vmcnt(10)
	s_barrier
	s_waitcnt lgkmcnt(0)
	s_waitcnt lgkmcnt(0)
	v_mfma_f32_16x16x32_bf16 v[62:65], v[160:163], v[176:179], v[62:65]
	v_mfma_f32_16x16x32_bf16 v[58:61], v[168:171], v[176:179], v[58:61]
	v_mfma_f32_16x16x32_bf16 v[54:57], v[160:163], v[184:187], v[54:57]
	v_mfma_f32_16x16x32_bf16 v[50:53], v[168:171], v[184:187], v[50:53]
	v_mfma_f32_16x16x32_bf16 v[30:33], v[160:163], v[198:201], v[30:33]
	v_mfma_f32_16x16x32_bf16 v[26:29], v[168:171], v[198:201], v[26:29]
	v_mfma_f32_16x16x32_bf16 v[22:25], v[160:163], v[206:209], v[22:25]
	v_mfma_f32_16x16x32_bf16 v[18:21], v[168:171], v[206:209], v[18:21]
	v_mfma_f32_16x16x32_bf16 v[62:65], v[164:167], v[180:183], v[62:65]
	v_mfma_f32_16x16x32_bf16 v[58:61], v[172:175], v[180:183], v[58:61]
	v_mfma_f32_16x16x32_bf16 v[54:57], v[164:167], v[188:191], v[54:57]
	v_mfma_f32_16x16x32_bf16 v[50:53], v[172:175], v[188:191], v[50:53]
	v_mfma_f32_16x16x32_bf16 v[30:33], v[164:167], v[202:205], v[30:33]
	v_mfma_f32_16x16x32_bf16 v[26:29], v[172:175], v[202:205], v[26:29]
	v_mfma_f32_16x16x32_bf16 v[22:25], v[164:167], v[210:213], v[22:25]
	v_mfma_f32_16x16x32_bf16 v[18:21], v[172:175], v[210:213], v[18:21]
	s_barrier
	s_add_u32 s0, s24, 0x40080
	s_addc_u32 s1, s25, 0
	s_add_i32 s20, s20, s35
	v_lshl_add_u64 v[160:161], s[0:1], 0, v[130:131]
	s_mov_b32 m0, s20
	s_nop 0
	global_load_lds_dwordx4 v[160:161], off
	v_lshl_add_u64 v[160:161], s[0:1], 0, v[132:133]
	s_add_i32 m0, s20, 0x2000
	s_nop 0
	global_load_lds_dwordx4 v[160:161], off
	v_add_u32_e32 v172, 0x10000, v139
	ds_read_b128 v[160:163], v172
	ds_read_b128 v[164:167], v172 offset:1024
	ds_read_b128 v[168:171], v172 offset:2048
	ds_read_b128 v[172:175], v172 offset:3072
	s_waitcnt vmcnt(6)
	s_barrier
	v_mfma_f32_16x16x32_bf16 v[46:49], v[214:217], v[176:179], v[46:49]
	v_mfma_f32_16x16x32_bf16 v[42:45], v[238:241], v[176:179], v[42:45]
	v_mfma_f32_16x16x32_bf16 v[38:41], v[214:217], v[184:187], v[38:41]
	v_mfma_f32_16x16x32_bf16 v[34:37], v[238:241], v[184:187], v[34:37]
	v_mfma_f32_16x16x32_bf16 v[14:17], v[214:217], v[198:201], v[14:17]
	v_mfma_f32_16x16x32_bf16 v[10:13], v[238:241], v[198:201], v[10:13]
	v_mfma_f32_16x16x32_bf16 v[6:9], v[214:217], v[206:209], v[6:9]
	v_mfma_f32_16x16x32_bf16 v[2:5], v[238:241], v[206:209], v[2:5]
	v_mfma_f32_16x16x32_bf16 v[46:49], v[218:221], v[180:183], v[46:49]
	v_mfma_f32_16x16x32_bf16 v[42:45], v[242:245], v[180:183], v[42:45]
	v_mfma_f32_16x16x32_bf16 v[38:41], v[218:221], v[188:191], v[38:41]
	v_mfma_f32_16x16x32_bf16 v[34:37], v[242:245], v[188:191], v[34:37]
	v_mfma_f32_16x16x32_bf16 v[14:17], v[218:221], v[202:205], v[14:17]
	v_mfma_f32_16x16x32_bf16 v[10:13], v[242:245], v[202:205], v[10:13]
	v_mfma_f32_16x16x32_bf16 v[6:9], v[218:221], v[210:213], v[6:9]
	v_mfma_f32_16x16x32_bf16 v[2:5], v[242:245], v[210:213], v[2:5]
	s_add_i32 s77, s77, 2
	s_cmp_gt_u32 s77, 13
	s_mov_b64 s[20:21], s[22:23]
	s_barrier
	s_cbranch_scc0 .LBB0_2475
	s_waitcnt lgkmcnt(0)
	v_mul_f32_e32 v142, 0xbfb8aa3b, v126
	v_mul_f32_e32 v143, 0xbfb8aa3b, v127
	v_exp_f32_e32 v142, v142
	v_exp_f32_e32 v143, v143
	v_lshl_add_u32 v136, s73, 8, v137
	v_lshl_or_b32 v138, s74, 8, v153
	v_add_f32_e32 v142, 1.0, v142
	v_add_f32_e32 v143, 1.0, v143
	v_rcp_f32_e32 v142, v142
	v_rcp_f32_e32 v143, v143
	v_or_b32_e32 v140, v136, v151
	v_ashrrev_i32_e32 v141, 31, v140
	v_lshlrev_b64 v[140:141], 10, v[140:141]
	v_pk_mul_f32 v[126:127], v[126:127], v[142:143]
	v_lshl_add_u64 v[140:141], v[134:135], 0, v[140:141]
	v_pk_mul_f32 v[122:123], v[122:123], v[126:127]
	s_and_b64 vcc, exec, s[16:17]
	v_cvt_pk_bf16_f32 v122, v122, v123
	v_mul_f32_e32 v123, 0xbfb8aa3b, v128
	v_exp_f32_e32 v123, v123
	v_mov_b32_e32 v142, v158
	s_mov_b32 s74, s14
	s_mov_b32 s73, s72
	v_add_f32_e32 v123, 1.0, v123
	v_rcp_f32_e32 v126, v123
	v_mul_f32_e32 v123, 0xbfb8aa3b, v129
	v_exp_f32_e32 v123, v123
	s_mov_b64 s[20:21], s[18:19]
	v_add_f32_e32 v123, 1.0, v123
	v_rcp_f32_e32 v127, v123
	s_nop 0
	v_pk_mul_f32 v[126:127], v[128:129], v[126:127]
	s_nop 0
	v_pk_mul_f32 v[124:125], v[124:125], v[126:127]
	s_nop 0
	v_cvt_pk_bf16_f32 v123, v124, v125
	v_mul_f32_e32 v124, 0xbfb8aa3b, v118
	v_mul_f32_e32 v125, 0xbfb8aa3b, v119
	v_exp_f32_e32 v124, v124
	v_exp_f32_e32 v125, v125
	v_add_f32_e32 v124, 1.0, v124
	v_add_f32_e32 v125, 1.0, v125
	v_rcp_f32_e32 v124, v124
	v_rcp_f32_e32 v125, v125
	s_nop 0
	v_pk_mul_f32 v[118:119], v[118:119], v[124:125]
	s_nop 0
	v_pk_mul_f32 v[114:115], v[114:115], v[118:119]
	v_mul_f32_e32 v118, 0xbfb8aa3b, v110
	v_mul_f32_e32 v119, 0xbfb8aa3b, v111
	v_exp_f32_e32 v118, v118
	v_exp_f32_e32 v119, v119
	v_cvt_pk_bf16_f32 v124, v114, v115
	v_mul_f32_e32 v114, 0xbfb8aa3b, v120
	v_add_f32_e32 v118, 1.0, v118
	v_add_f32_e32 v119, 1.0, v119
	v_rcp_f32_e32 v118, v118
	v_rcp_f32_e32 v119, v119
	v_mul_f32_e32 v115, 0xbfb8aa3b, v121
	v_exp_f32_e32 v114, v114
	v_exp_f32_e32 v115, v115
	v_pk_mul_f32 v[110:111], v[110:111], v[118:119]
	v_permlane16_swap_b32_e32 v122, v124
	v_pk_mul_f32 v[106:107], v[106:107], v[110:111]
	v_add_f32_e32 v114, 1.0, v114
	v_cvt_pk_bf16_f32 v106, v106, v107
	v_mul_f32_e32 v107, 0xbfb8aa3b, v112
	v_exp_f32_e32 v107, v107
	v_add_f32_e32 v115, 1.0, v115
	v_rcp_f32_e32 v114, v114
	v_rcp_f32_e32 v115, v115
	v_add_f32_e32 v107, 1.0, v107
	v_rcp_f32_e32 v110, v107
	v_mul_f32_e32 v107, 0xbfb8aa3b, v113
	v_exp_f32_e32 v107, v107
	v_pk_mul_f32 v[114:115], v[120:121], v[114:115]
	v_add_f32_e32 v107, 1.0, v107
	v_rcp_f32_e32 v111, v107
	v_pk_mul_f32 v[114:115], v[116:117], v[114:115]
	v_pk_mul_f32 v[110:111], v[112:113], v[110:111]
	s_nop 0
	v_pk_mul_f32 v[108:109], v[108:109], v[110:111]
	v_cvt_pk_bf16_f32 v125, v114, v115
	v_cvt_pk_bf16_f32 v107, v108, v109
	v_mul_f32_e32 v108, 0xbfb8aa3b, v102
	v_mul_f32_e32 v109, 0xbfb8aa3b, v103
	v_exp_f32_e32 v108, v108
	v_exp_f32_e32 v109, v109
	v_ashrrev_i32_e32 v114, 1, v138
	v_ashrrev_i32_e32 v115, 31, v114
	v_add_f32_e32 v108, 1.0, v108
	v_add_f32_e32 v109, 1.0, v109
	v_rcp_f32_e32 v108, v108
	v_rcp_f32_e32 v109, v109
	v_lshlrev_b64 v[114:115], 1, v[114:115]
	v_permlane16_swap_b32_e32 v123, v125
	v_pk_mul_f32 v[102:103], v[102:103], v[108:109]
	v_lshl_add_u64 v[116:117], v[140:141], 0, v[114:115]
	v_pk_mul_f32 v[98:99], v[98:99], v[102:103]
	v_mov_b32_e32 v138, v156
	v_cvt_pk_bf16_f32 v108, v98, v99
	v_mul_f32_e32 v98, 0xbfb8aa3b, v104
	v_mul_f32_e32 v99, 0xbfb8aa3b, v105
	v_exp_f32_e32 v98, v98
	v_exp_f32_e32 v99, v99
	v_permlane16_swap_b32_e32 v106, v108
	v_add_f32_e32 v98, 1.0, v98
	v_add_f32_e32 v99, 1.0, v99
	v_rcp_f32_e32 v98, v98
	v_rcp_f32_e32 v99, v99
	v_mov_b32_e32 v140, v157
	global_store_dwordx4 v[116:117], v[122:125], off
	v_pk_mul_f32 v[98:99], v[104:105], v[98:99]
	s_nop 0
	v_pk_mul_f32 v[98:99], v[100:101], v[98:99]
	v_mul_f32_e32 v100, 0xbfb8aa3b, v94
	v_mul_f32_e32 v101, 0xbfb8aa3b, v95
	v_exp_f32_e32 v100, v100
	v_exp_f32_e32 v101, v101
	v_cvt_pk_bf16_f32 v109, v98, v99
	v_or_b32_e32 v98, v136, v152
	v_add_f32_e32 v100, 1.0, v100
	v_add_f32_e32 v101, 1.0, v101
	v_rcp_f32_e32 v100, v100
	v_rcp_f32_e32 v101, v101
	v_ashrrev_i32_e32 v99, 31, v98
	v_lshlrev_b64 v[98:99], 10, v[98:99]
	v_lshl_add_u64 v[98:99], v[134:135], 0, v[98:99]
	v_pk_mul_f32 v[94:95], v[94:95], v[100:101]
	v_permlane16_swap_b32_e32 v107, v109
	v_pk_mul_f32 v[90:91], v[90:91], v[94:95]
	global_store_dwordx4 v[116:117], v[106:109], off offset:128
	v_cvt_pk_bf16_f32 v90, v90, v91
	v_mul_f32_e32 v91, 0xbfb8aa3b, v96
	v_exp_f32_e32 v91, v91
	s_nop 0
	v_add_f32_e32 v91, 1.0, v91
	v_rcp_f32_e32 v94, v91
	v_mul_f32_e32 v91, 0xbfb8aa3b, v97
	v_exp_f32_e32 v91, v91
	s_nop 0
	v_add_f32_e32 v91, 1.0, v91
	v_rcp_f32_e32 v95, v91
	s_nop 0
	v_pk_mul_f32 v[94:95], v[96:97], v[94:95]
	s_nop 0
	v_pk_mul_f32 v[92:93], v[92:93], v[94:95]
	s_nop 0
	v_cvt_pk_bf16_f32 v91, v92, v93
	v_mul_f32_e32 v92, 0xbfb8aa3b, v86
	v_mul_f32_e32 v93, 0xbfb8aa3b, v87
	v_exp_f32_e32 v92, v92
	v_exp_f32_e32 v93, v93
	v_add_f32_e32 v92, 1.0, v92
	v_add_f32_e32 v93, 1.0, v93
	v_rcp_f32_e32 v92, v92
	v_rcp_f32_e32 v93, v93
	s_nop 0
	v_pk_mul_f32 v[86:87], v[86:87], v[92:93]
	s_nop 0
	v_pk_mul_f32 v[82:83], v[82:83], v[86:87]
	s_nop 0
	v_cvt_pk_bf16_f32 v92, v82, v83
	v_mul_f32_e32 v82, 0xbfb8aa3b, v88
	v_mul_f32_e32 v83, 0xbfb8aa3b, v89
	v_exp_f32_e32 v82, v82
	v_exp_f32_e32 v83, v83
	v_permlane16_swap_b32_e32 v90, v92
	v_add_f32_e32 v82, 1.0, v82
	v_add_f32_e32 v83, 1.0, v83
	v_rcp_f32_e32 v82, v82
	v_rcp_f32_e32 v83, v83
	s_nop 0
	v_pk_mul_f32 v[82:83], v[88:89], v[82:83]
	s_nop 0
	v_pk_mul_f32 v[82:83], v[84:85], v[82:83]
	v_mul_f32_e32 v84, 0xbfb8aa3b, v78
	v_mul_f32_e32 v85, 0xbfb8aa3b, v79
	v_exp_f32_e32 v84, v84
	v_exp_f32_e32 v85, v85
	v_cvt_pk_bf16_f32 v93, v82, v83
	s_nop 1
	v_permlane16_swap_b32_e32 v91, v93
	v_add_f32_e32 v84, 1.0, v84
	v_add_f32_e32 v85, 1.0, v85
	v_rcp_f32_e32 v84, v84
	v_rcp_f32_e32 v85, v85
	v_lshl_add_u64 v[82:83], v[98:99], 0, v[114:115]
	global_store_dwordx4 v[82:83], v[90:93], off
	v_pk_mul_f32 v[78:79], v[78:79], v[84:85]
	s_nop 0
	v_pk_mul_f32 v[74:75], v[74:75], v[78:79]
	s_nop 0
	v_cvt_pk_bf16_f32 v74, v74, v75
	v_mul_f32_e32 v75, 0xbfb8aa3b, v80
	v_exp_f32_e32 v75, v75
	s_nop 0
	v_add_f32_e32 v75, 1.0, v75
	v_rcp_f32_e32 v78, v75
	v_mul_f32_e32 v75, 0xbfb8aa3b, v81
	v_exp_f32_e32 v75, v75
	s_nop 0
	v_add_f32_e32 v75, 1.0, v75
	v_rcp_f32_e32 v79, v75
	s_nop 0
	v_pk_mul_f32 v[78:79], v[80:81], v[78:79]
	s_nop 0
	v_pk_mul_f32 v[76:77], v[76:77], v[78:79]
	s_nop 0
	v_cvt_pk_bf16_f32 v75, v76, v77
	v_mul_f32_e32 v76, 0xbfb8aa3b, v70
	v_mul_f32_e32 v77, 0xbfb8aa3b, v71
	v_exp_f32_e32 v76, v76
	v_exp_f32_e32 v77, v77
	v_add_f32_e32 v76, 1.0, v76
	v_add_f32_e32 v77, 1.0, v77
	v_rcp_f32_e32 v76, v76
	v_rcp_f32_e32 v77, v77
	s_nop 0
	v_pk_mul_f32 v[70:71], v[70:71], v[76:77]
	s_nop 0
	v_pk_mul_f32 v[66:67], v[66:67], v[70:71]
	v_add_u32_e32 v70, 0x80, v136
	v_cvt_pk_bf16_f32 v76, v66, v67
	v_mul_f32_e32 v66, 0xbfb8aa3b, v72
	v_mul_f32_e32 v67, 0xbfb8aa3b, v73
	v_exp_f32_e32 v66, v66
	v_exp_f32_e32 v67, v67
	v_permlane16_swap_b32_e32 v74, v76
	v_add_f32_e32 v66, 1.0, v66
	v_add_f32_e32 v67, 1.0, v67
	v_rcp_f32_e32 v66, v66
	v_rcp_f32_e32 v67, v67
	v_mov_b32_e32 v136, v155
	v_pk_mul_f32 v[66:67], v[72:73], v[66:67]
	s_nop 0
	v_pk_mul_f32 v[66:67], v[68:69], v[66:67]
	v_mul_f32_e32 v68, 0xbfb8aa3b, v62
	v_mul_f32_e32 v69, 0xbfb8aa3b, v63
	v_exp_f32_e32 v68, v68
	v_exp_f32_e32 v69, v69
	v_cvt_pk_bf16_f32 v77, v66, v67
	v_or_b32_e32 v66, v70, v151
	v_add_f32_e32 v68, 1.0, v68
	v_add_f32_e32 v69, 1.0, v69
	v_rcp_f32_e32 v68, v68
	v_rcp_f32_e32 v69, v69
	v_ashrrev_i32_e32 v67, 31, v66
	v_lshlrev_b64 v[66:67], 10, v[66:67]
	v_lshl_add_u64 v[66:67], v[134:135], 0, v[66:67]
	v_pk_mul_f32 v[62:63], v[62:63], v[68:69]
	v_permlane16_swap_b32_e32 v75, v77
	v_pk_mul_f32 v[58:59], v[58:59], v[62:63]
	global_store_dwordx4 v[82:83], v[74:77], off offset:128
	v_cvt_pk_bf16_f32 v58, v58, v59
	v_mul_f32_e32 v59, 0xbfb8aa3b, v64
	v_exp_f32_e32 v59, v59
	s_nop 0
	v_add_f32_e32 v59, 1.0, v59
	v_rcp_f32_e32 v62, v59
	v_mul_f32_e32 v59, 0xbfb8aa3b, v65
	v_exp_f32_e32 v59, v59
	s_nop 0
	v_add_f32_e32 v59, 1.0, v59
	v_rcp_f32_e32 v63, v59
	s_nop 0
	v_pk_mul_f32 v[62:63], v[64:65], v[62:63]
	s_nop 0
	v_pk_mul_f32 v[60:61], v[60:61], v[62:63]
	s_nop 0
	v_cvt_pk_bf16_f32 v59, v60, v61
	v_mul_f32_e32 v60, 0xbfb8aa3b, v54
	v_mul_f32_e32 v61, 0xbfb8aa3b, v55
	v_exp_f32_e32 v60, v60
	v_exp_f32_e32 v61, v61
	v_add_f32_e32 v60, 1.0, v60
	v_add_f32_e32 v61, 1.0, v61
	v_rcp_f32_e32 v60, v60
	v_rcp_f32_e32 v61, v61
	s_nop 0
	v_pk_mul_f32 v[54:55], v[54:55], v[60:61]
	s_nop 0
	v_pk_mul_f32 v[50:51], v[50:51], v[54:55]
	s_nop 0
	v_cvt_pk_bf16_f32 v60, v50, v51
	v_mul_f32_e32 v50, 0xbfb8aa3b, v56
	v_mul_f32_e32 v51, 0xbfb8aa3b, v57
	v_exp_f32_e32 v50, v50
	v_exp_f32_e32 v51, v51
	v_permlane16_swap_b32_e32 v58, v60
	v_add_f32_e32 v50, 1.0, v50
	v_add_f32_e32 v51, 1.0, v51
	v_rcp_f32_e32 v50, v50
	v_rcp_f32_e32 v51, v51
	s_nop 0
	v_pk_mul_f32 v[50:51], v[56:57], v[50:51]
	s_nop 0
	v_pk_mul_f32 v[50:51], v[52:53], v[50:51]
	v_mul_f32_e32 v52, 0xbfb8aa3b, v46
	v_mul_f32_e32 v53, 0xbfb8aa3b, v47
	v_exp_f32_e32 v52, v52
	v_exp_f32_e32 v53, v53
	v_cvt_pk_bf16_f32 v61, v50, v51
	s_nop 1
	v_permlane16_swap_b32_e32 v59, v61
	v_add_f32_e32 v52, 1.0, v52
	v_add_f32_e32 v53, 1.0, v53
	v_rcp_f32_e32 v52, v52
	v_rcp_f32_e32 v53, v53
	v_lshl_add_u64 v[50:51], v[66:67], 0, v[114:115]
	global_store_dwordx4 v[50:51], v[58:61], off
	v_pk_mul_f32 v[46:47], v[46:47], v[52:53]
	s_nop 0
	v_pk_mul_f32 v[42:43], v[42:43], v[46:47]
	s_nop 0
	v_cvt_pk_bf16_f32 v42, v42, v43
	v_mul_f32_e32 v43, 0xbfb8aa3b, v48
	v_exp_f32_e32 v43, v43
	s_nop 0
	v_add_f32_e32 v43, 1.0, v43
	v_rcp_f32_e32 v46, v43
	v_mul_f32_e32 v43, 0xbfb8aa3b, v49
	v_exp_f32_e32 v43, v43
	s_nop 0
	v_add_f32_e32 v43, 1.0, v43
	v_rcp_f32_e32 v47, v43
	s_nop 0
	v_pk_mul_f32 v[46:47], v[48:49], v[46:47]
	s_nop 0
	v_pk_mul_f32 v[44:45], v[44:45], v[46:47]
	s_nop 0
	v_cvt_pk_bf16_f32 v43, v44, v45
	v_mul_f32_e32 v44, 0xbfb8aa3b, v38
	v_mul_f32_e32 v45, 0xbfb8aa3b, v39
	v_exp_f32_e32 v44, v44
	v_exp_f32_e32 v45, v45
	v_add_f32_e32 v44, 1.0, v44
	v_add_f32_e32 v45, 1.0, v45
	v_rcp_f32_e32 v44, v44
	v_rcp_f32_e32 v45, v45
	s_nop 0
	v_pk_mul_f32 v[38:39], v[38:39], v[44:45]
	s_nop 0
	v_pk_mul_f32 v[34:35], v[34:35], v[38:39]
	s_nop 0
	v_cvt_pk_bf16_f32 v44, v34, v35
	v_mul_f32_e32 v34, 0xbfb8aa3b, v40
	v_mul_f32_e32 v35, 0xbfb8aa3b, v41
	v_exp_f32_e32 v34, v34
	v_exp_f32_e32 v35, v35
	v_permlane16_swap_b32_e32 v42, v44
	v_add_f32_e32 v34, 1.0, v34
	v_add_f32_e32 v35, 1.0, v35
	v_rcp_f32_e32 v34, v34
	v_rcp_f32_e32 v35, v35
	s_nop 0
	v_pk_mul_f32 v[34:35], v[40:41], v[34:35]
	s_nop 0
	v_pk_mul_f32 v[34:35], v[36:37], v[34:35]
	v_mul_f32_e32 v36, 0xbfb8aa3b, v30
	v_mul_f32_e32 v37, 0xbfb8aa3b, v31
	v_exp_f32_e32 v36, v36
	v_exp_f32_e32 v37, v37
	v_cvt_pk_bf16_f32 v45, v34, v35
	v_or_b32_e32 v34, v70, v152
	v_add_f32_e32 v36, 1.0, v36
	v_add_f32_e32 v37, 1.0, v37
	v_rcp_f32_e32 v36, v36
	v_rcp_f32_e32 v37, v37
	v_ashrrev_i32_e32 v35, 31, v34
	v_lshlrev_b64 v[34:35], 10, v[34:35]
	v_lshl_add_u64 v[34:35], v[134:135], 0, v[34:35]
	v_pk_mul_f32 v[30:31], v[30:31], v[36:37]
	v_permlane16_swap_b32_e32 v43, v45
	v_pk_mul_f32 v[26:27], v[26:27], v[30:31]
	global_store_dwordx4 v[50:51], v[42:45], off offset:128
	v_cvt_pk_bf16_f32 v26, v26, v27
	v_mul_f32_e32 v27, 0xbfb8aa3b, v32
	v_exp_f32_e32 v27, v27
	s_nop 0
	v_add_f32_e32 v27, 1.0, v27
	v_rcp_f32_e32 v30, v27
	v_mul_f32_e32 v27, 0xbfb8aa3b, v33
	v_exp_f32_e32 v27, v27
	s_nop 0
	v_add_f32_e32 v27, 1.0, v27
	v_rcp_f32_e32 v31, v27
	s_nop 0
	v_pk_mul_f32 v[30:31], v[32:33], v[30:31]
	s_nop 0
	v_pk_mul_f32 v[28:29], v[28:29], v[30:31]
	s_nop 0
	v_cvt_pk_bf16_f32 v27, v28, v29
	v_mul_f32_e32 v28, 0xbfb8aa3b, v22
	v_mul_f32_e32 v29, 0xbfb8aa3b, v23
	v_exp_f32_e32 v28, v28
	v_exp_f32_e32 v29, v29
	v_add_f32_e32 v28, 1.0, v28
	v_add_f32_e32 v29, 1.0, v29
	v_rcp_f32_e32 v28, v28
	v_rcp_f32_e32 v29, v29
	s_nop 0
	v_pk_mul_f32 v[22:23], v[22:23], v[28:29]
	s_nop 0
	v_pk_mul_f32 v[18:19], v[18:19], v[22:23]
	s_nop 0
	v_cvt_pk_bf16_f32 v28, v18, v19
	v_mul_f32_e32 v18, 0xbfb8aa3b, v24
	v_mul_f32_e32 v19, 0xbfb8aa3b, v25
	v_exp_f32_e32 v18, v18
	v_exp_f32_e32 v19, v19
	v_permlane16_swap_b32_e32 v26, v28
	v_add_f32_e32 v18, 1.0, v18
	v_add_f32_e32 v19, 1.0, v19
	v_rcp_f32_e32 v18, v18
	v_rcp_f32_e32 v19, v19
	s_nop 0
	v_pk_mul_f32 v[18:19], v[24:25], v[18:19]
	s_nop 0
	v_pk_mul_f32 v[18:19], v[20:21], v[18:19]
	v_mul_f32_e32 v20, 0xbfb8aa3b, v14
	v_mul_f32_e32 v21, 0xbfb8aa3b, v15
	v_exp_f32_e32 v20, v20
	v_exp_f32_e32 v21, v21
	v_cvt_pk_bf16_f32 v29, v18, v19
	s_nop 1
	v_permlane16_swap_b32_e32 v27, v29
	v_add_f32_e32 v20, 1.0, v20
	v_add_f32_e32 v21, 1.0, v21
	v_rcp_f32_e32 v20, v20
	v_rcp_f32_e32 v21, v21
	v_lshl_add_u64 v[18:19], v[34:35], 0, v[114:115]
	global_store_dwordx4 v[18:19], v[26:29], off
	v_pk_mul_f32 v[14:15], v[14:15], v[20:21]
	s_nop 0
	v_pk_mul_f32 v[10:11], v[10:11], v[14:15]
	s_nop 0
	v_cvt_pk_bf16_f32 v10, v10, v11
	v_mul_f32_e32 v11, 0xbfb8aa3b, v16
	v_exp_f32_e32 v11, v11
	s_nop 0
	v_add_f32_e32 v11, 1.0, v11
	v_rcp_f32_e32 v14, v11
	v_mul_f32_e32 v11, 0xbfb8aa3b, v17
	v_exp_f32_e32 v11, v11
	s_nop 0
	v_add_f32_e32 v11, 1.0, v11
	v_rcp_f32_e32 v15, v11
	s_nop 0
	v_pk_mul_f32 v[14:15], v[16:17], v[14:15]
	s_nop 0
	v_pk_mul_f32 v[12:13], v[12:13], v[14:15]
	s_nop 0
	v_cvt_pk_bf16_f32 v11, v12, v13
	v_mul_f32_e32 v12, 0xbfb8aa3b, v6
	v_mul_f32_e32 v13, 0xbfb8aa3b, v7
	v_exp_f32_e32 v12, v12
	v_exp_f32_e32 v13, v13
	v_add_f32_e32 v12, 1.0, v12
	v_add_f32_e32 v13, 1.0, v13
	v_rcp_f32_e32 v12, v12
	v_rcp_f32_e32 v13, v13
	s_nop 0
	v_pk_mul_f32 v[6:7], v[6:7], v[12:13]
	s_nop 0
	v_pk_mul_f32 v[2:3], v[2:3], v[6:7]
	s_nop 0
	v_cvt_pk_bf16_f32 v12, v2, v3
	v_mul_f32_e32 v2, 0xbfb8aa3b, v8
	v_mul_f32_e32 v3, 0xbfb8aa3b, v9
	v_exp_f32_e32 v2, v2
	v_exp_f32_e32 v3, v3
	v_permlane16_swap_b32_e32 v10, v12
	v_add_f32_e32 v2, 1.0, v2
	v_add_f32_e32 v3, 1.0, v3
	v_rcp_f32_e32 v2, v2
	v_rcp_f32_e32 v3, v3
	s_nop 0
	v_pk_mul_f32 v[2:3], v[8:9], v[2:3]
	s_nop 0
	v_pk_mul_f32 v[2:3], v[4:5], v[2:3]
	s_nop 0
	v_cvt_pk_bf16_f32 v13, v2, v3
	s_nop 1
	v_permlane16_swap_b32_e32 v11, v13
	global_store_dwordx4 v[18:19], v[10:13], off offset:128
	s_cbranch_vccz .LBB0_2465
	s_waitcnt vmcnt(0)
	s_cmpk_gt_u32 s29, 0xff
	s_cbranch_scc1 .LBB0_2479
	s_barrier

.LBB0_2562:
	s_ashr_i32 s11, s10, 31
	s_xor_b64 s[18:19], s[26:27], -1
	s_lshl_b64 s[0:1], s[10:11], 18
	s_add_u32 s16, s31, s0
	s_addc_u32 s17, s34, s1
	s_and_b64 s[0:1], s[26:27], exec
	s_cselect_b32 s11, s17, s23
	s_cselect_b32 s74, s16, s22
	s_ashr_i32 s13, s12, 31
	s_lshl_b64 s[0:1], s[12:13], 20
	s_add_u32 s13, s35, s0
	s_addc_u32 s21, s38, s1
	s_ashr_i32 s15, s14, 31
	s_lshl_b64 s[0:1], s[14:15], 18
	s_add_u32 s20, s13, s0
	s_addc_u32 s21, s21, s1
	s_and_b64 s[0:1], s[26:27], exec
	s_cselect_b32 s13, s21, s25
	s_cselect_b32 s15, s20, s24
	s_add_u32 s22, s22, 0x20080
	s_addc_u32 s23, s23, 0
	s_add_u32 s75, s24, 0x100
	v_mov_b32_e32 v2, 0
	s_addc_u32 s76, s25, 0
	s_mov_b32 s77, -2
	v_mov_b32_e32 v3, v2
	v_mov_b32_e32 v4, v2
	v_mov_b32_e32 v5, v2
	v_mov_b32_e32 v6, v2
	v_mov_b32_e32 v7, v2
	v_mov_b32_e32 v8, v2
	v_mov_b32_e32 v9, v2
	v_mov_b32_e32 v10, v2
	v_mov_b32_e32 v11, v2
	v_mov_b32_e32 v12, v2
	v_mov_b32_e32 v13, v2
	v_mov_b32_e32 v14, v2
	v_mov_b32_e32 v15, v2
	v_mov_b32_e32 v16, v2
	v_mov_b32_e32 v17, v2
	v_mov_b32_e32 v26, v2
	v_mov_b32_e32 v27, v2
	v_mov_b32_e32 v28, v2
	v_mov_b32_e32 v29, v2
	v_mov_b32_e32 v30, v2
	v_mov_b32_e32 v31, v2
	v_mov_b32_e32 v32, v2
	v_mov_b32_e32 v33, v2
	v_mov_b32_e32 v42, v2
	v_mov_b32_e32 v43, v2
	v_mov_b32_e32 v44, v2
	v_mov_b32_e32 v45, v2
	v_mov_b32_e32 v46, v2
	v_mov_b32_e32 v47, v2
	v_mov_b32_e32 v48, v2
	v_mov_b32_e32 v49, v2
	v_mov_b32_e32 v18, v2
	v_mov_b32_e32 v19, v2
	v_mov_b32_e32 v20, v2
	v_mov_b32_e32 v21, v2
	v_mov_b32_e32 v22, v2
	v_mov_b32_e32 v23, v2
	v_mov_b32_e32 v24, v2
	v_mov_b32_e32 v25, v2
	v_mov_b32_e32 v34, v2
	v_mov_b32_e32 v35, v2
	v_mov_b32_e32 v36, v2
	v_mov_b32_e32 v37, v2
	v_mov_b32_e32 v38, v2
	v_mov_b32_e32 v39, v2
	v_mov_b32_e32 v40, v2
	v_mov_b32_e32 v41, v2
	v_mov_b32_e32 v50, v2
	v_mov_b32_e32 v51, v2
	v_mov_b32_e32 v52, v2
	v_mov_b32_e32 v53, v2
	v_mov_b32_e32 v54, v2
	v_mov_b32_e32 v55, v2
	v_mov_b32_e32 v56, v2
	v_mov_b32_e32 v57, v2
	v_mov_b32_e32 v58, v2
	v_mov_b32_e32 v59, v2
	v_mov_b32_e32 v60, v2
	v_mov_b32_e32 v61, v2
	v_mov_b32_e32 v62, v2
	v_mov_b32_e32 v63, v2
	v_mov_b32_e32 v64, v2
	v_mov_b32_e32 v65, v2
	v_mov_b32_e32 v66, v2
	v_mov_b32_e32 v67, v2
	v_mov_b32_e32 v68, v2
	v_mov_b32_e32 v69, v2
	v_mov_b32_e32 v70, v2
	v_mov_b32_e32 v71, v2
	v_mov_b32_e32 v72, v2
	v_mov_b32_e32 v73, v2
	v_mov_b32_e32 v74, v2
	v_mov_b32_e32 v75, v2
	v_mov_b32_e32 v76, v2
	v_mov_b32_e32 v77, v2
	v_mov_b32_e32 v78, v2
	v_mov_b32_e32 v79, v2
	v_mov_b32_e32 v80, v2
	v_mov_b32_e32 v81, v2
	v_mov_b32_e32 v90, v2
	v_mov_b32_e32 v91, v2
	v_mov_b32_e32 v92, v2
	v_mov_b32_e32 v93, v2
	v_mov_b32_e32 v94, v2
	v_mov_b32_e32 v95, v2
	v_mov_b32_e32 v96, v2
	v_mov_b32_e32 v97, v2
	v_mov_b32_e32 v106, v2
	v_mov_b32_e32 v107, v2
	v_mov_b32_e32 v108, v2
	v_mov_b32_e32 v109, v2
	v_mov_b32_e32 v110, v2
	v_mov_b32_e32 v111, v2
	v_mov_b32_e32 v112, v2
	v_mov_b32_e32 v113, v2
	v_mov_b32_e32 v82, v2
	v_mov_b32_e32 v83, v2
	v_mov_b32_e32 v84, v2
	v_mov_b32_e32 v85, v2
	v_mov_b32_e32 v86, v2
	v_mov_b32_e32 v87, v2
	v_mov_b32_e32 v88, v2
	v_mov_b32_e32 v89, v2
	v_mov_b32_e32 v98, v2
	v_mov_b32_e32 v99, v2
	v_mov_b32_e32 v100, v2
	v_mov_b32_e32 v101, v2
	v_mov_b32_e32 v102, v2
	v_mov_b32_e32 v103, v2
	v_mov_b32_e32 v104, v2
	v_mov_b32_e32 v105, v2
	v_mov_b32_e32 v114, v2
	v_mov_b32_e32 v115, v2
	v_mov_b32_e32 v116, v2
	v_mov_b32_e32 v117, v2
	v_mov_b32_e32 v118, v2
	v_mov_b32_e32 v119, v2
	v_mov_b32_e32 v120, v2
	v_mov_b32_e32 v121, v2
	v_mov_b32_e32 v122, v2
	v_mov_b32_e32 v123, v2
	v_mov_b32_e32 v124, v2
	v_mov_b32_e32 v125, v2
	v_mov_b32_e32 v126, v2
	v_mov_b32_e32 v127, v2
	v_mov_b32_e32 v128, v2
	v_mov_b32_e32 v129, v2
	v_add_u32_e32 v156, 0x10000, v140
	ds_read_b128 v[144:147], v156
	ds_read_b128 v[148:151], v156 offset:1024
	ds_read_b128 v[152:155], v156 offset:2048
	ds_read_b128 v[156:159], v156 offset:3072
.LBB0_2563:
	s_add_u32 s0, s22, 0xfffe0080
	s_addc_u32 s1, s23, -1
	s_add_i32 s33, 0, 0x10000
	s_cmp_eq_u32 s77, 4
	s_cselect_b32 s27, s11, s1
	s_cselect_b32 s26, s74, s0
	s_cselect_b32 s25, s13, s76
	s_cselect_b32 s24, s15, s75
	v_lshl_add_u64 v[192:193], s[22:23], 0, v[136:137]
	s_add_i32 m0, s9, 0xc000
	ds_read_b128 v[160:163], v142
	ds_read_b128 v[164:167], v142 offset:1024
	ds_read_b128 v[168:171], v142 offset:2048
	ds_read_b128 v[172:175], v142 offset:3072
	ds_read_b128 v[176:179], v142 offset:4096
	ds_read_b128 v[180:183], v142 offset:5120
	ds_read_b128 v[184:187], v142 offset:6144
	ds_read_b128 v[188:191], v142 offset:7168
	global_load_lds_dwordx4 v[192:193], off
	v_lshl_add_u64 v[192:193], s[22:23], 0, v[138:139]
	s_add_i32 m0, s9, 0xe000
	s_nop 0
	global_load_lds_dwordx4 v[192:193], off
	s_waitcnt lgkmcnt(8)
	s_barrier
	s_waitcnt lgkmcnt(0)
	s_waitcnt lgkmcnt(0)
	v_mfma_f32_16x16x32_bf16 v[126:129], v[144:147], v[160:163], v[126:129]
	v_mfma_f32_16x16x32_bf16 v[122:125], v[152:155], v[160:163], v[122:125]
	v_mfma_f32_16x16x32_bf16 v[118:121], v[144:147], v[168:171], v[118:121]
	v_mfma_f32_16x16x32_bf16 v[114:117], v[152:155], v[168:171], v[114:117]
	v_mfma_f32_16x16x32_bf16 v[102:105], v[144:147], v[176:179], v[102:105]
	v_mfma_f32_16x16x32_bf16 v[98:101], v[152:155], v[176:179], v[98:101]
	v_mfma_f32_16x16x32_bf16 v[86:89], v[144:147], v[184:187], v[86:89]
	v_mfma_f32_16x16x32_bf16 v[82:85], v[152:155], v[184:187], v[82:85]
	v_mfma_f32_16x16x32_bf16 v[126:129], v[148:151], v[164:167], v[126:129]
	v_mfma_f32_16x16x32_bf16 v[122:125], v[156:159], v[164:167], v[122:125]
	v_mfma_f32_16x16x32_bf16 v[118:121], v[148:151], v[172:175], v[118:121]
	v_mfma_f32_16x16x32_bf16 v[114:117], v[156:159], v[172:175], v[114:117]
	v_mfma_f32_16x16x32_bf16 v[102:105], v[148:151], v[180:183], v[102:105]
	v_mfma_f32_16x16x32_bf16 v[98:101], v[156:159], v[180:183], v[98:101]
	v_mfma_f32_16x16x32_bf16 v[86:89], v[148:151], v[188:191], v[86:89]
	v_mfma_f32_16x16x32_bf16 v[82:85], v[156:159], v[188:191], v[82:85]
	s_barrier
	s_add_i32 s36, 0, 0x14000
	s_add_i32 s0, s33, s40
	v_add_u32_e32 v143, s36, v140
	v_lshl_add_u64 v[192:193], s[24:25], 0, v[194:195]
	s_mov_b32 m0, s0
	ds_read_b128 v[198:201], v143
	ds_read_b128 v[202:205], v143 offset:1024
	ds_read_b128 v[206:209], v143 offset:2048
	ds_read_b128 v[210:213], v143 offset:3072
	global_load_lds_dwordx4 v[192:193], off
	v_lshl_add_u64 v[214:215], s[24:25], 0, v[134:135]
	s_add_i32 m0, s0, 0x2000
	s_nop 0
	global_load_lds_dwordx4 v[214:215], off
	s_barrier
	s_waitcnt lgkmcnt(0)
	s_waitcnt lgkmcnt(0)
	v_mfma_f32_16x16x32_bf16 v[110:113], v[198:201], v[160:163], v[110:113]
	v_mfma_f32_16x16x32_bf16 v[106:109], v[206:209], v[160:163], v[106:109]
	v_mfma_f32_16x16x32_bf16 v[94:97], v[198:201], v[168:171], v[94:97]
	v_mfma_f32_16x16x32_bf16 v[90:93], v[206:209], v[168:171], v[90:93]
	v_mfma_f32_16x16x32_bf16 v[78:81], v[198:201], v[176:179], v[78:81]
	v_mfma_f32_16x16x32_bf16 v[74:77], v[206:209], v[176:179], v[74:77]
	v_mfma_f32_16x16x32_bf16 v[70:73], v[198:201], v[184:187], v[70:73]
	v_mfma_f32_16x16x32_bf16 v[66:69], v[206:209], v[184:187], v[66:69]
	v_mfma_f32_16x16x32_bf16 v[110:113], v[202:205], v[164:167], v[110:113]
	v_mfma_f32_16x16x32_bf16 v[106:109], v[210:213], v[164:167], v[106:109]
	v_mfma_f32_16x16x32_bf16 v[94:97], v[202:205], v[172:175], v[94:97]
	v_mfma_f32_16x16x32_bf16 v[90:93], v[210:213], v[172:175], v[90:93]
	v_mfma_f32_16x16x32_bf16 v[78:81], v[202:205], v[180:183], v[78:81]
	v_mfma_f32_16x16x32_bf16 v[74:77], v[210:213], v[180:183], v[74:77]
	v_mfma_f32_16x16x32_bf16 v[70:73], v[202:205], v[188:191], v[70:73]
	v_mfma_f32_16x16x32_bf16 v[66:69], v[210:213], v[188:191], v[66:69]
	s_mov_b32 m0, s9
	v_lshl_add_u64 v[216:217], s[26:27], 0, v[130:131]
	s_barrier
	ds_read_b128 v[160:163], v142 offset:16384
	ds_read_b128 v[164:167], v142 offset:17408
	ds_read_b128 v[168:171], v142 offset:18432
	ds_read_b128 v[172:175], v142 offset:19456
	ds_read_b128 v[176:179], v142 offset:20480
	ds_read_b128 v[180:183], v142 offset:21504
	ds_read_b128 v[184:187], v142 offset:22528
	ds_read_b128 v[188:191], v142 offset:23552
	global_load_lds_dwordx4 v[216:217], off
	v_lshl_add_u64 v[218:219], s[26:27], 0, v[132:133]
	s_mov_b32 m0, s43
	s_nop 0
	global_load_lds_dwordx4 v[218:219], off
	s_waitcnt vmcnt(10)
	s_barrier
	s_waitcnt lgkmcnt(0)
	s_waitcnt lgkmcnt(0)
	v_mfma_f32_16x16x32_bf16 v[62:65], v[144:147], v[160:163], v[62:65]
	v_mfma_f32_16x16x32_bf16 v[58:61], v[152:155], v[160:163], v[58:61]
	v_mfma_f32_16x16x32_bf16 v[54:57], v[144:147], v[168:171], v[54:57]
	v_mfma_f32_16x16x32_bf16 v[50:53], v[152:155], v[168:171], v[50:53]
	v_mfma_f32_16x16x32_bf16 v[38:41], v[144:147], v[176:179], v[38:41]
	v_mfma_f32_16x16x32_bf16 v[34:37], v[152:155], v[176:179], v[34:37]
	v_mfma_f32_16x16x32_bf16 v[22:25], v[144:147], v[184:187], v[22:25]
	v_mfma_f32_16x16x32_bf16 v[18:21], v[152:155], v[184:187], v[18:21]
	v_mfma_f32_16x16x32_bf16 v[62:65], v[148:151], v[164:167], v[62:65]
	v_mfma_f32_16x16x32_bf16 v[58:61], v[156:159], v[164:167], v[58:61]
	v_mfma_f32_16x16x32_bf16 v[54:57], v[148:151], v[172:175], v[54:57]
	v_mfma_f32_16x16x32_bf16 v[50:53], v[156:159], v[172:175], v[50:53]
	v_mfma_f32_16x16x32_bf16 v[38:41], v[148:151], v[180:183], v[38:41]
	v_mfma_f32_16x16x32_bf16 v[34:37], v[156:159], v[180:183], v[34:37]
	v_mfma_f32_16x16x32_bf16 v[22:25], v[148:151], v[188:191], v[22:25]
	v_mfma_f32_16x16x32_bf16 v[18:21], v[156:159], v[188:191], v[18:21]
	s_barrier
	s_add_u32 s0, s24, 0x20000
	s_addc_u32 s1, s25, 0
	s_add_i32 s33, s36, s40
	v_lshl_add_u64 v[144:145], s[0:1], 0, v[194:195]
	s_mov_b32 m0, s33
	s_nop 0
	global_load_lds_dwordx4 v[144:145], off
	v_lshl_add_u64 v[144:145], s[0:1], 0, v[134:135]
	s_add_i32 m0, s33, 0x2000
	s_nop 0
	global_load_lds_dwordx4 v[144:145], off
	v_add_u32_e32 v156, 0x18000, v140
	ds_read_b128 v[144:147], v156
	ds_read_b128 v[148:151], v156 offset:1024
	ds_read_b128 v[152:155], v156 offset:2048
	ds_read_b128 v[156:159], v156 offset:3072
	s_waitcnt vmcnt(6)
	s_barrier
	v_mfma_f32_16x16x32_bf16 v[46:49], v[198:201], v[160:163], v[46:49]
	v_mfma_f32_16x16x32_bf16 v[42:45], v[206:209], v[160:163], v[42:45]
	v_mfma_f32_16x16x32_bf16 v[30:33], v[198:201], v[168:171], v[30:33]
	v_mfma_f32_16x16x32_bf16 v[26:29], v[206:209], v[168:171], v[26:29]
	v_mfma_f32_16x16x32_bf16 v[14:17], v[198:201], v[176:179], v[14:17]
	v_mfma_f32_16x16x32_bf16 v[10:13], v[206:209], v[176:179], v[10:13]
	v_mfma_f32_16x16x32_bf16 v[6:9], v[198:201], v[184:187], v[6:9]
	v_mfma_f32_16x16x32_bf16 v[2:5], v[206:209], v[184:187], v[2:5]
	v_mfma_f32_16x16x32_bf16 v[46:49], v[202:205], v[164:167], v[46:49]
	v_mfma_f32_16x16x32_bf16 v[42:45], v[210:213], v[164:167], v[42:45]
	v_mfma_f32_16x16x32_bf16 v[30:33], v[202:205], v[172:175], v[30:33]
	v_mfma_f32_16x16x32_bf16 v[26:29], v[210:213], v[172:175], v[26:29]
	v_mfma_f32_16x16x32_bf16 v[14:17], v[202:205], v[180:183], v[14:17]
	v_mfma_f32_16x16x32_bf16 v[10:13], v[210:213], v[180:183], v[10:13]
	v_mfma_f32_16x16x32_bf16 v[6:9], v[202:205], v[188:191], v[6:9]
	v_mfma_f32_16x16x32_bf16 v[2:5], v[210:213], v[188:191], v[2:5]
	s_add_i32 s33, 0, 0x18000
	s_barrier
	s_add_u32 s0, s26, 0x20000
	s_addc_u32 s1, s27, 0
	s_mov_b32 m0, s64
	v_lshl_add_u64 v[198:199], s[0:1], 0, v[130:131]
	ds_read_b128 v[160:163], v142 offset:32768
	ds_read_b128 v[164:167], v142 offset:33792
	ds_read_b128 v[168:171], v142 offset:34816
	ds_read_b128 v[172:175], v142 offset:35840
	ds_read_b128 v[176:179], v142 offset:36864
	ds_read_b128 v[180:183], v142 offset:37888
	ds_read_b128 v[184:187], v142 offset:38912
	ds_read_b128 v[188:191], v142 offset:39936
	global_load_lds_dwordx4 v[198:199], off
	v_lshl_add_u64 v[198:199], s[0:1], 0, v[132:133]
	s_mov_b32 m0, s65
	s_nop 0
	global_load_lds_dwordx4 v[198:199], off
	s_waitcnt lgkmcnt(8)
	s_barrier
	s_waitcnt lgkmcnt(0)
	s_waitcnt lgkmcnt(0)
	v_mfma_f32_16x16x32_bf16 v[126:129], v[144:147], v[160:163], v[126:129]
	v_mfma_f32_16x16x32_bf16 v[122:125], v[152:155], v[160:163], v[122:125]
	v_mfma_f32_16x16x32_bf16 v[118:121], v[144:147], v[168:171], v[118:121]
	v_mfma_f32_16x16x32_bf16 v[114:117], v[152:155], v[168:171], v[114:117]
	v_mfma_f32_16x16x32_bf16 v[102:105], v[144:147], v[176:179], v[102:105]
	v_mfma_f32_16x16x32_bf16 v[98:101], v[152:155], v[176:179], v[98:101]
	v_mfma_f32_16x16x32_bf16 v[86:89], v[144:147], v[184:187], v[86:89]
	v_mfma_f32_16x16x32_bf16 v[82:85], v[152:155], v[184:187], v[82:85]
	v_mfma_f32_16x16x32_bf16 v[126:129], v[148:151], v[164:167], v[126:129]
	v_mfma_f32_16x16x32_bf16 v[122:125], v[156:159], v[164:167], v[122:125]
	v_mfma_f32_16x16x32_bf16 v[118:121], v[148:151], v[172:175], v[118:121]
	v_mfma_f32_16x16x32_bf16 v[114:117], v[156:159], v[172:175], v[114:117]
	v_mfma_f32_16x16x32_bf16 v[102:105], v[148:151], v[180:183], v[102:105]
	v_mfma_f32_16x16x32_bf16 v[98:101], v[156:159], v[180:183], v[98:101]
	v_mfma_f32_16x16x32_bf16 v[86:89], v[148:151], v[188:191], v[86:89]
	v_mfma_f32_16x16x32_bf16 v[82:85], v[156:159], v[188:191], v[82:85]
	s_barrier
	s_add_i32 s26, 0, 0x1c000
	s_add_i32 s0, s33, s40
	v_add_u32_e32 v143, s26, v140
	v_lshl_add_u64 v[192:193], v[192:193], 0, s[54:55]
	s_mov_b32 m0, s0
	ds_read_b128 v[198:201], v143
	ds_read_b128 v[202:205], v143 offset:1024
	ds_read_b128 v[206:209], v143 offset:2048
	ds_read_b128 v[210:213], v143 offset:3072
	global_load_lds_dwordx4 v[192:193], off
	v_lshl_add_u64 v[192:193], v[214:215], 0, s[54:55]
	s_add_i32 m0, s0, 0x2000
	s_nop 0
	global_load_lds_dwordx4 v[192:193], off
	s_barrier
	s_waitcnt lgkmcnt(0)
	s_waitcnt lgkmcnt(0)
	v_mfma_f32_16x16x32_bf16 v[110:113], v[198:201], v[160:163], v[110:113]
	v_mfma_f32_16x16x32_bf16 v[106:109], v[206:209], v[160:163], v[106:109]
	v_mfma_f32_16x16x32_bf16 v[94:97], v[198:201], v[168:171], v[94:97]
	v_mfma_f32_16x16x32_bf16 v[90:93], v[206:209], v[168:171], v[90:93]
	v_mfma_f32_16x16x32_bf16 v[78:81], v[198:201], v[176:179], v[78:81]
	v_mfma_f32_16x16x32_bf16 v[74:77], v[206:209], v[176:179], v[74:77]
	v_mfma_f32_16x16x32_bf16 v[70:73], v[198:201], v[184:187], v[70:73]
	v_mfma_f32_16x16x32_bf16 v[66:69], v[206:209], v[184:187], v[66:69]
	v_mfma_f32_16x16x32_bf16 v[110:113], v[202:205], v[164:167], v[110:113]
	v_mfma_f32_16x16x32_bf16 v[106:109], v[210:213], v[164:167], v[106:109]
	v_mfma_f32_16x16x32_bf16 v[94:97], v[202:205], v[172:175], v[94:97]
	v_mfma_f32_16x16x32_bf16 v[90:93], v[210:213], v[172:175], v[90:93]
	v_mfma_f32_16x16x32_bf16 v[78:81], v[202:205], v[180:183], v[78:81]
	v_mfma_f32_16x16x32_bf16 v[74:77], v[210:213], v[180:183], v[74:77]
	v_mfma_f32_16x16x32_bf16 v[70:73], v[202:205], v[188:191], v[70:73]
	v_mfma_f32_16x16x32_bf16 v[66:69], v[210:213], v[188:191], v[66:69]
	s_mov_b32 m0, s66
	v_lshl_add_u64 v[192:193], v[216:217], 0, s[54:55]
	s_barrier
	ds_read_b128 v[160:163], v142 offset:49152
	ds_read_b128 v[164:167], v142 offset:50176
	ds_read_b128 v[168:171], v142 offset:51200
	ds_read_b128 v[172:175], v142 offset:52224
	ds_read_b128 v[176:179], v142 offset:53248
	ds_read_b128 v[180:183], v142 offset:54272
	ds_read_b128 v[184:187], v142 offset:55296
	ds_read_b128 v[188:191], v142 offset:56320
	global_load_lds_dwordx4 v[192:193], off
	v_lshl_add_u64 v[192:193], v[218:219], 0, s[54:55]
	s_mov_b32 m0, s67
	s_nop 0
	global_load_lds_dwordx4 v[192:193], off
	s_waitcnt vmcnt(10)
	s_barrier
	s_waitcnt lgkmcnt(0)
	s_waitcnt lgkmcnt(0)
	v_mfma_f32_16x16x32_bf16 v[62:65], v[144:147], v[160:163], v[62:65]
	v_mfma_f32_16x16x32_bf16 v[58:61], v[152:155], v[160:163], v[58:61]
	v_mfma_f32_16x16x32_bf16 v[54:57], v[144:147], v[168:171], v[54:57]
	v_mfma_f32_16x16x32_bf16 v[50:53], v[152:155], v[168:171], v[50:53]
	v_mfma_f32_16x16x32_bf16 v[38:41], v[144:147], v[176:179], v[38:41]
	v_mfma_f32_16x16x32_bf16 v[34:37], v[152:155], v[176:179], v[34:37]
	v_mfma_f32_16x16x32_bf16 v[22:25], v[144:147], v[184:187], v[22:25]
	v_mfma_f32_16x16x32_bf16 v[18:21], v[152:155], v[184:187], v[18:21]
	v_mfma_f32_16x16x32_bf16 v[62:65], v[148:151], v[164:167], v[62:65]
	v_mfma_f32_16x16x32_bf16 v[58:61], v[156:159], v[164:167], v[58:61]
	v_mfma_f32_16x16x32_bf16 v[54:57], v[148:151], v[172:175], v[54:57]
	v_mfma_f32_16x16x32_bf16 v[50:53], v[156:159], v[172:175], v[50:53]
	v_mfma_f32_16x16x32_bf16 v[38:41], v[148:151], v[180:183], v[38:41]
	v_mfma_f32_16x16x32_bf16 v[34:37], v[156:159], v[180:183], v[34:37]
	v_mfma_f32_16x16x32_bf16 v[22:25], v[148:151], v[188:191], v[22:25]
	v_mfma_f32_16x16x32_bf16 v[18:21], v[156:159], v[188:191], v[18:21]
	s_barrier
	s_add_u32 s0, s24, 0x20080
	s_addc_u32 s1, s25, 0
	s_add_i32 s24, s26, s40
	v_lshl_add_u64 v[144:145], s[0:1], 0, v[194:195]
	s_mov_b32 m0, s24
	s_nop 0
	global_load_lds_dwordx4 v[144:145], off
	v_lshl_add_u64 v[144:145], s[0:1], 0, v[134:135]
	s_add_i32 m0, s24, 0x2000
	s_nop 0
	global_load_lds_dwordx4 v[144:145], off
	v_add_u32_e32 v156, 0x10000, v140
	ds_read_b128 v[144:147], v156
	ds_read_b128 v[148:151], v156 offset:1024
	ds_read_b128 v[152:155], v156 offset:2048
	ds_read_b128 v[156:159], v156 offset:3072
	s_waitcnt vmcnt(6)
	s_barrier
	v_mfma_f32_16x16x32_bf16 v[46:49], v[198:201], v[160:163], v[46:49]
	v_mfma_f32_16x16x32_bf16 v[42:45], v[206:209], v[160:163], v[42:45]
	v_mfma_f32_16x16x32_bf16 v[30:33], v[198:201], v[168:171], v[30:33]
	v_mfma_f32_16x16x32_bf16 v[26:29], v[206:209], v[168:171], v[26:29]
	v_mfma_f32_16x16x32_bf16 v[14:17], v[198:201], v[176:179], v[14:17]
	v_mfma_f32_16x16x32_bf16 v[10:13], v[206:209], v[176:179], v[10:13]
	v_mfma_f32_16x16x32_bf16 v[6:9], v[198:201], v[184:187], v[6:9]
	v_mfma_f32_16x16x32_bf16 v[2:5], v[206:209], v[184:187], v[2:5]
	v_mfma_f32_16x16x32_bf16 v[46:49], v[202:205], v[164:167], v[46:49]
	v_mfma_f32_16x16x32_bf16 v[42:45], v[210:213], v[164:167], v[42:45]
	v_mfma_f32_16x16x32_bf16 v[30:33], v[202:205], v[172:175], v[30:33]
	v_mfma_f32_16x16x32_bf16 v[26:29], v[210:213], v[172:175], v[26:29]
	v_mfma_f32_16x16x32_bf16 v[14:17], v[202:205], v[180:183], v[14:17]
	v_mfma_f32_16x16x32_bf16 v[10:13], v[210:213], v[180:183], v[10:13]
	v_mfma_f32_16x16x32_bf16 v[6:9], v[202:205], v[188:191], v[6:9]
	v_mfma_f32_16x16x32_bf16 v[2:5], v[210:213], v[188:191], v[2:5]
	s_add_i32 s77, s77, 2
	s_add_u32 s22, s22, 0x100
	s_addc_u32 s23, s23, 0
	s_add_u32 s75, s75, 0x100
	s_addc_u32 s76, s76, 0
	s_cmp_gt_u32 s77, 5
	s_barrier
	s_cbranch_scc0 .LBB0_2563
	s_waitcnt lgkmcnt(0)
	v_lshl_add_u32 v144, s8, 8, v1
	v_lshl_or_b32 v146, s68, 8, v141
	v_ashrrev_i32_e32 v145, 31, v144
	v_lshlrev_b64 v[148:149], 11, v[144:145]
	v_ashrrev_i32_e32 v147, 31, v146
	v_lshl_add_u64 v[148:149], s[6:7], 0, v[148:149]
	v_cvt_pk_bf16_f32 v126, v126, v127
	v_cvt_pk_bf16_f32 v127, v128, v129
	v_cvt_pk_bf16_f32 v128, v122, v123
	v_lshlrev_b64 v[122:123], 1, v[146:147]
	v_cvt_pk_bf16_f32 v129, v124, v125
	v_lshl_add_u64 v[124:125], v[148:149], 0, v[122:123]
	s_mov_b64 s[0:1], 0x40000
	v_cvt_pk_bf16_f32 v62, v62, v63
	v_cvt_pk_bf16_f32 v63, v64, v65
	v_cvt_pk_bf16_f32 v64, v58, v59
	v_lshl_add_u64 v[58:59], v[124:125], 0, s[0:1]
	s_mov_b32 s0, 0x40000
	v_cvt_pk_bf16_f32 v110, v110, v111
	v_cvt_pk_bf16_f32 v111, v112, v113
	v_cvt_pk_bf16_f32 v112, v106, v107
	v_or_b32_e32 v106, 16, v144
	v_cvt_pk_bf16_f32 v65, v60, v61
	v_add_co_u32_e32 v60, vcc, s0, v124
	v_cvt_pk_bf16_f32 v46, v46, v47
	v_cvt_pk_bf16_f32 v47, v48, v49
	v_cvt_pk_bf16_f32 v48, v42, v43
	v_cvt_pk_bf16_f32 v49, v44, v45
	s_mov_b64 s[0:1], 0x48000
	v_ashrrev_i32_e32 v107, 31, v106
	v_addc_co_u32_e32 v61, vcc, 0, v125, vcc
	global_store_dwordx4 v[58:59], v[46:49], off offset:256
	v_cvt_pk_bf16_f32 v113, v108, v109
	v_lshlrev_b64 v[106:107], 11, v[106:107]
	v_lshl_add_u64 v[46:47], v[124:125], 0, s[0:1]
	s_mov_b32 s0, 0x48000
	v_cvt_pk_bf16_f32 v94, v94, v95
	v_cvt_pk_bf16_f32 v95, v96, v97
	v_cvt_pk_bf16_f32 v96, v90, v91
	v_or_b32_e32 v90, 32, v144
	v_add_co_u32_e32 v48, vcc, s0, v124
	v_cvt_pk_bf16_f32 v30, v30, v31
	v_cvt_pk_bf16_f32 v31, v32, v33
	v_cvt_pk_bf16_f32 v32, v26, v27
	v_cvt_pk_bf16_f32 v33, v28, v29
	s_mov_b64 s[0:1], 0x50000
	global_store_dwordx4 v[124:125], v[110:113], off offset:256
	v_ashrrev_i32_e32 v91, 31, v90
	v_addc_co_u32_e32 v49, vcc, 0, v125, vcc
	v_lshl_add_u64 v[110:111], s[6:7], 0, v[106:107]
	global_store_dwordx4 v[46:47], v[30:33], off offset:256
	v_lshl_add_u64 v[110:111], v[110:111], 0, v[122:123]
	v_cvt_pk_bf16_f32 v97, v92, v93
	v_lshl_add_u64 v[30:31], v[124:125], 0, s[0:1]
	s_mov_b32 s0, 0x50000
	v_lshlrev_b64 v[90:91], 11, v[90:91]
	v_cvt_pk_bf16_f32 v78, v78, v79
	v_cvt_pk_bf16_f32 v79, v80, v81
	v_cvt_pk_bf16_f32 v80, v74, v75
	v_or_b32_e32 v74, 48, v144
	v_add_co_u32_e32 v32, vcc, s0, v124
	v_cvt_pk_bf16_f32 v14, v14, v15
	v_cvt_pk_bf16_f32 v15, v16, v17
	v_cvt_pk_bf16_f32 v16, v10, v11
	v_cvt_pk_bf16_f32 v17, v12, v13
	s_mov_b64 s[0:1], 0x58000
	global_store_dwordx4 v[110:111], v[94:97], off offset:256
	v_ashrrev_i32_e32 v75, 31, v74
	v_addc_co_u32_e32 v33, vcc, 0, v125, vcc
	v_lshl_add_u64 v[94:95], s[6:7], 0, v[90:91]
	global_store_dwordx4 v[30:31], v[14:17], off offset:256
	v_lshl_add_u64 v[94:95], v[94:95], 0, v[122:123]
	v_cvt_pk_bf16_f32 v81, v76, v77
	v_lshl_add_u64 v[14:15], v[124:125], 0, s[0:1]
	s_mov_b32 s0, 0x58000
	v_lshlrev_b64 v[74:75], 11, v[74:75]
	v_add_co_u32_e32 v16, vcc, s0, v124
	global_store_dwordx4 v[94:95], v[78:81], off offset:256
	s_nop 0
	v_addc_co_u32_e32 v17, vcc, 0, v125, vcc
	v_lshl_add_u64 v[78:79], s[6:7], 0, v[74:75]
	v_cvt_pk_bf16_f32 v106, v118, v119
	v_cvt_pk_bf16_f32 v107, v120, v121
	v_cvt_pk_bf16_f32 v108, v114, v115
	v_cvt_pk_bf16_f32 v109, v116, v117
	v_cvt_pk_bf16_f32 v90, v102, v103
	v_cvt_pk_bf16_f32 v91, v104, v105
	v_cvt_pk_bf16_f32 v92, v98, v99
	v_cvt_pk_bf16_f32 v93, v100, v101
	v_cvt_pk_bf16_f32 v74, v86, v87
	v_cvt_pk_bf16_f32 v75, v88, v89
	v_cvt_pk_bf16_f32 v76, v82, v83
	v_cvt_pk_bf16_f32 v77, v84, v85
	v_lshl_add_u64 v[78:79], v[78:79], 0, v[122:123]
	v_cvt_pk_bf16_f32 v70, v70, v71
	v_cvt_pk_bf16_f32 v71, v72, v73
	v_cvt_pk_bf16_f32 v72, v66, v67
	v_cvt_pk_bf16_f32 v73, v68, v69
	v_cvt_pk_bf16_f32 v42, v54, v55
	v_cvt_pk_bf16_f32 v43, v56, v57
	v_cvt_pk_bf16_f32 v44, v50, v51
	v_cvt_pk_bf16_f32 v45, v52, v53
	v_cvt_pk_bf16_f32 v26, v38, v39
	v_cvt_pk_bf16_f32 v27, v40, v41
	v_cvt_pk_bf16_f32 v28, v34, v35
	v_cvt_pk_bf16_f32 v29, v36, v37
	v_cvt_pk_bf16_f32 v10, v22, v23
	v_cvt_pk_bf16_f32 v11, v24, v25
	v_cvt_pk_bf16_f32 v12, v18, v19
	v_cvt_pk_bf16_f32 v13, v20, v21
	v_cvt_pk_bf16_f32 v6, v6, v7
	v_cvt_pk_bf16_f32 v7, v8, v9
	v_cvt_pk_bf16_f32 v8, v2, v3
	v_cvt_pk_bf16_f32 v9, v4, v5
	s_and_b64 vcc, exec, s[18:19]
	s_mov_b32 s68, s14
	s_mov_b32 s8, s10
	s_mov_b64 s[24:25], s[20:21]
	s_mov_b64 s[22:23], s[16:17]
	global_store_dwordx4 v[124:125], v[126:129], off
	global_store_dwordx4 v[110:111], v[106:109], off
	global_store_dwordx4 v[94:95], v[90:93], off
	global_store_dwordx4 v[78:79], v[74:77], off
	global_store_dwordx4 v[78:79], v[70:73], off offset:256
	global_store_dwordx4 v[60:61], v[62:65], off
	global_store_dwordx4 v[48:49], v[42:45], off
	global_store_dwordx4 v[32:33], v[26:29], off
	global_store_dwordx4 v[16:17], v[10:13], off
	global_store_dwordx4 v[14:15], v[6:9], off offset:256
	s_cbranch_vccz .LBB0_2555
	s_waitcnt vmcnt(0)
	s_cmpk_gt_u32 s29, 0xff
	s_cbranch_scc1 .LBB0_2567
	s_barrier
